# hand-written down-weight conversion: each wave converts 16 adjacent items (same source rows), 3 in flight, on top of best
# speedup vs baseline: 1.0011x; 1.0011x over previous
;     __device__ __forceinline__ void operator()(const f32x4 (&acc)[2][2][4][2], const Unit& u, int wr, int wc, int fr, int fq) const {
;         asm volatile("" : "+v"(fr), "+v"(fq));
;         const int e = blkE[u.z], c0 = u.pn * 128 + wc * 32 + 8 * fq, row0 = wr * 64 + fr;
;         const float* bg = bup + (size_t)e * 2 * FF + c0; const f32x4 g0 = *(const f32x4*)bg, g1 = *(const f32x4*)(bg + 4), l0 = *(const f32x4*)(bg + FF), l1 = *(const f32x4*)(bg + FF + 4);
;         float rsb[8];
; #pragma unroll
;         for (int q = 0; q < 8; ++q) rsb[q] = ssq[tokTab[u.pm * 256 + row0 + (q >> 2) * 128 + (q & 3) * 16]] * W8_INV;
; #pragma unroll
;         for (int ai = 0; ai < 2; ++ai)
; #pragma unroll
;             for (int m = 0; m < 4; ++m) { const int r = row0 + ai * 128 + m * 16; const float rs = rsb[ai * 4 + m];
;                 float a[8];
; #pragma unroll
;                 for (int j = 0; j < 8; ++j) { const float gb = j < 4 ? g0[j & 3] : g1[j & 3], lb = j < 4 ? l0[j & 3] : l1[j & 3];
;                     const float gl = fminf(acc[ai][0][m][j >> 2][j & 3] * rs + gb, 7.0f), ln = fminf(fmaxf(acc[ai][1][m][j >> 2][j & 3] * rs + lb, -7.0f), 7.0f);
;                     a[j] = gl * __builtin_amdgcn_rcpf(1.0f + __builtin_amdgcn_exp2f(-1.702f * 1.4426950408889634f * gl)) * (ln + 1.0f); }
;                 v2u w; w.x = pk4_fp8(a[0], a[1], a[2], a[3]); w.y = pk4_fp8(a[4], a[5], a[6], a[7]);
;                 *(v2u*)(ACT + ((size_t)u.z * 256 + r) * FF + c0) = w; }
;     }
.LBB0_1534:
	s_lshl_b32 s4, s40, 7
	v_mov_b32_e32 v2, v218
	v_mov_b32_e32 v3, v219
	s_or_b32 s4, s4, s89
	v_mov_b32_e32 v0, s35
	v_lshl_add_u32 v16, v3, 3, s4
	v_readlane_b32 s0, v254, 2
	v_readlane_b32 s4, v254, 6
	s_lshl_b32 s4, s65, 10
	v_add_u32_e32 v18, s88, v2
	s_add_i32 s4, s4, 0
	v_lshl_add_u32 v2, v18, 2, s4
	v_add_u32_e32 v9, 0x20400, v2
	ds_read2_b32 v[4:5], v9 offset1:16
	ds_read_b32 v0, v0
	v_readlane_b32 s1, v254, 3
	v_ashrrev_i32_e32 v17, 31, v16
	ds_read2_b32 v[20:21], v9 offset0:160 offset1:176
	s_waitcnt lgkmcnt(0)
	v_ashrrev_i32_e32 v11, 31, v4
	v_mov_b32_e32 v10, v4
	v_lshl_add_u64 v[10:11], v[10:11], 2, s[14:15]
	global_load_dword v19, v[10:11], off
	ds_read2_b32 v[10:11], v9 offset0:32 offset1:48
	v_ashrrev_i32_e32 v13, 31, v5
	v_mov_b32_e32 v12, v5
	v_lshl_add_u64 v[4:5], v[12:13], 2, s[14:15]
	global_load_dword v24, v[4:5], off
	s_waitcnt lgkmcnt(0)
	v_ashrrev_i32_e32 v5, 31, v10
	v_mov_b32_e32 v4, v10
	v_lshl_add_u64 v[4:5], v[4:5], 2, s[14:15]
	global_load_dword v25, v[4:5], off
	ds_read2_b32 v[4:5], v9 offset0:128 offset1:144
	v_ashrrev_i32_e32 v13, 31, v11
	v_mov_b32_e32 v12, v11
	v_lshl_add_u64 v[10:11], v[12:13], 2, s[14:15]
	v_ashrrev_i32_e32 v1, 31, v0
	global_load_dword v26, v[10:11], off
	s_waitcnt lgkmcnt(0)
	v_ashrrev_i32_e32 v11, 31, v4
	v_mov_b32_e32 v10, v4
	v_lshlrev_b64 v[0:1], 14, v[0:1]
	v_lshl_add_u64 v[10:11], v[10:11], 2, s[14:15]
	v_lshl_add_u64 v[0:1], s[0:1], 0, v[0:1]
	global_load_dword v27, v[10:11], off
	v_ashrrev_i32_e32 v11, 31, v5
	v_mov_b32_e32 v10, v5
	v_lshl_add_u64 v[6:7], v[16:17], 2, v[0:1]
	v_lshl_add_u64 v[4:5], v[10:11], 2, s[14:15]
	global_load_dwordx4 v[0:3], v[6:7], off
	global_load_dword v28, v[4:5], off
	v_ashrrev_i32_e32 v5, 31, v20
	v_mov_b32_e32 v4, v20
	v_add_co_u32_e32 v8, vcc, s56, v6
	v_lshl_add_u64 v[4:5], v[4:5], 2, s[14:15]
	global_load_dword v29, v[4:5], off
	v_addc_co_u32_e32 v9, vcc, 0, v7, vcc
	global_load_dwordx4 v[8:11], v[8:9], off
	s_nop 0
	global_load_dwordx4 v[12:15], v[6:7], off offset:16
	v_readlane_b32 s5, v254, 7
	s_mov_b64 s[4:5], 0x2000
	v_ashrrev_i32_e32 v23, 31, v21
	v_lshl_add_u64 v[4:5], v[6:7], 0, s[4:5]
	global_load_dwordx4 v[4:7], v[4:5], off offset:16
	v_mov_b32_e32 v22, v21
	v_lshl_add_u64 v[20:21], v[22:23], 2, s[14:15]
	global_load_dword v20, v[20:21], off
	s_ashr_i32 s39, s38, 31
	s_lshl_b64 s[4:5], s[38:39], 19
	s_add_u32 s4, s93, s4
	s_addc_u32 s5, s87, s5
	v_readlane_b32 s0, v254, 10
	s_cmp_lg_u32 s65, s0
	v_readlane_b32 s2, v254, 4
	v_readlane_b32 s3, v254, 5
	v_readlane_b32 s6, v254, 8
	v_readlane_b32 s7, v254, 9
	s_waitcnt vmcnt(0)
	v_mul_f32_e32 v19, 0x3b800000, v19
	v_mul_f32_e32 v30, 0x3b800000, v24
	v_mul_f32_e32 v25, 0x3b800000, v25
	v_mul_f32_e32 v24, 0x3b800000, v26
	v_mul_f32_e32 v23, 0x3b800000, v27
	v_fma_f32 v26, v192, v19, v0
	v_mul_f32_e32 v22, 0x3b800000, v28
	v_fma_f32 v28, v193, v19, v1
	v_min_f32_e32 v26, 0x40e00000, v26
	v_min_f32_e32 v28, 0x40e00000, v28
	v_fma_f32 v31, v194, v19, v2
	v_mul_f32_e32 v34, 0xc01d265f, v26
	v_mul_f32_e32 v35, 0xc01d265f, v28
	v_min_f32_e32 v31, 0x40e00000, v31
	v_exp_f32_e32 v34, v34
	v_exp_f32_e32 v35, v35
	v_mul_f32_e32 v36, 0xc01d265f, v31
	v_fma_f32 v33, v195, v19, v3
	v_exp_f32_e32 v36, v36
	v_min_f32_e32 v33, 0x40e00000, v33
	v_mul_f32_e32 v37, 0xc01d265f, v33
	v_add_f32_e32 v34, 1.0, v34
	v_add_f32_e32 v35, 1.0, v35
	v_exp_f32_e32 v37, v37
	v_rcp_f32_e32 v34, v34
	v_rcp_f32_e32 v35, v35
	v_add_f32_e32 v36, 1.0, v36
	v_mul_f32_e32 v21, 0x3b800000, v29
	v_fma_f32 v27, v188, v19, v8
	v_fma_f32 v29, v189, v19, v9
	v_rcp_f32_e32 v36, v36
	v_med3_f32 v27, v27, s23, v236
	v_med3_f32 v29, v29, s23, v236
	v_fma_f32 v32, v190, v19, v10
	v_add_f32_e32 v27, 1.0, v27
	v_add_f32_e32 v29, 1.0, v29
	v_add_f32_e32 v37, 1.0, v37
	v_mul_f32_e32 v26, v26, v34
	v_mul_f32_e32 v28, v28, v35
	v_med3_f32 v32, v32, s23, v236
	v_mul_f32_e32 v26, v27, v26
	v_mul_f32_e32 v27, v29, v28
	v_rcp_f32_e32 v28, v37
	v_add_f32_e32 v32, 1.0, v32
	v_mul_f32_e32 v31, v31, v36
	v_mul_f32_e32 v29, v32, v31
	v_fma_f32 v32, v184, v19, v12
	v_min_f32_e32 v32, 0x40e00000, v32
	v_mul_f32_e32 v28, v33, v28
	v_mul_f32_e32 v33, 0xc01d265f, v32
	v_exp_f32_e32 v33, v33
	v_fma_f32 v34, v185, v19, v13
	v_min_f32_e32 v34, 0x40e00000, v34
	v_mul_f32_e32 v35, 0xc01d265f, v34
	v_add_f32_e32 v33, 1.0, v33
	v_rcp_f32_e32 v33, v33
	v_exp_f32_e32 v35, v35
	v_fma_f32 v31, v191, v19, v11
	v_fma_f32 v36, v187, v19, v15
	v_mul_f32_e32 v32, v32, v33
	v_add_f32_e32 v33, 1.0, v35
	v_rcp_f32_e32 v33, v33
	v_med3_f32 v31, v31, s23, v236
	v_min_f32_e32 v36, 0x40e00000, v36
	v_add_f32_e32 v31, 1.0, v31
	v_mul_f32_e32 v33, v34, v33
	v_fma_f32 v34, v186, v19, v14
	v_min_f32_e32 v34, 0x40e00000, v34
	v_mul_f32_e32 v35, 0xc01d265f, v34
	v_exp_f32_e32 v35, v35
	v_mul_f32_e32 v37, 0xc01d265f, v36
	v_mul_f32_e32 v28, v31, v28
	v_fma_f32 v31, v180, v19, v4
	v_add_f32_e32 v35, 1.0, v35
	v_rcp_f32_e32 v35, v35
	v_exp_f32_e32 v37, v37
	v_med3_f32 v31, v31, s23, v236
	v_add_f32_e32 v31, 1.0, v31
	v_mul_f32_e32 v31, v31, v32
	v_fma_f32 v32, v181, v19, v5
	v_med3_f32 v32, v32, s23, v236
	v_mul_f32_e32 v34, v34, v35
	v_add_f32_e32 v35, 1.0, v37
	v_add_f32_e32 v32, 1.0, v32
	v_rcp_f32_e32 v35, v35
	v_mul_f32_e32 v32, v32, v33
	v_fma_f32 v33, v182, v19, v6
	v_med3_f32 v33, v33, s23, v236
	v_fma_f32 v19, v183, v19, v7
	v_add_f32_e32 v33, 1.0, v33
	v_med3_f32 v19, v19, s23, v236
	v_mul_f32_e32 v33, v33, v34
	v_mul_f32_e32 v34, v36, v35
	v_add_f32_e32 v19, 1.0, v19
	v_mul_f32_e32 v19, v19, v34
	v_med3_f32 v34, v26, s24, v237
	v_med3_f32 v27, v27, s24, v237
	v_mov_b32_e32 v26, v65
	v_cvt_pk_fp8_f32 v26, v34, v27
	v_med3_f32 v31, v31, s24, v237
	v_med3_f32 v32, v32, s24, v237
;     __device__ __forceinline__ void operator()(const f32x4 (&acc)[2][2][4][2], const Unit& u, int wr, int wc, int fr, int fq) const {
;     ...
; #pragma unroll
;         for (int ai = 0; ai < 2; ++ai)
; #pragma unroll
;             for (int m = 0; m < 4; ++m) { const int r = row0 + ai * 128 + m * 16; const float rs = rsb[ai * 4 + m];
;                 float a[8];
; #pragma unroll
;                 for (int j = 0; j < 8; ++j) { const float gb = j < 4 ? g0[j & 3] : g1[j & 3], lb = j < 4 ? l0[j & 3] : l1[j & 3];
;                     const float gl = fminf(acc[ai][0][m][j >> 2][j & 3] * rs + gb, 7.0f), ln = fminf(fmaxf(acc[ai][1][m][j >> 2][j & 3] * rs + lb, -7.0f), 7.0f);
;                     a[j] = gl * __builtin_amdgcn_rcpf(1.0f + __builtin_amdgcn_exp2f(-1.702f * 1.4426950408889634f * gl)) * (ln + 1.0f); }
;                 v2u w; w.x = pk4_fp8(a[0], a[1], a[2], a[3]); w.y = pk4_fp8(a[4], a[5], a[6], a[7]);
;                 *(v2u*)(ACT + ((size_t)u.z * 256 + r) * FF + c0) = w; }
	v_mov_b32_e32 v27, v65
	v_cvt_pk_fp8_f32 v27, v31, v32
	v_med3_f32 v29, v29, s24, v237
	v_med3_f32 v28, v28, s24, v237
	v_cvt_pk_fp8_f32 v26, v29, v28 op_sel:[0,0,1]
	v_med3_f32 v28, v33, s24, v237
	v_med3_f32 v19, v19, s24, v237
	v_cvt_pk_fp8_f32 v27, v28, v19 op_sel:[0,0,1]
	v_ashrrev_i32_e32 v19, 31, v18
	v_lshlrev_b64 v[18:19], 11, v[18:19]
	v_lshl_add_u64 v[18:19], s[4:5], 0, v[18:19]
	v_lshl_add_u64 v[16:17], v[18:19], 0, v[16:17]
	global_store_dwordx2 v[16:17], v[26:27], off
	v_fma_f32 v26, v177, v30, v1
	v_min_f32_e32 v26, 0x40e00000, v26
	v_fma_f32 v28, v176, v30, v0
	v_mul_f32_e32 v27, 0xc01d265f, v26
	v_min_f32_e32 v28, 0x40e00000, v28
	v_exp_f32_e32 v27, v27
	v_mul_f32_e32 v29, 0xc01d265f, v28
	v_exp_f32_e32 v29, v29
	v_fma_f32 v32, v169, v30, v13
	v_add_f32_e32 v27, 1.0, v27
	v_rcp_f32_e32 v27, v27
	v_add_f32_e32 v19, 1.0, v29
	v_rcp_f32_e32 v19, v19
	v_fma_f32 v29, v179, v30, v3
	v_mul_f32_e32 v26, v26, v27
	v_fma_f32 v27, v178, v30, v2
	v_min_f32_e32 v27, 0x40e00000, v27
	v_mul_f32_e32 v19, v28, v19
	v_mul_f32_e32 v28, 0xc01d265f, v27
	v_exp_f32_e32 v28, v28
	v_min_f32_e32 v29, 0x40e00000, v29
	v_mul_f32_e32 v31, 0xc01d265f, v29
	v_exp_f32_e32 v31, v31
	v_add_f32_e32 v28, 1.0, v28
	v_rcp_f32_e32 v28, v28
	v_min_f32_e32 v32, 0x40e00000, v32
	v_mul_f32_e32 v33, 0xc01d265f, v32
	v_exp_f32_e32 v33, v33
	v_mul_f32_e32 v27, v27, v28
	v_add_f32_e32 v28, 1.0, v31
	v_rcp_f32_e32 v28, v28
	v_fma_f32 v18, v172, v30, v8
	v_med3_f32 v18, v18, s23, v236
	v_add_f32_e32 v18, 1.0, v18
	v_mul_f32_e32 v28, v29, v28
	v_fma_f32 v29, v168, v30, v12
	v_min_f32_e32 v29, 0x40e00000, v29
	v_mul_f32_e32 v31, 0xc01d265f, v29
	v_exp_f32_e32 v31, v31
	v_mul_f32_e32 v18, v18, v19
	v_fma_f32 v19, v173, v30, v9
	v_med3_f32 v19, v19, s23, v236
	v_add_f32_e32 v31, 1.0, v31
	v_rcp_f32_e32 v31, v31
	v_add_f32_e32 v19, 1.0, v19
	v_mul_f32_e32 v19, v19, v26
	v_fma_f32 v26, v174, v30, v10
	v_mul_f32_e32 v29, v29, v31
	v_add_f32_e32 v31, 1.0, v33
	v_rcp_f32_e32 v31, v31
	v_med3_f32 v26, v26, s23, v236
	v_add_f32_e32 v26, 1.0, v26
	v_mul_f32_e32 v26, v26, v27
	v_mul_f32_e32 v31, v32, v31
	v_fma_f32 v32, v170, v30, v14
	v_min_f32_e32 v32, 0x40e00000, v32
	v_mul_f32_e32 v33, 0xc01d265f, v32
	v_exp_f32_e32 v33, v33
	v_fma_f32 v27, v175, v30, v11
	v_fma_f32 v34, v171, v30, v15
	v_med3_f32 v27, v27, s23, v236
	v_min_f32_e32 v34, 0x40e00000, v34
	v_add_f32_e32 v27, 1.0, v27
	v_add_f32_e32 v33, 1.0, v33
	v_mul_f32_e32 v35, 0xc01d265f, v34
	v_mul_f32_e32 v27, v27, v28
	v_fma_f32 v28, v164, v30, v4
	v_rcp_f32_e32 v33, v33
	v_exp_f32_e32 v35, v35
	v_med3_f32 v28, v28, s23, v236
	v_add_f32_e32 v28, 1.0, v28
	v_mul_f32_e32 v28, v28, v29
	v_fma_f32 v29, v165, v30, v5
	v_med3_f32 v29, v29, s23, v236
	v_mul_f32_e32 v32, v32, v33
	v_add_f32_e32 v33, 1.0, v35
	v_add_f32_e32 v29, 1.0, v29
	v_rcp_f32_e32 v33, v33
	v_mul_f32_e32 v29, v29, v31
	v_fma_f32 v31, v166, v30, v6
	v_med3_f32 v31, v31, s23, v236
	v_fma_f32 v30, v167, v30, v7
	v_add_f32_e32 v31, 1.0, v31
	v_med3_f32 v30, v30, s23, v236
	v_mul_f32_e32 v31, v31, v32
	v_mul_f32_e32 v32, v34, v33
	v_add_f32_e32 v30, 1.0, v30
	v_mul_f32_e32 v30, v30, v32
	v_med3_f32 v32, v18, s24, v237
	v_med3_f32 v19, v19, s24, v237
	v_mov_b32_e32 v18, v65
	v_cvt_pk_fp8_f32 v18, v32, v19
	v_med3_f32 v28, v28, s24, v237
	v_med3_f32 v29, v29, s24, v237
	v_mov_b32_e32 v19, v65
	v_cvt_pk_fp8_f32 v19, v28, v29
	v_med3_f32 v26, v26, s24, v237
	v_med3_f32 v27, v27, s24, v237
	v_cvt_pk_fp8_f32 v18, v26, v27 op_sel:[0,0,1]
	v_med3_f32 v26, v31, s24, v237
	v_med3_f32 v27, v30, s24, v237
	v_cvt_pk_fp8_f32 v19, v26, v27 op_sel:[0,0,1]
	v_fma_f32 v27, v160, v25, v0
	v_min_f32_e32 v28, 0x40e00000, v27
	v_add_co_u32_e32 v26, vcc, s73, v16
	v_mul_f32_e32 v27, 0xc01d265f, v28
	v_exp_f32_e32 v29, v27
	v_addc_co_u32_e32 v27, vcc, 0, v17, vcc
	global_store_dwordx2 v[26:27], v[18:19], off
	v_fma_f32 v26, v161, v25, v1
	v_min_f32_e32 v26, 0x40e00000, v26
	v_mul_f32_e32 v27, 0xc01d265f, v26
	v_exp_f32_e32 v27, v27
	v_add_f32_e32 v19, 1.0, v29
	v_rcp_f32_e32 v19, v19
	v_fma_f32 v29, v163, v25, v3
	v_add_f32_e32 v27, 1.0, v27
	v_rcp_f32_e32 v27, v27
	v_mul_f32_e32 v19, v28, v19
	v_min_f32_e32 v29, 0x40e00000, v29
	v_mul_f32_e32 v30, 0xc01d265f, v29
	v_mul_f32_e32 v26, v26, v27
	v_fma_f32 v27, v162, v25, v2
	v_min_f32_e32 v27, 0x40e00000, v27
	v_mul_f32_e32 v28, 0xc01d265f, v27
	v_exp_f32_e32 v28, v28
	v_exp_f32_e32 v30, v30
	v_fma_f32 v31, v153, v25, v13
	v_min_f32_e32 v31, 0x40e00000, v31
	v_add_f32_e32 v28, 1.0, v28
	v_rcp_f32_e32 v28, v28
	v_mul_f32_e32 v32, 0xc01d265f, v31
	v_exp_f32_e32 v32, v32
	v_fma_f32 v18, v156, v25, v8
	v_mul_f32_e32 v27, v27, v28
	v_add_f32_e32 v28, 1.0, v30
	v_rcp_f32_e32 v28, v28
	v_med3_f32 v18, v18, s23, v236
	v_add_f32_e32 v18, 1.0, v18
	v_mul_f32_e32 v18, v18, v19
	v_mul_f32_e32 v28, v29, v28
	v_fma_f32 v29, v152, v25, v12
	v_min_f32_e32 v29, 0x40e00000, v29
	v_mul_f32_e32 v30, 0xc01d265f, v29
	v_exp_f32_e32 v30, v30
	v_fma_f32 v19, v157, v25, v9
	v_med3_f32 v19, v19, s23, v236
	v_add_f32_e32 v19, 1.0, v19
	v_add_f32_e32 v30, 1.0, v30
	v_rcp_f32_e32 v30, v30
	v_mul_f32_e32 v19, v19, v26
	v_fma_f32 v26, v158, v25, v10
	v_med3_f32 v26, v26, s23, v236
	v_mul_f32_e32 v29, v29, v30
	v_add_f32_e32 v30, 1.0, v32
	v_rcp_f32_e32 v30, v30
	v_add_f32_e32 v26, 1.0, v26
	v_mul_f32_e32 v26, v26, v27
	v_fma_f32 v27, v159, v25, v11
	v_mul_f32_e32 v30, v31, v30
	v_fma_f32 v31, v154, v25, v14
	v_min_f32_e32 v31, 0x40e00000, v31
	v_mul_f32_e32 v32, 0xc01d265f, v31
	v_exp_f32_e32 v32, v32
	v_fma_f32 v33, v155, v25, v15
	v_med3_f32 v27, v27, s23, v236
	v_min_f32_e32 v33, 0x40e00000, v33
	v_add_f32_e32 v27, 1.0, v27
	v_add_f32_e32 v32, 1.0, v32
;     __device__ __forceinline__ void operator()(const f32x4 (&acc)[2][2][4][2], const Unit& u, int wr, int wc, int fr, int fq) const {
;     ...
; #pragma unroll
;         for (int ai = 0; ai < 2; ++ai)
; #pragma unroll
;             for (int m = 0; m < 4; ++m) { const int r = row0 + ai * 128 + m * 16; const float rs = rsb[ai * 4 + m];
;                 float a[8];
; #pragma unroll
;                 for (int j = 0; j < 8; ++j) { const float gb = j < 4 ? g0[j & 3] : g1[j & 3], lb = j < 4 ? l0[j & 3] : l1[j & 3];
;                     const float gl = fminf(acc[ai][0][m][j >> 2][j & 3] * rs + gb, 7.0f), ln = fminf(fmaxf(acc[ai][1][m][j >> 2][j & 3] * rs + lb, -7.0f), 7.0f);
;                     a[j] = gl * __builtin_amdgcn_rcpf(1.0f + __builtin_amdgcn_exp2f(-1.702f * 1.4426950408889634f * gl)) * (ln + 1.0f); }
;                 v2u w; w.x = pk4_fp8(a[0], a[1], a[2], a[3]); w.y = pk4_fp8(a[4], a[5], a[6], a[7]);
;                 *(v2u*)(ACT + ((size_t)u.z * 256 + r) * FF + c0) = w; }
	v_mul_f32_e32 v34, 0xc01d265f, v33
	v_mul_f32_e32 v27, v27, v28
	v_fma_f32 v28, v148, v25, v4
	v_rcp_f32_e32 v32, v32
	v_exp_f32_e32 v34, v34
	v_med3_f32 v28, v28, s23, v236
	v_add_f32_e32 v28, 1.0, v28
	v_mul_f32_e32 v28, v28, v29
	v_fma_f32 v29, v149, v25, v5
	v_med3_f32 v29, v29, s23, v236
	v_mul_f32_e32 v31, v31, v32
	v_add_f32_e32 v32, 1.0, v34
	v_add_f32_e32 v29, 1.0, v29
	v_rcp_f32_e32 v32, v32
	v_mul_f32_e32 v29, v29, v30
	v_fma_f32 v30, v150, v25, v6
	v_med3_f32 v30, v30, s23, v236
	v_fma_f32 v25, v151, v25, v7
	v_add_f32_e32 v30, 1.0, v30
	v_med3_f32 v25, v25, s23, v236
	v_mul_f32_e32 v30, v30, v31
	v_mul_f32_e32 v31, v33, v32
	v_add_f32_e32 v25, 1.0, v25
	v_mul_f32_e32 v25, v25, v31
	v_med3_f32 v31, v18, s24, v237
	v_med3_f32 v19, v19, s24, v237
	v_mov_b32_e32 v18, v65
	v_cvt_pk_fp8_f32 v18, v31, v19
	v_med3_f32 v28, v28, s24, v237
	v_med3_f32 v29, v29, s24, v237
	v_mov_b32_e32 v19, v65
	v_cvt_pk_fp8_f32 v19, v28, v29
	v_med3_f32 v26, v26, s24, v237
	v_med3_f32 v27, v27, s24, v237
	v_cvt_pk_fp8_f32 v18, v26, v27 op_sel:[0,0,1]
	v_med3_f32 v26, v30, s24, v237
	v_med3_f32 v25, v25, s24, v237
	v_cvt_pk_fp8_f32 v19, v26, v25 op_sel:[0,0,1]
	v_fma_f32 v25, v144, v24, v0
	v_min_f32_e32 v25, 0x40e00000, v25
	v_mul_f32_e32 v27, 0xc01d265f, v25
	v_add_co_u32_e32 v26, vcc, s57, v16
	v_exp_f32_e32 v28, v27
	s_nop 0
	v_addc_co_u32_e32 v27, vcc, 0, v17, vcc
	global_store_dwordx2 v[26:27], v[18:19], off
	v_fma_f32 v26, v145, v24, v1
	v_min_f32_e32 v26, 0x40e00000, v26
	v_add_f32_e32 v19, 1.0, v28
	v_mul_f32_e32 v27, 0xc01d265f, v26
	v_rcp_f32_e32 v19, v19
	v_exp_f32_e32 v27, v27
	v_fma_f32 v28, v147, v24, v3
	v_min_f32_e32 v28, 0x40e00000, v28
	v_mul_f32_e32 v19, v25, v19
	v_add_f32_e32 v25, 1.0, v27
	v_rcp_f32_e32 v25, v25
	v_mul_f32_e32 v29, 0xc01d265f, v28
	v_exp_f32_e32 v29, v29
	v_fma_f32 v30, v137, v24, v13
	v_mul_f32_e32 v25, v26, v25
	v_fma_f32 v26, v146, v24, v2
	v_min_f32_e32 v26, 0x40e00000, v26
	v_mul_f32_e32 v27, 0xc01d265f, v26
	v_exp_f32_e32 v27, v27
	v_min_f32_e32 v30, 0x40e00000, v30
	v_mul_f32_e32 v31, 0xc01d265f, v30
	v_exp_f32_e32 v31, v31
	v_add_f32_e32 v27, 1.0, v27
	v_rcp_f32_e32 v27, v27
	v_fma_f32 v18, v140, v24, v8
	v_med3_f32 v18, v18, s23, v236
	v_add_f32_e32 v18, 1.0, v18
	v_mul_f32_e32 v26, v26, v27
	v_add_f32_e32 v27, 1.0, v29
	v_rcp_f32_e32 v27, v27
	v_mul_f32_e32 v18, v18, v19
	v_fma_f32 v19, v141, v24, v9
	v_med3_f32 v19, v19, s23, v236
	v_mul_f32_e32 v27, v28, v27
	v_fma_f32 v28, v136, v24, v12
	v_min_f32_e32 v28, 0x40e00000, v28
	v_mul_f32_e32 v29, 0xc01d265f, v28
	v_exp_f32_e32 v29, v29
	v_add_f32_e32 v19, 1.0, v19
	v_mul_f32_e32 v19, v19, v25
	v_fma_f32 v25, v142, v24, v10
	v_add_f32_e32 v29, 1.0, v29
	v_rcp_f32_e32 v29, v29
	v_med3_f32 v25, v25, s23, v236
	v_add_f32_e32 v25, 1.0, v25
	v_mul_f32_e32 v25, v25, v26
	v_mul_f32_e32 v28, v28, v29
	v_add_f32_e32 v29, 1.0, v31
	v_rcp_f32_e32 v29, v29
	v_fma_f32 v26, v143, v24, v11
	v_fma_f32 v32, v139, v24, v15
	v_med3_f32 v26, v26, s23, v236
	v_mul_f32_e32 v29, v30, v29
	v_fma_f32 v30, v138, v24, v14
	v_min_f32_e32 v30, 0x40e00000, v30
	v_mul_f32_e32 v31, 0xc01d265f, v30
	v_exp_f32_e32 v31, v31
	v_min_f32_e32 v32, 0x40e00000, v32
	v_add_f32_e32 v26, 1.0, v26
	v_mul_f32_e32 v33, 0xc01d265f, v32
	v_add_f32_e32 v31, 1.0, v31
	v_mul_f32_e32 v26, v26, v27
	v_fma_f32 v27, v132, v24, v4
	v_rcp_f32_e32 v31, v31
	v_exp_f32_e32 v33, v33
	v_med3_f32 v27, v27, s23, v236
	v_add_f32_e32 v27, 1.0, v27
	v_mul_f32_e32 v27, v27, v28
	v_fma_f32 v28, v133, v24, v5
	v_med3_f32 v28, v28, s23, v236
	v_mul_f32_e32 v30, v30, v31
	v_add_f32_e32 v31, 1.0, v33
	v_add_f32_e32 v28, 1.0, v28
	v_rcp_f32_e32 v31, v31
	v_mul_f32_e32 v28, v28, v29
	v_fma_f32 v29, v134, v24, v6
	v_med3_f32 v29, v29, s23, v236
	v_fma_f32 v24, v135, v24, v7
	v_add_f32_e32 v29, 1.0, v29
	v_med3_f32 v24, v24, s23, v236
	v_mul_f32_e32 v29, v29, v30
	v_mul_f32_e32 v30, v32, v31
	v_add_f32_e32 v24, 1.0, v24
	v_mul_f32_e32 v24, v24, v30
	v_med3_f32 v30, v18, s24, v237
	v_med3_f32 v19, v19, s24, v237
	v_mov_b32_e32 v18, v65
	v_cvt_pk_fp8_f32 v18, v30, v19
	v_med3_f32 v27, v27, s24, v237
	v_med3_f32 v28, v28, s24, v237
	v_mov_b32_e32 v19, v65
	v_cvt_pk_fp8_f32 v19, v27, v28
	v_med3_f32 v25, v25, s24, v237
	v_med3_f32 v26, v26, s24, v237
	v_cvt_pk_fp8_f32 v18, v25, v26 op_sel:[0,0,1]
	v_med3_f32 v25, v29, s24, v237
	v_med3_f32 v24, v24, s24, v237
	v_cvt_pk_fp8_f32 v19, v25, v24 op_sel:[0,0,1]
	v_fma_f32 v25, v128, v23, v0
	v_min_f32_e32 v26, 0x40e00000, v25
	v_add_co_u32_e32 v24, vcc, s69, v16
	v_mul_f32_e32 v25, 0xc01d265f, v26
	v_exp_f32_e32 v27, v25
	v_addc_co_u32_e32 v25, vcc, 0, v17, vcc
	global_store_dwordx2 v[24:25], v[18:19], off
	v_fma_f32 v24, v129, v23, v1
	v_min_f32_e32 v24, 0x40e00000, v24
	v_mul_f32_e32 v25, 0xc01d265f, v24
	v_exp_f32_e32 v25, v25
	v_add_f32_e32 v19, 1.0, v27
	v_rcp_f32_e32 v19, v19
	v_fma_f32 v27, v131, v23, v3
	v_add_f32_e32 v25, 1.0, v25
	v_rcp_f32_e32 v25, v25
	v_mul_f32_e32 v19, v26, v19
	v_min_f32_e32 v27, 0x40e00000, v27
	v_mul_f32_e32 v28, 0xc01d265f, v27
	v_mul_f32_e32 v24, v24, v25
	v_fma_f32 v25, v130, v23, v2
	v_min_f32_e32 v25, 0x40e00000, v25
	v_mul_f32_e32 v26, 0xc01d265f, v25
	v_exp_f32_e32 v26, v26
	v_exp_f32_e32 v28, v28
	v_fma_f32 v29, v121, v23, v13
	v_min_f32_e32 v29, 0x40e00000, v29
	v_add_f32_e32 v26, 1.0, v26
	v_rcp_f32_e32 v26, v26
	v_mul_f32_e32 v30, 0xc01d265f, v29
	v_exp_f32_e32 v30, v30
	v_fma_f32 v18, v124, v23, v8
	v_mul_f32_e32 v25, v25, v26
	v_add_f32_e32 v26, 1.0, v28
	v_rcp_f32_e32 v26, v26
	v_med3_f32 v18, v18, s23, v236
	v_add_f32_e32 v18, 1.0, v18
	v_mul_f32_e32 v18, v18, v19
	v_mul_f32_e32 v26, v27, v26
	v_fma_f32 v27, v120, v23, v12
;     __device__ __forceinline__ void operator()(const f32x4 (&acc)[2][2][4][2], const Unit& u, int wr, int wc, int fr, int fq) const {
;     ...
; #pragma unroll
;         for (int ai = 0; ai < 2; ++ai)
; #pragma unroll
;             for (int m = 0; m < 4; ++m) { const int r = row0 + ai * 128 + m * 16; const float rs = rsb[ai * 4 + m];
;                 float a[8];
; #pragma unroll
;                 for (int j = 0; j < 8; ++j) { const float gb = j < 4 ? g0[j & 3] : g1[j & 3], lb = j < 4 ? l0[j & 3] : l1[j & 3];
;                     const float gl = fminf(acc[ai][0][m][j >> 2][j & 3] * rs + gb, 7.0f), ln = fminf(fmaxf(acc[ai][1][m][j >> 2][j & 3] * rs + lb, -7.0f), 7.0f);
;                     a[j] = gl * __builtin_amdgcn_rcpf(1.0f + __builtin_amdgcn_exp2f(-1.702f * 1.4426950408889634f * gl)) * (ln + 1.0f); }
;                 v2u w; w.x = pk4_fp8(a[0], a[1], a[2], a[3]); w.y = pk4_fp8(a[4], a[5], a[6], a[7]);
;                 *(v2u*)(ACT + ((size_t)u.z * 256 + r) * FF + c0) = w; }
	v_min_f32_e32 v27, 0x40e00000, v27
	v_mul_f32_e32 v28, 0xc01d265f, v27
	v_exp_f32_e32 v28, v28
	v_fma_f32 v19, v125, v23, v9
	v_med3_f32 v19, v19, s23, v236
	v_add_f32_e32 v19, 1.0, v19
	v_add_f32_e32 v28, 1.0, v28
	v_rcp_f32_e32 v28, v28
	v_mul_f32_e32 v19, v19, v24
	v_fma_f32 v24, v126, v23, v10
	v_med3_f32 v24, v24, s23, v236
	v_mul_f32_e32 v27, v27, v28
	v_add_f32_e32 v28, 1.0, v30
	v_rcp_f32_e32 v28, v28
	v_add_f32_e32 v24, 1.0, v24
	v_mul_f32_e32 v24, v24, v25
	v_fma_f32 v25, v127, v23, v11
	v_mul_f32_e32 v28, v29, v28
	v_fma_f32 v29, v122, v23, v14
	v_min_f32_e32 v29, 0x40e00000, v29
	v_mul_f32_e32 v30, 0xc01d265f, v29
	v_exp_f32_e32 v30, v30
	v_fma_f32 v31, v123, v23, v15
	v_med3_f32 v25, v25, s23, v236
	v_min_f32_e32 v31, 0x40e00000, v31
	v_add_f32_e32 v25, 1.0, v25
	v_add_f32_e32 v30, 1.0, v30
	v_mul_f32_e32 v32, 0xc01d265f, v31
	v_mul_f32_e32 v25, v25, v26
	v_fma_f32 v26, v116, v23, v4
	v_rcp_f32_e32 v30, v30
	v_exp_f32_e32 v32, v32
	v_med3_f32 v26, v26, s23, v236
	v_add_f32_e32 v26, 1.0, v26
	v_mul_f32_e32 v26, v26, v27
	v_fma_f32 v27, v117, v23, v5
	v_med3_f32 v27, v27, s23, v236
	v_mul_f32_e32 v29, v29, v30
	v_add_f32_e32 v30, 1.0, v32
	v_add_f32_e32 v27, 1.0, v27
	v_rcp_f32_e32 v30, v30
	v_mul_f32_e32 v27, v27, v28
	v_fma_f32 v28, v118, v23, v6
	v_med3_f32 v28, v28, s23, v236
	v_fma_f32 v23, v119, v23, v7
	v_add_f32_e32 v28, 1.0, v28
	v_med3_f32 v23, v23, s23, v236
	v_mul_f32_e32 v28, v28, v29
	v_mul_f32_e32 v29, v31, v30
	v_add_f32_e32 v23, 1.0, v23
	v_mul_f32_e32 v23, v23, v29
	v_med3_f32 v29, v18, s24, v237
	v_med3_f32 v19, v19, s24, v237
	v_mov_b32_e32 v18, v65
	v_cvt_pk_fp8_f32 v18, v29, v19
	v_med3_f32 v26, v26, s24, v237
	v_med3_f32 v27, v27, s24, v237
	v_mov_b32_e32 v19, v65
	v_cvt_pk_fp8_f32 v19, v26, v27
	v_med3_f32 v24, v24, s24, v237
	v_med3_f32 v25, v25, s24, v237
	v_cvt_pk_fp8_f32 v18, v24, v25 op_sel:[0,0,1]
	v_med3_f32 v24, v28, s24, v237
	v_med3_f32 v23, v23, s24, v237
	v_cvt_pk_fp8_f32 v19, v24, v23 op_sel:[0,0,1]
	v_fma_f32 v23, v112, v22, v0
	v_min_f32_e32 v23, 0x40e00000, v23
	s_mov_b32 s4, 0x40000
	v_mul_f32_e32 v25, 0xc01d265f, v23
	v_add_co_u32_e32 v24, vcc, s4, v16
	v_exp_f32_e32 v26, v25
	s_nop 0
	v_addc_co_u32_e32 v25, vcc, 0, v17, vcc
	global_store_dwordx2 v[24:25], v[18:19], off
	v_fma_f32 v24, v113, v22, v1
	v_min_f32_e32 v24, 0x40e00000, v24
	v_add_f32_e32 v19, 1.0, v26
	v_mul_f32_e32 v25, 0xc01d265f, v24
	v_rcp_f32_e32 v19, v19
	v_exp_f32_e32 v25, v25
	v_fma_f32 v26, v115, v22, v3
	v_min_f32_e32 v26, 0x40e00000, v26
	v_mul_f32_e32 v19, v23, v19
	v_add_f32_e32 v23, 1.0, v25
	v_rcp_f32_e32 v23, v23
	v_mul_f32_e32 v27, 0xc01d265f, v26
	v_exp_f32_e32 v27, v27
	v_fma_f32 v28, v105, v22, v13
	v_mul_f32_e32 v23, v24, v23
	v_fma_f32 v24, v114, v22, v2
	v_min_f32_e32 v24, 0x40e00000, v24
	v_mul_f32_e32 v25, 0xc01d265f, v24
	v_exp_f32_e32 v25, v25
	v_min_f32_e32 v28, 0x40e00000, v28
	v_mul_f32_e32 v29, 0xc01d265f, v28
	v_exp_f32_e32 v29, v29
	v_add_f32_e32 v25, 1.0, v25
	v_rcp_f32_e32 v25, v25
	v_fma_f32 v18, v108, v22, v8
	v_med3_f32 v18, v18, s23, v236
	v_add_f32_e32 v18, 1.0, v18
	v_mul_f32_e32 v24, v24, v25
	v_add_f32_e32 v25, 1.0, v27
	v_rcp_f32_e32 v25, v25
	v_mul_f32_e32 v18, v18, v19
	v_fma_f32 v19, v109, v22, v9
	v_med3_f32 v19, v19, s23, v236
	v_mul_f32_e32 v25, v26, v25
	v_fma_f32 v26, v104, v22, v12
	v_min_f32_e32 v26, 0x40e00000, v26
	v_mul_f32_e32 v27, 0xc01d265f, v26
	v_exp_f32_e32 v27, v27
	v_add_f32_e32 v19, 1.0, v19
	v_mul_f32_e32 v19, v19, v23
	v_fma_f32 v23, v110, v22, v10
	v_add_f32_e32 v27, 1.0, v27
	v_rcp_f32_e32 v27, v27
	v_med3_f32 v23, v23, s23, v236
	v_add_f32_e32 v23, 1.0, v23
	v_mul_f32_e32 v23, v23, v24
	v_mul_f32_e32 v26, v26, v27
	v_add_f32_e32 v27, 1.0, v29
	v_rcp_f32_e32 v27, v27
	v_fma_f32 v24, v111, v22, v11
	v_fma_f32 v30, v107, v22, v15
	v_med3_f32 v24, v24, s23, v236
	v_mul_f32_e32 v27, v28, v27
	v_fma_f32 v28, v106, v22, v14
	v_min_f32_e32 v28, 0x40e00000, v28
	v_mul_f32_e32 v29, 0xc01d265f, v28
	v_exp_f32_e32 v29, v29
	v_min_f32_e32 v30, 0x40e00000, v30
	v_add_f32_e32 v24, 1.0, v24
	v_mul_f32_e32 v31, 0xc01d265f, v30
	v_add_f32_e32 v29, 1.0, v29
	v_mul_f32_e32 v24, v24, v25
	v_fma_f32 v25, v100, v22, v4
	v_rcp_f32_e32 v29, v29
	v_exp_f32_e32 v31, v31
	v_med3_f32 v25, v25, s23, v236
	v_add_f32_e32 v25, 1.0, v25
	v_mul_f32_e32 v25, v25, v26
	v_fma_f32 v26, v101, v22, v5
	v_med3_f32 v26, v26, s23, v236
	v_mul_f32_e32 v28, v28, v29
	v_add_f32_e32 v29, 1.0, v31
	v_add_f32_e32 v26, 1.0, v26
	v_rcp_f32_e32 v29, v29
	v_mul_f32_e32 v26, v26, v27
	v_fma_f32 v27, v102, v22, v6
	v_med3_f32 v27, v27, s23, v236
	v_fma_f32 v22, v103, v22, v7
	v_add_f32_e32 v27, 1.0, v27
	v_med3_f32 v22, v22, s23, v236
	v_mul_f32_e32 v27, v27, v28
	v_mul_f32_e32 v28, v30, v29
	v_add_f32_e32 v22, 1.0, v22
	v_mul_f32_e32 v22, v22, v28
	v_med3_f32 v28, v18, s24, v237
	v_med3_f32 v19, v19, s24, v237
	v_mov_b32_e32 v18, v65
	v_cvt_pk_fp8_f32 v18, v28, v19
	v_med3_f32 v25, v25, s24, v237
	v_med3_f32 v26, v26, s24, v237
	v_mov_b32_e32 v19, v65
	v_cvt_pk_fp8_f32 v19, v25, v26
	v_med3_f32 v23, v23, s24, v237
	v_med3_f32 v24, v24, s24, v237
	v_cvt_pk_fp8_f32 v18, v23, v24 op_sel:[0,0,1]
	v_med3_f32 v23, v27, s24, v237
	v_med3_f32 v22, v22, s24, v237
	v_cvt_pk_fp8_f32 v19, v23, v22 op_sel:[0,0,1]
	v_fma_f32 v23, v96, v21, v0
	s_mov_b32 s4, 0x48000
	v_min_f32_e32 v24, 0x40e00000, v23
	v_add_co_u32_e32 v22, vcc, s4, v16
	v_mul_f32_e32 v23, 0xc01d265f, v24
	v_exp_f32_e32 v25, v23
	v_addc_co_u32_e32 v23, vcc, 0, v17, vcc
	global_store_dwordx2 v[22:23], v[18:19], off
	v_fma_f32 v22, v97, v21, v1
	v_min_f32_e32 v22, 0x40e00000, v22
	v_mul_f32_e32 v23, 0xc01d265f, v22
	v_exp_f32_e32 v23, v23
	v_add_f32_e32 v19, 1.0, v25
;     __device__ __forceinline__ void operator()(const f32x4 (&acc)[2][2][4][2], const Unit& u, int wr, int wc, int fr, int fq) const {
;     ...
; #pragma unroll
;         for (int ai = 0; ai < 2; ++ai)
; #pragma unroll
;             for (int m = 0; m < 4; ++m) { const int r = row0 + ai * 128 + m * 16; const float rs = rsb[ai * 4 + m];
;                 float a[8];
; #pragma unroll
;                 for (int j = 0; j < 8; ++j) { const float gb = j < 4 ? g0[j & 3] : g1[j & 3], lb = j < 4 ? l0[j & 3] : l1[j & 3];
;                     const float gl = fminf(acc[ai][0][m][j >> 2][j & 3] * rs + gb, 7.0f), ln = fminf(fmaxf(acc[ai][1][m][j >> 2][j & 3] * rs + lb, -7.0f), 7.0f);
;                     a[j] = gl * __builtin_amdgcn_rcpf(1.0f + __builtin_amdgcn_exp2f(-1.702f * 1.4426950408889634f * gl)) * (ln + 1.0f); }
;                 v2u w; w.x = pk4_fp8(a[0], a[1], a[2], a[3]); w.y = pk4_fp8(a[4], a[5], a[6], a[7]);
;                 *(v2u*)(ACT + ((size_t)u.z * 256 + r) * FF + c0) = w; }
;     }
	v_rcp_f32_e32 v19, v19
	v_fma_f32 v25, v99, v21, v3
	v_add_f32_e32 v23, 1.0, v23
	v_rcp_f32_e32 v23, v23
	v_mul_f32_e32 v19, v24, v19
	v_min_f32_e32 v25, 0x40e00000, v25
	v_mul_f32_e32 v26, 0xc01d265f, v25
	v_mul_f32_e32 v22, v22, v23
	v_fma_f32 v23, v98, v21, v2
	v_min_f32_e32 v23, 0x40e00000, v23
	v_mul_f32_e32 v24, 0xc01d265f, v23
	v_exp_f32_e32 v24, v24
	v_exp_f32_e32 v26, v26
	v_fma_f32 v27, v89, v21, v13
	v_min_f32_e32 v27, 0x40e00000, v27
	v_add_f32_e32 v24, 1.0, v24
	v_rcp_f32_e32 v24, v24
	v_mul_f32_e32 v28, 0xc01d265f, v27
	v_exp_f32_e32 v28, v28
	v_fma_f32 v18, v92, v21, v8
	v_mul_f32_e32 v23, v23, v24
	v_add_f32_e32 v24, 1.0, v26
	v_rcp_f32_e32 v24, v24
	v_med3_f32 v18, v18, s23, v236
	v_add_f32_e32 v18, 1.0, v18
	v_mul_f32_e32 v18, v18, v19
	v_mul_f32_e32 v24, v25, v24
	v_fma_f32 v25, v88, v21, v12
	v_min_f32_e32 v25, 0x40e00000, v25
	v_mul_f32_e32 v26, 0xc01d265f, v25
	v_exp_f32_e32 v26, v26
	v_fma_f32 v19, v93, v21, v9
	v_med3_f32 v19, v19, s23, v236
	v_add_f32_e32 v19, 1.0, v19
	v_add_f32_e32 v26, 1.0, v26
	v_rcp_f32_e32 v26, v26
	v_mul_f32_e32 v19, v19, v22
	v_fma_f32 v22, v94, v21, v10
	v_med3_f32 v22, v22, s23, v236
	v_mul_f32_e32 v25, v25, v26
	v_add_f32_e32 v26, 1.0, v28
	v_rcp_f32_e32 v26, v26
	v_add_f32_e32 v22, 1.0, v22
	v_mul_f32_e32 v22, v22, v23
	v_fma_f32 v23, v95, v21, v11
	v_mul_f32_e32 v26, v27, v26
	v_fma_f32 v27, v90, v21, v14
	v_min_f32_e32 v27, 0x40e00000, v27
	v_mul_f32_e32 v28, 0xc01d265f, v27
	v_exp_f32_e32 v28, v28
	v_fma_f32 v29, v91, v21, v15
	v_med3_f32 v23, v23, s23, v236
	v_min_f32_e32 v29, 0x40e00000, v29
	v_add_f32_e32 v23, 1.0, v23
	v_add_f32_e32 v28, 1.0, v28
	v_mul_f32_e32 v30, 0xc01d265f, v29
	v_mul_f32_e32 v23, v23, v24
	v_fma_f32 v24, v84, v21, v4
	v_rcp_f32_e32 v28, v28
	v_exp_f32_e32 v30, v30
	v_med3_f32 v24, v24, s23, v236
	v_add_f32_e32 v24, 1.0, v24
	v_mul_f32_e32 v24, v24, v25
	v_fma_f32 v25, v85, v21, v5
	v_med3_f32 v25, v25, s23, v236
	v_mul_f32_e32 v27, v27, v28
	v_add_f32_e32 v28, 1.0, v30
	v_add_f32_e32 v25, 1.0, v25
	v_rcp_f32_e32 v28, v28
	v_mul_f32_e32 v25, v25, v26
	v_fma_f32 v26, v86, v21, v6
	v_med3_f32 v26, v26, s23, v236
	v_fma_f32 v21, v87, v21, v7
	v_add_f32_e32 v26, 1.0, v26
	v_med3_f32 v21, v21, s23, v236
	v_mul_f32_e32 v26, v26, v27
	v_mul_f32_e32 v27, v29, v28
	v_add_f32_e32 v21, 1.0, v21
	v_mul_f32_e32 v21, v21, v27
	v_med3_f32 v27, v18, s24, v237
	v_med3_f32 v19, v19, s24, v237
	v_mov_b32_e32 v18, v65
	v_cvt_pk_fp8_f32 v18, v27, v19
	v_med3_f32 v24, v24, s24, v237
	v_med3_f32 v25, v25, s24, v237
	v_mov_b32_e32 v19, v65
	v_cvt_pk_fp8_f32 v19, v24, v25
	v_mul_f32_e32 v20, 0x3b800000, v20
	v_med3_f32 v22, v22, s24, v237
	v_med3_f32 v23, v23, s24, v237
	v_fma_f32 v14, v74, v20, v14
	v_cvt_pk_fp8_f32 v18, v22, v23 op_sel:[0,0,1]
	v_med3_f32 v22, v26, s24, v237
	v_med3_f32 v21, v21, s24, v237
	v_min_f32_e32 v14, 0x40e00000, v14
	v_cvt_pk_fp8_f32 v19, v22, v21 op_sel:[0,0,1]
	v_mul_f32_e32 v21, 0xc01d265f, v14
	v_exp_f32_e32 v21, v21
	s_mov_b32 s4, 0x50000
	v_add_co_u32_e32 v22, vcc, s4, v16
	v_fma_f32 v13, v73, v20, v13
	s_nop 0
	v_addc_co_u32_e32 v23, vcc, 0, v17, vcc
	global_store_dwordx2 v[22:23], v[18:19], off
	v_add_f32_e32 v18, 1.0, v21
	v_rcp_f32_e32 v18, v18
	v_min_f32_e32 v13, 0x40e00000, v13
	v_fma_f32 v6, v70, v20, v6
	v_med3_f32 v6, v6, s23, v236
	v_mul_f32_e32 v14, v14, v18
	v_mul_f32_e32 v18, 0xc01d265f, v13
	v_exp_f32_e32 v18, v18
	v_add_f32_e32 v6, 1.0, v6
	v_fma_f32 v12, v72, v20, v12
	v_mul_f32_e32 v6, v6, v14
	v_add_f32_e32 v14, 1.0, v18
	v_min_f32_e32 v12, 0x40e00000, v12
	v_rcp_f32_e32 v14, v14
	v_mul_f32_e32 v18, 0xc01d265f, v12
	v_exp_f32_e32 v18, v18
	v_fma_f32 v5, v69, v20, v5
	v_med3_f32 v5, v5, s23, v236
	v_add_f32_e32 v5, 1.0, v5
	v_mul_f32_e32 v13, v13, v14
	v_mul_f32_e32 v5, v5, v13
	v_add_f32_e32 v13, 1.0, v18
	v_rcp_f32_e32 v13, v13
	v_fma_f32 v3, v83, v20, v3
	v_min_f32_e32 v3, 0x40e00000, v3
	v_fma_f32 v4, v68, v20, v4
	v_mul_f32_e32 v12, v12, v13
	v_mul_f32_e32 v13, 0xc01d265f, v3
	v_exp_f32_e32 v13, v13
	v_med3_f32 v4, v4, s23, v236
	v_add_f32_e32 v4, 1.0, v4
	v_fma_f32 v2, v82, v20, v2
	v_mul_f32_e32 v4, v4, v12
	v_add_f32_e32 v12, 1.0, v13
	v_min_f32_e32 v2, 0x40e00000, v2
	v_rcp_f32_e32 v12, v12
	v_mul_f32_e32 v13, 0xc01d265f, v2
	v_exp_f32_e32 v13, v13
	v_fma_f32 v11, v79, v20, v11
	v_med3_f32 v11, v11, s23, v236
	v_add_f32_e32 v11, 1.0, v11
	v_mul_f32_e32 v3, v3, v12
	v_mul_f32_e32 v3, v11, v3
	v_add_f32_e32 v11, 1.0, v13
	v_rcp_f32_e32 v11, v11
	v_fma_f32 v10, v78, v20, v10
	v_med3_f32 v10, v10, s23, v236
	v_fma_f32 v1, v81, v20, v1
	v_add_f32_e32 v10, 1.0, v10
	v_mul_f32_e32 v2, v2, v11
	v_min_f32_e32 v1, 0x40e00000, v1
	v_mul_f32_e32 v2, v10, v2
	v_mul_f32_e32 v10, 0xc01d265f, v1
	v_exp_f32_e32 v10, v10
	v_fmac_f32_e32 v0, v80, v20
	v_min_f32_e32 v0, 0x40e00000, v0
	v_mul_f32_e32 v11, 0xc01d265f, v0
	v_add_f32_e32 v10, 1.0, v10
	v_rcp_f32_e32 v10, v10
	v_exp_f32_e32 v11, v11
	v_fma_f32 v9, v77, v20, v9
	v_med3_f32 v9, v9, s23, v236
	v_fmac_f32_e32 v15, v75, v20
	v_add_f32_e32 v9, 1.0, v9
	v_mul_f32_e32 v1, v1, v10
	v_min_f32_e32 v10, 0x40e00000, v15
	v_mul_f32_e32 v1, v9, v1
	v_add_f32_e32 v9, 1.0, v11
	v_mul_f32_e32 v11, 0xc01d265f, v10
	v_rcp_f32_e32 v9, v9
	v_exp_f32_e32 v11, v11
	v_fmac_f32_e32 v8, v76, v20
	v_med3_f32 v8, v8, s23, v236
	v_mul_f32_e32 v0, v0, v9
	v_add_f32_e32 v9, 1.0, v11
	v_rcp_f32_e32 v9, v9
	v_fmac_f32_e32 v7, v71, v20
	v_add_f32_e32 v8, 1.0, v8
	v_med3_f32 v7, v7, s23, v236
	v_mul_f32_e32 v0, v8, v0
	v_mul_f32_e32 v8, v10, v9
	v_add_f32_e32 v7, 1.0, v7
	v_mul_f32_e32 v7, v7, v8
	v_med3_f32 v8, v0, s24, v237
	v_med3_f32 v1, v1, s24, v237
	v_mov_b32_e32 v0, v65
	v_cvt_pk_fp8_f32 v0, v8, v1
	v_med3_f32 v4, v4, s24, v237
	v_med3_f32 v5, v5, s24, v237
	v_mov_b32_e32 v1, v65
	v_cvt_pk_fp8_f32 v1, v4, v5
	v_med3_f32 v2, v2, s24, v237
	v_med3_f32 v3, v3, s24, v237
	v_cvt_pk_fp8_f32 v0, v2, v3 op_sel:[0,0,1]
	v_med3_f32 v2, v6, s24, v237
	v_med3_f32 v3, v7, s24, v237
	v_cvt_pk_fp8_f32 v1, v2, v3 op_sel:[0,0,1]
	v_add_co_u32_e32 v2, vcc, 0x58000, v16
	s_nop 1
	v_addc_co_u32_e32 v3, vcc, 0, v17, vcc
	global_store_dwordx2 v[2:3], v[0:1], off
	s_cbranch_scc1 .LBB0_1541
; __device__ __forceinline__ int lane_id_now() { unsigned z = 0u; asm volatile("" : "+v"(z)); return (int)__builtin_amdgcn_mbcnt_hi(~0u, __builtin_amdgcn_mbcnt_lo(~0u, z)); }
; #define GAS __attribute__((address_space(1)))
; template <bool GAIN, bool NT = false> __device__ __forceinline__ void titem8_load(const TItem& d, int lane, f32x4 (&r)[16], f32x4 (&g)[4]) {
;     const int q = lane & 7, kg = lane >> 3; const unsigned lo = (unsigned)((16 * kg) * d.N + 4 * q) * 4u;
;     const GAS char* base = (const GAS char*)d.src;
; #pragma unroll
;     for (int j = 0; j < 16; ++j) { const GAS f32x4* p = (const GAS f32x4*)(base + (size_t)j * (size_t)d.N * 4 + lo); r[j] = NT ? __builtin_nontemporal_load(p) : *p; }
;     if constexpr (GAIN) { const GAS char* gb = (const GAS char*)d.gain; const unsigned go = (unsigned)(16 * kg) * 4u;
; #pragma unroll
;         for (int j4 = 0; j4 < 4; ++j4) g[j4] = *(const GAS f32x4*)(gb + 16 * j4 + go); }
;     asm volatile("" ::: "memory"); __builtin_amdgcn_sched_barrier(0);
; }
; template <bool GAIN, bool NT = false> __device__ __forceinline__ void titem8_store(const TItem& d, int lane, const f32x4 (&r)[16], const f32x4 (&g)[4]) {
;     const int q = lane & 7, kg = lane >> 3; const unsigned lo = (unsigned)((4 * q) * d.ldk + 16 * kg);
;     GAS char* base = (GAS char*)d.dst;
;     f32x4 s[16];
; #pragma unroll
;     for (int j = 0; j < 16; ++j) s[j] = r[j] * ((GAIN ? g[j >> 2][j & 3] : 1.0f) * W8_SCALE);
; #pragma unroll
;     for (int i = 0; i < 4; ++i) { v4u w;
;         w.x = pk4_fp8w(s[0][i], s[1][i], s[2][i], s[3][i]); w.y = pk4_fp8w(s[4][i], s[5][i], s[6][i], s[7][i]);
;         w.z = pk4_fp8w(s[8][i], s[9][i], s[10][i], s[11][i]); w.w = pk4_fp8w(s[12][i], s[13][i], s[14][i], s[15][i]);
;         GAS v4u* p = (GAS v4u*)(base + (size_t)i * (size_t)d.ldk + lo);
;         if (NT) __builtin_nontemporal_store(w, p); else *p = w; }
; }
;     __device__ __forceinline__ void convert_share() const {
;         const int lane = lane_id_now(), gw = c * NWAVES + wave, NGW = G * NWAVES;
;         constexpr int NIT = E * (FF / 128) * (D / 32);
;         TSTREAM(NIT, dec_dn, TI8L_NT, TI8S_NT);
;     }
;     __device__ __forceinline__ void done(const Unit& u) const { if (u.pm == (c & 7)) convert_share(); }
	v_readlane_b32 s0, v254, 26
	v_readlane_b32 s1, v254, 27
	v_mov_b32_e32 v0, v65
	s_andn2_b64 vcc, exec, s[0:1]
	s_cbranch_vccnz .LBB0_1541
	v_mbcnt_lo_u32_b32 v64, -1, 0
	v_mbcnt_hi_u32_b32 v64, -1, v64
	v_and_b32_e32 v194, 7, v64
	v_lshrrev_b32_e32 v195, 3, v64
	v_lshlrev_b32_e32 v246, 17, v195
	v_lshl_or_b32 v246, v194, 4, v246
	v_add_u32_e32 v247, 0x2000, v246
	v_add_u32_e32 v248, 0x4000, v246
	v_add_u32_e32 v249, 0x6000, v246
	v_lshlrev_b32_e32 v250, 13, v194
	v_lshl_or_b32 v250, v195, 4, v250
	v_add_u32_e32 v251, 0x1000, v250
	v_readlane_b32 s0, v254, 60
	v_readlane_b32 s4, v254, 4
	v_readlane_b32 s5, v254, 5
	s_nop 3
	s_lshl_b32 s1, s92, 3
	s_add_i32 s0, s0, s1
	s_lshr_b32 s1, s0, 6
	s_bfe_u32 s2, s0, 0x40002
	s_and_b32 s0, s0, 3
	s_lshl_b32 s0, s0, 4
	s_lshl_b32 s35, s1, 24
	s_lshl_b32 s38, s2, 20
	s_add_i32 s35, s35, s38
	s_lshl_b32 s38, s0, 7
	s_add_i32 s35, s35, s38
	s_add_u32 s4, s4, s35
	s_addc_u32 s5, s5, 0
	s_add_u32 s6, s4, 0x8000
	s_addc_u32 s7, s5, 0
	s_add_u32 s8, s4, 0x10000
	s_addc_u32 s9, s5, 0
	s_add_u32 s38, s4, 0x18000
	s_addc_u32 s39, s5, 0
	s_lshl_b32 s35, s1, 22
	s_lshl_b32 s40, s0, 16
	s_add_i32 s35, s35, s40
	s_lshl_b32 s40, s2, 7
	s_add_i32 s35, s35, s40
	s_add_u32 s42, s78, 0x57dc8000
	s_addc_u32 s43, s79, 0
	s_add_u32 s42, s42, s35
	s_addc_u32 s43, s43, 0
	global_load_dwordx4 v[0:3], v246, s[4:5] offset:0 nt
	global_load_dwordx4 v[4:7], v247, s[4:5] offset:0 nt
	global_load_dwordx4 v[8:11], v248, s[4:5] offset:0 nt
	global_load_dwordx4 v[12:15], v249, s[4:5] offset:0 nt
	global_load_dwordx4 v[16:19], v246, s[6:7] offset:0 nt
	global_load_dwordx4 v[20:23], v247, s[6:7] offset:0 nt
	global_load_dwordx4 v[24:27], v248, s[6:7] offset:0 nt
	global_load_dwordx4 v[28:31], v249, s[6:7] offset:0 nt
	global_load_dwordx4 v[32:35], v246, s[8:9] offset:0 nt
	global_load_dwordx4 v[36:39], v247, s[8:9] offset:0 nt
	global_load_dwordx4 v[40:43], v248, s[8:9] offset:0 nt
	global_load_dwordx4 v[44:47], v249, s[8:9] offset:0 nt
	global_load_dwordx4 v[48:51], v246, s[38:39] offset:0 nt
	global_load_dwordx4 v[52:55], v247, s[38:39] offset:0 nt
	global_load_dwordx4 v[56:59], v248, s[38:39] offset:0 nt
	global_load_dwordx4 v[60:63], v249, s[38:39] offset:0 nt
	global_load_dwordx4 v[66:69], v246, s[4:5] offset:128 nt
	global_load_dwordx4 v[70:73], v247, s[4:5] offset:128 nt
	global_load_dwordx4 v[74:77], v248, s[4:5] offset:128 nt
	global_load_dwordx4 v[78:81], v249, s[4:5] offset:128 nt
	global_load_dwordx4 v[82:85], v246, s[6:7] offset:128 nt
	global_load_dwordx4 v[86:89], v247, s[6:7] offset:128 nt
	global_load_dwordx4 v[90:93], v248, s[6:7] offset:128 nt
	global_load_dwordx4 v[94:97], v249, s[6:7] offset:128 nt
	global_load_dwordx4 v[98:101], v246, s[8:9] offset:128 nt
	global_load_dwordx4 v[102:105], v247, s[8:9] offset:128 nt
	global_load_dwordx4 v[106:109], v248, s[8:9] offset:128 nt
	global_load_dwordx4 v[110:113], v249, s[8:9] offset:128 nt
	global_load_dwordx4 v[114:117], v246, s[38:39] offset:128 nt
	global_load_dwordx4 v[118:121], v247, s[38:39] offset:128 nt
	global_load_dwordx4 v[122:125], v248, s[38:39] offset:128 nt
	global_load_dwordx4 v[126:129], v249, s[38:39] offset:128 nt
	global_load_dwordx4 v[130:133], v246, s[4:5] offset:256 nt
	global_load_dwordx4 v[134:137], v247, s[4:5] offset:256 nt
	global_load_dwordx4 v[138:141], v248, s[4:5] offset:256 nt
	global_load_dwordx4 v[142:145], v249, s[4:5] offset:256 nt
	global_load_dwordx4 v[146:149], v246, s[6:7] offset:256 nt
	global_load_dwordx4 v[150:153], v247, s[6:7] offset:256 nt
	global_load_dwordx4 v[154:157], v248, s[6:7] offset:256 nt
	global_load_dwordx4 v[158:161], v249, s[6:7] offset:256 nt
	global_load_dwordx4 v[162:165], v246, s[8:9] offset:256 nt
	global_load_dwordx4 v[166:169], v247, s[8:9] offset:256 nt
	global_load_dwordx4 v[170:173], v248, s[8:9] offset:256 nt
	global_load_dwordx4 v[174:177], v249, s[8:9] offset:256 nt
	global_load_dwordx4 v[178:181], v246, s[38:39] offset:256 nt
	global_load_dwordx4 v[182:185], v247, s[38:39] offset:256 nt
	global_load_dwordx4 v[186:189], v248, s[38:39] offset:256 nt
	global_load_dwordx4 v[190:193], v249, s[38:39] offset:256 nt
	s_waitcnt vmcnt(32)
	v_pk_mul_f32 v[0:1], v[0:1], s[30:31] op_sel_hi:[1,0]
	v_pk_mul_f32 v[2:3], v[2:3], s[30:31] op_sel_hi:[1,0]
	v_pk_mul_f32 v[4:5], v[4:5], s[30:31] op_sel_hi:[1,0]
	v_pk_mul_f32 v[6:7], v[6:7], s[30:31] op_sel_hi:[1,0]
	v_pk_mul_f32 v[8:9], v[8:9], s[30:31] op_sel_hi:[1,0]
	v_pk_mul_f32 v[10:11], v[10:11], s[30:31] op_sel_hi:[1,0]
	v_pk_mul_f32 v[12:13], v[12:13], s[30:31] op_sel_hi:[1,0]
	v_pk_mul_f32 v[14:15], v[14:15], s[30:31] op_sel_hi:[1,0]
	v_pk_mul_f32 v[16:17], v[16:17], s[30:31] op_sel_hi:[1,0]
	v_pk_mul_f32 v[18:19], v[18:19], s[30:31] op_sel_hi:[1,0]
	v_pk_mul_f32 v[20:21], v[20:21], s[30:31] op_sel_hi:[1,0]
	v_pk_mul_f32 v[22:23], v[22:23], s[30:31] op_sel_hi:[1,0]
	v_pk_mul_f32 v[24:25], v[24:25], s[30:31] op_sel_hi:[1,0]
	v_pk_mul_f32 v[26:27], v[26:27], s[30:31] op_sel_hi:[1,0]
	v_pk_mul_f32 v[28:29], v[28:29], s[30:31] op_sel_hi:[1,0]
	v_pk_mul_f32 v[30:31], v[30:31], s[30:31] op_sel_hi:[1,0]
	v_pk_mul_f32 v[32:33], v[32:33], s[30:31] op_sel_hi:[1,0]
	v_pk_mul_f32 v[34:35], v[34:35], s[30:31] op_sel_hi:[1,0]
	v_pk_mul_f32 v[36:37], v[36:37], s[30:31] op_sel_hi:[1,0]
	v_pk_mul_f32 v[38:39], v[38:39], s[30:31] op_sel_hi:[1,0]
	v_pk_mul_f32 v[40:41], v[40:41], s[30:31] op_sel_hi:[1,0]
	v_pk_mul_f32 v[42:43], v[42:43], s[30:31] op_sel_hi:[1,0]
	v_pk_mul_f32 v[44:45], v[44:45], s[30:31] op_sel_hi:[1,0]
	v_pk_mul_f32 v[46:47], v[46:47], s[30:31] op_sel_hi:[1,0]
	v_pk_mul_f32 v[48:49], v[48:49], s[30:31] op_sel_hi:[1,0]
	v_pk_mul_f32 v[50:51], v[50:51], s[30:31] op_sel_hi:[1,0]
; #define GAS __attribute__((address_space(1)))
; template <bool GAIN, bool NT = false> __device__ __forceinline__ void titem8_load(const TItem& d, int lane, f32x4 (&r)[16], f32x4 (&g)[4]) {
;     const int q = lane & 7, kg = lane >> 3; const unsigned lo = (unsigned)((16 * kg) * d.N + 4 * q) * 4u;
;     const GAS char* base = (const GAS char*)d.src;
; #pragma unroll
;     for (int j = 0; j < 16; ++j) { const GAS f32x4* p = (const GAS f32x4*)(base + (size_t)j * (size_t)d.N * 4 + lo); r[j] = NT ? __builtin_nontemporal_load(p) : *p; }
;     if constexpr (GAIN) { const GAS char* gb = (const GAS char*)d.gain; const unsigned go = (unsigned)(16 * kg) * 4u;
; #pragma unroll
;         for (int j4 = 0; j4 < 4; ++j4) g[j4] = *(const GAS f32x4*)(gb + 16 * j4 + go); }
;     asm volatile("" ::: "memory"); __builtin_amdgcn_sched_barrier(0);
; }
; template <bool GAIN, bool NT = false> __device__ __forceinline__ void titem8_store(const TItem& d, int lane, const f32x4 (&r)[16], const f32x4 (&g)[4]) {
;     const int q = lane & 7, kg = lane >> 3; const unsigned lo = (unsigned)((4 * q) * d.ldk + 16 * kg);
;     GAS char* base = (GAS char*)d.dst;
;     f32x4 s[16];
; #pragma unroll
;     for (int j = 0; j < 16; ++j) s[j] = r[j] * ((GAIN ? g[j >> 2][j & 3] : 1.0f) * W8_SCALE);
; #pragma unroll
;     for (int i = 0; i < 4; ++i) { v4u w;
;         w.x = pk4_fp8w(s[0][i], s[1][i], s[2][i], s[3][i]); w.y = pk4_fp8w(s[4][i], s[5][i], s[6][i], s[7][i]);
;         w.z = pk4_fp8w(s[8][i], s[9][i], s[10][i], s[11][i]); w.w = pk4_fp8w(s[12][i], s[13][i], s[14][i], s[15][i]);
;         GAS v4u* p = (GAS v4u*)(base + (size_t)i * (size_t)d.ldk + lo);
;         if (NT) __builtin_nontemporal_store(w, p); else *p = w; }
; }
	v_pk_mul_f32 v[52:53], v[52:53], s[30:31] op_sel_hi:[1,0]
	v_pk_mul_f32 v[54:55], v[54:55], s[30:31] op_sel_hi:[1,0]
	v_pk_mul_f32 v[56:57], v[56:57], s[30:31] op_sel_hi:[1,0]
	v_pk_mul_f32 v[58:59], v[58:59], s[30:31] op_sel_hi:[1,0]
	v_pk_mul_f32 v[60:61], v[60:61], s[30:31] op_sel_hi:[1,0]
	v_pk_mul_f32 v[62:63], v[62:63], s[30:31] op_sel_hi:[1,0]
	v_med3_f32 v0, v0, s24, v237
	v_med3_f32 v1, v1, s24, v237
	v_med3_f32 v2, v2, s24, v237
	v_med3_f32 v3, v3, s24, v237
	v_med3_f32 v4, v4, s24, v237
	v_med3_f32 v5, v5, s24, v237
	v_med3_f32 v6, v6, s24, v237
	v_med3_f32 v7, v7, s24, v237
	v_med3_f32 v8, v8, s24, v237
	v_med3_f32 v9, v9, s24, v237
	v_med3_f32 v10, v10, s24, v237
	v_med3_f32 v11, v11, s24, v237
	v_med3_f32 v12, v12, s24, v237
	v_med3_f32 v13, v13, s24, v237
	v_med3_f32 v14, v14, s24, v237
	v_med3_f32 v15, v15, s24, v237
	v_med3_f32 v16, v16, s24, v237
	v_med3_f32 v17, v17, s24, v237
	v_med3_f32 v18, v18, s24, v237
	v_med3_f32 v19, v19, s24, v237
	v_med3_f32 v20, v20, s24, v237
	v_med3_f32 v21, v21, s24, v237
	v_med3_f32 v22, v22, s24, v237
	v_med3_f32 v23, v23, s24, v237
	v_med3_f32 v24, v24, s24, v237
	v_med3_f32 v25, v25, s24, v237
	v_med3_f32 v26, v26, s24, v237
	v_med3_f32 v27, v27, s24, v237
	v_med3_f32 v28, v28, s24, v237
	v_med3_f32 v29, v29, s24, v237
	v_med3_f32 v30, v30, s24, v237
	v_med3_f32 v31, v31, s24, v237
	v_med3_f32 v32, v32, s24, v237
	v_med3_f32 v33, v33, s24, v237
	v_med3_f32 v34, v34, s24, v237
	v_med3_f32 v35, v35, s24, v237
	v_med3_f32 v36, v36, s24, v237
	v_med3_f32 v37, v37, s24, v237
	v_med3_f32 v38, v38, s24, v237
	v_med3_f32 v39, v39, s24, v237
	v_med3_f32 v40, v40, s24, v237
	v_med3_f32 v41, v41, s24, v237
	v_med3_f32 v42, v42, s24, v237
	v_med3_f32 v43, v43, s24, v237
	v_med3_f32 v44, v44, s24, v237
	v_med3_f32 v45, v45, s24, v237
	v_med3_f32 v46, v46, s24, v237
	v_med3_f32 v47, v47, s24, v237
	v_med3_f32 v48, v48, s24, v237
	v_med3_f32 v49, v49, s24, v237
	v_med3_f32 v50, v50, s24, v237
	v_med3_f32 v51, v51, s24, v237
	v_med3_f32 v52, v52, s24, v237
	v_med3_f32 v53, v53, s24, v237
	v_med3_f32 v54, v54, s24, v237
	v_med3_f32 v55, v55, s24, v237
	v_med3_f32 v56, v56, s24, v237
	v_med3_f32 v57, v57, s24, v237
	v_med3_f32 v58, v58, s24, v237
	v_med3_f32 v59, v59, s24, v237
	v_med3_f32 v60, v60, s24, v237
	v_med3_f32 v61, v61, s24, v237
	v_med3_f32 v62, v62, s24, v237
	v_med3_f32 v63, v63, s24, v237
	v_cvt_pk_fp8_f32 v0, v0, v4
	v_cvt_pk_fp8_f32 v0, v8, v12 op_sel:[0,0,1]
	v_cvt_pk_fp8_f32 v4, v1, v5
	v_cvt_pk_fp8_f32 v4, v9, v13 op_sel:[0,0,1]
	v_cvt_pk_fp8_f32 v8, v2, v6
	v_cvt_pk_fp8_f32 v8, v10, v14 op_sel:[0,0,1]
	v_cvt_pk_fp8_f32 v12, v3, v7
	v_cvt_pk_fp8_f32 v12, v11, v15 op_sel:[0,0,1]
	v_cvt_pk_fp8_f32 v1, v16, v20
	v_cvt_pk_fp8_f32 v1, v24, v28 op_sel:[0,0,1]
	v_cvt_pk_fp8_f32 v5, v17, v21
	v_cvt_pk_fp8_f32 v5, v25, v29 op_sel:[0,0,1]
	v_cvt_pk_fp8_f32 v9, v18, v22
	v_cvt_pk_fp8_f32 v9, v26, v30 op_sel:[0,0,1]
	v_cvt_pk_fp8_f32 v13, v19, v23
	v_cvt_pk_fp8_f32 v13, v27, v31 op_sel:[0,0,1]
	v_cvt_pk_fp8_f32 v2, v32, v36
	v_cvt_pk_fp8_f32 v2, v40, v44 op_sel:[0,0,1]
	v_cvt_pk_fp8_f32 v6, v33, v37
	v_cvt_pk_fp8_f32 v6, v41, v45 op_sel:[0,0,1]
	v_cvt_pk_fp8_f32 v10, v34, v38
	v_cvt_pk_fp8_f32 v10, v42, v46 op_sel:[0,0,1]
	v_cvt_pk_fp8_f32 v14, v35, v39
	v_cvt_pk_fp8_f32 v14, v43, v47 op_sel:[0,0,1]
	v_cvt_pk_fp8_f32 v3, v48, v52
	v_cvt_pk_fp8_f32 v3, v56, v60 op_sel:[0,0,1]
	v_cvt_pk_fp8_f32 v7, v49, v53
	v_cvt_pk_fp8_f32 v7, v57, v61 op_sel:[0,0,1]
	v_cvt_pk_fp8_f32 v11, v50, v54
	v_cvt_pk_fp8_f32 v11, v58, v62 op_sel:[0,0,1]
	v_cvt_pk_fp8_f32 v15, v51, v55
	v_cvt_pk_fp8_f32 v15, v59, v63 op_sel:[0,0,1]
	global_store_dwordx4 v250, v[0:3], s[42:43] nt
	global_store_dwordx4 v250, v[4:7], s[42:43] offset:2048 nt
	global_store_dwordx4 v251, v[8:11], s[42:43] nt
	global_store_dwordx4 v251, v[12:15], s[42:43] offset:2048 nt
	s_add_u32 s42, s42, 0x10000
	s_addc_u32 s43, s43, 0
	global_load_dwordx4 v[0:3], v246, s[4:5] offset:384 nt
	global_load_dwordx4 v[4:7], v247, s[4:5] offset:384 nt
	global_load_dwordx4 v[8:11], v248, s[4:5] offset:384 nt
	global_load_dwordx4 v[12:15], v249, s[4:5] offset:384 nt
	global_load_dwordx4 v[16:19], v246, s[6:7] offset:384 nt
	global_load_dwordx4 v[20:23], v247, s[6:7] offset:384 nt
	global_load_dwordx4 v[24:27], v248, s[6:7] offset:384 nt
	global_load_dwordx4 v[28:31], v249, s[6:7] offset:384 nt
	global_load_dwordx4 v[32:35], v246, s[8:9] offset:384 nt
	global_load_dwordx4 v[36:39], v247, s[8:9] offset:384 nt
	global_load_dwordx4 v[40:43], v248, s[8:9] offset:384 nt
	global_load_dwordx4 v[44:47], v249, s[8:9] offset:384 nt
	global_load_dwordx4 v[48:51], v246, s[38:39] offset:384 nt
	global_load_dwordx4 v[52:55], v247, s[38:39] offset:384 nt
	global_load_dwordx4 v[56:59], v248, s[38:39] offset:384 nt
	global_load_dwordx4 v[60:63], v249, s[38:39] offset:384 nt
	s_waitcnt vmcnt(36)
; #define GAS __attribute__((address_space(1)))
; template <bool GAIN, bool NT = false> __device__ __forceinline__ void titem8_load(const TItem& d, int lane, f32x4 (&r)[16], f32x4 (&g)[4]) {
;     const int q = lane & 7, kg = lane >> 3; const unsigned lo = (unsigned)((16 * kg) * d.N + 4 * q) * 4u;
;     const GAS char* base = (const GAS char*)d.src;
; #pragma unroll
;     for (int j = 0; j < 16; ++j) { const GAS f32x4* p = (const GAS f32x4*)(base + (size_t)j * (size_t)d.N * 4 + lo); r[j] = NT ? __builtin_nontemporal_load(p) : *p; }
;     if constexpr (GAIN) { const GAS char* gb = (const GAS char*)d.gain; const unsigned go = (unsigned)(16 * kg) * 4u;
; #pragma unroll
;         for (int j4 = 0; j4 < 4; ++j4) g[j4] = *(const GAS f32x4*)(gb + 16 * j4 + go); }
;     asm volatile("" ::: "memory"); __builtin_amdgcn_sched_barrier(0);
; }
; template <bool GAIN, bool NT = false> __device__ __forceinline__ void titem8_store(const TItem& d, int lane, const f32x4 (&r)[16], const f32x4 (&g)[4]) {
;     const int q = lane & 7, kg = lane >> 3; const unsigned lo = (unsigned)((4 * q) * d.ldk + 16 * kg);
;     GAS char* base = (GAS char*)d.dst;
;     f32x4 s[16];
; #pragma unroll
;     for (int j = 0; j < 16; ++j) s[j] = r[j] * ((GAIN ? g[j >> 2][j & 3] : 1.0f) * W8_SCALE);
; #pragma unroll
;     for (int i = 0; i < 4; ++i) { v4u w;
;         w.x = pk4_fp8w(s[0][i], s[1][i], s[2][i], s[3][i]); w.y = pk4_fp8w(s[4][i], s[5][i], s[6][i], s[7][i]);
;         w.z = pk4_fp8w(s[8][i], s[9][i], s[10][i], s[11][i]); w.w = pk4_fp8w(s[12][i], s[13][i], s[14][i], s[15][i]);
;         GAS v4u* p = (GAS v4u*)(base + (size_t)i * (size_t)d.ldk + lo);
;         if (NT) __builtin_nontemporal_store(w, p); else *p = w; }
; }
	v_pk_mul_f32 v[66:67], v[66:67], s[30:31] op_sel_hi:[1,0]
	v_pk_mul_f32 v[68:69], v[68:69], s[30:31] op_sel_hi:[1,0]
	v_pk_mul_f32 v[70:71], v[70:71], s[30:31] op_sel_hi:[1,0]
	v_pk_mul_f32 v[72:73], v[72:73], s[30:31] op_sel_hi:[1,0]
	v_pk_mul_f32 v[74:75], v[74:75], s[30:31] op_sel_hi:[1,0]
	v_pk_mul_f32 v[76:77], v[76:77], s[30:31] op_sel_hi:[1,0]
	v_pk_mul_f32 v[78:79], v[78:79], s[30:31] op_sel_hi:[1,0]
	v_pk_mul_f32 v[80:81], v[80:81], s[30:31] op_sel_hi:[1,0]
	v_pk_mul_f32 v[82:83], v[82:83], s[30:31] op_sel_hi:[1,0]
	v_pk_mul_f32 v[84:85], v[84:85], s[30:31] op_sel_hi:[1,0]
	v_pk_mul_f32 v[86:87], v[86:87], s[30:31] op_sel_hi:[1,0]
	v_pk_mul_f32 v[88:89], v[88:89], s[30:31] op_sel_hi:[1,0]
	v_pk_mul_f32 v[90:91], v[90:91], s[30:31] op_sel_hi:[1,0]
	v_pk_mul_f32 v[92:93], v[92:93], s[30:31] op_sel_hi:[1,0]
	v_pk_mul_f32 v[94:95], v[94:95], s[30:31] op_sel_hi:[1,0]
	v_pk_mul_f32 v[96:97], v[96:97], s[30:31] op_sel_hi:[1,0]
	v_pk_mul_f32 v[98:99], v[98:99], s[30:31] op_sel_hi:[1,0]
	v_pk_mul_f32 v[100:101], v[100:101], s[30:31] op_sel_hi:[1,0]
	v_pk_mul_f32 v[102:103], v[102:103], s[30:31] op_sel_hi:[1,0]
	v_pk_mul_f32 v[104:105], v[104:105], s[30:31] op_sel_hi:[1,0]
	v_pk_mul_f32 v[106:107], v[106:107], s[30:31] op_sel_hi:[1,0]
	v_pk_mul_f32 v[108:109], v[108:109], s[30:31] op_sel_hi:[1,0]
	v_pk_mul_f32 v[110:111], v[110:111], s[30:31] op_sel_hi:[1,0]
	v_pk_mul_f32 v[112:113], v[112:113], s[30:31] op_sel_hi:[1,0]
	v_pk_mul_f32 v[114:115], v[114:115], s[30:31] op_sel_hi:[1,0]
	v_pk_mul_f32 v[116:117], v[116:117], s[30:31] op_sel_hi:[1,0]
	v_pk_mul_f32 v[118:119], v[118:119], s[30:31] op_sel_hi:[1,0]
	v_pk_mul_f32 v[120:121], v[120:121], s[30:31] op_sel_hi:[1,0]
	v_pk_mul_f32 v[122:123], v[122:123], s[30:31] op_sel_hi:[1,0]
	v_pk_mul_f32 v[124:125], v[124:125], s[30:31] op_sel_hi:[1,0]
	v_pk_mul_f32 v[126:127], v[126:127], s[30:31] op_sel_hi:[1,0]
	v_pk_mul_f32 v[128:129], v[128:129], s[30:31] op_sel_hi:[1,0]
	v_med3_f32 v66, v66, s24, v237
	v_med3_f32 v67, v67, s24, v237
	v_med3_f32 v68, v68, s24, v237
	v_med3_f32 v69, v69, s24, v237
	v_med3_f32 v70, v70, s24, v237
	v_med3_f32 v71, v71, s24, v237
	v_med3_f32 v72, v72, s24, v237
	v_med3_f32 v73, v73, s24, v237
	v_med3_f32 v74, v74, s24, v237
	v_med3_f32 v75, v75, s24, v237
	v_med3_f32 v76, v76, s24, v237
	v_med3_f32 v77, v77, s24, v237
	v_med3_f32 v78, v78, s24, v237
	v_med3_f32 v79, v79, s24, v237
	v_med3_f32 v80, v80, s24, v237
	v_med3_f32 v81, v81, s24, v237
	v_med3_f32 v82, v82, s24, v237
	v_med3_f32 v83, v83, s24, v237
	v_med3_f32 v84, v84, s24, v237
	v_med3_f32 v85, v85, s24, v237
	v_med3_f32 v86, v86, s24, v237
	v_med3_f32 v87, v87, s24, v237
	v_med3_f32 v88, v88, s24, v237
	v_med3_f32 v89, v89, s24, v237
	v_med3_f32 v90, v90, s24, v237
	v_med3_f32 v91, v91, s24, v237
	v_med3_f32 v92, v92, s24, v237
	v_med3_f32 v93, v93, s24, v237
	v_med3_f32 v94, v94, s24, v237
	v_med3_f32 v95, v95, s24, v237
	v_med3_f32 v96, v96, s24, v237
	v_med3_f32 v97, v97, s24, v237
	v_med3_f32 v98, v98, s24, v237
	v_med3_f32 v99, v99, s24, v237
	v_med3_f32 v100, v100, s24, v237
	v_med3_f32 v101, v101, s24, v237
	v_med3_f32 v102, v102, s24, v237
	v_med3_f32 v103, v103, s24, v237
	v_med3_f32 v104, v104, s24, v237
	v_med3_f32 v105, v105, s24, v237
	v_med3_f32 v106, v106, s24, v237
	v_med3_f32 v107, v107, s24, v237
	v_med3_f32 v108, v108, s24, v237
	v_med3_f32 v109, v109, s24, v237
	v_med3_f32 v110, v110, s24, v237
	v_med3_f32 v111, v111, s24, v237
	v_med3_f32 v112, v112, s24, v237
	v_med3_f32 v113, v113, s24, v237
	v_med3_f32 v114, v114, s24, v237
	v_med3_f32 v115, v115, s24, v237
	v_med3_f32 v116, v116, s24, v237
	v_med3_f32 v117, v117, s24, v237
	v_med3_f32 v118, v118, s24, v237
	v_med3_f32 v119, v119, s24, v237
	v_med3_f32 v120, v120, s24, v237
	v_med3_f32 v121, v121, s24, v237
	v_med3_f32 v122, v122, s24, v237
	v_med3_f32 v123, v123, s24, v237
	v_med3_f32 v124, v124, s24, v237
	v_med3_f32 v125, v125, s24, v237
	v_med3_f32 v126, v126, s24, v237
	v_med3_f32 v127, v127, s24, v237
	v_med3_f32 v128, v128, s24, v237
	v_med3_f32 v129, v129, s24, v237
	v_cvt_pk_fp8_f32 v66, v66, v70
	v_cvt_pk_fp8_f32 v66, v74, v78 op_sel:[0,0,1]
	v_cvt_pk_fp8_f32 v70, v67, v71
	v_cvt_pk_fp8_f32 v70, v75, v79 op_sel:[0,0,1]
	v_cvt_pk_fp8_f32 v74, v68, v72
	v_cvt_pk_fp8_f32 v74, v76, v80 op_sel:[0,0,1]
	v_cvt_pk_fp8_f32 v78, v69, v73
	v_cvt_pk_fp8_f32 v78, v77, v81 op_sel:[0,0,1]
	v_cvt_pk_fp8_f32 v67, v82, v86
	v_cvt_pk_fp8_f32 v67, v90, v94 op_sel:[0,0,1]
	v_cvt_pk_fp8_f32 v71, v83, v87
	v_cvt_pk_fp8_f32 v71, v91, v95 op_sel:[0,0,1]
	v_cvt_pk_fp8_f32 v75, v84, v88
	v_cvt_pk_fp8_f32 v75, v92, v96 op_sel:[0,0,1]
	v_cvt_pk_fp8_f32 v79, v85, v89
	v_cvt_pk_fp8_f32 v79, v93, v97 op_sel:[0,0,1]
	v_cvt_pk_fp8_f32 v68, v98, v102
	v_cvt_pk_fp8_f32 v68, v106, v110 op_sel:[0,0,1]
	v_cvt_pk_fp8_f32 v72, v99, v103
	v_cvt_pk_fp8_f32 v72, v107, v111 op_sel:[0,0,1]
	v_cvt_pk_fp8_f32 v76, v100, v104
	v_cvt_pk_fp8_f32 v76, v108, v112 op_sel:[0,0,1]
	v_cvt_pk_fp8_f32 v80, v101, v105
	v_cvt_pk_fp8_f32 v80, v109, v113 op_sel:[0,0,1]
	v_cvt_pk_fp8_f32 v69, v114, v118
	v_cvt_pk_fp8_f32 v69, v122, v126 op_sel:[0,0,1]
	v_cvt_pk_fp8_f32 v73, v115, v119
	v_cvt_pk_fp8_f32 v73, v123, v127 op_sel:[0,0,1]
	v_cvt_pk_fp8_f32 v77, v116, v120
	v_cvt_pk_fp8_f32 v77, v124, v128 op_sel:[0,0,1]
	v_cvt_pk_fp8_f32 v81, v117, v121
	v_cvt_pk_fp8_f32 v81, v125, v129 op_sel:[0,0,1]
	global_store_dwordx4 v250, v[66:69], s[42:43] nt
	global_store_dwordx4 v250, v[70:73], s[42:43] offset:2048 nt
	global_store_dwordx4 v251, v[74:77], s[42:43] nt
	global_store_dwordx4 v251, v[78:81], s[42:43] offset:2048 nt
	s_add_u32 s42, s42, 0x10000
	s_addc_u32 s43, s43, 0
	global_load_dwordx4 v[66:69], v246, s[4:5] offset:512 nt
	global_load_dwordx4 v[70:73], v247, s[4:5] offset:512 nt
	global_load_dwordx4 v[74:77], v248, s[4:5] offset:512 nt
	global_load_dwordx4 v[78:81], v249, s[4:5] offset:512 nt
	global_load_dwordx4 v[82:85], v246, s[6:7] offset:512 nt
	global_load_dwordx4 v[86:89], v247, s[6:7] offset:512 nt
	global_load_dwordx4 v[90:93], v248, s[6:7] offset:512 nt
	global_load_dwordx4 v[94:97], v249, s[6:7] offset:512 nt
	global_load_dwordx4 v[98:101], v246, s[8:9] offset:512 nt
	global_load_dwordx4 v[102:105], v247, s[8:9] offset:512 nt
	global_load_dwordx4 v[106:109], v248, s[8:9] offset:512 nt
	global_load_dwordx4 v[110:113], v249, s[8:9] offset:512 nt
	global_load_dwordx4 v[114:117], v246, s[38:39] offset:512 nt
	global_load_dwordx4 v[118:121], v247, s[38:39] offset:512 nt
	global_load_dwordx4 v[122:125], v248, s[38:39] offset:512 nt
	global_load_dwordx4 v[126:129], v249, s[38:39] offset:512 nt
	s_waitcnt vmcnt(40)
; #define GAS __attribute__((address_space(1)))
; template <bool GAIN, bool NT = false> __device__ __forceinline__ void titem8_load(const TItem& d, int lane, f32x4 (&r)[16], f32x4 (&g)[4]) {
;     const int q = lane & 7, kg = lane >> 3; const unsigned lo = (unsigned)((16 * kg) * d.N + 4 * q) * 4u;
;     const GAS char* base = (const GAS char*)d.src;
; #pragma unroll
;     for (int j = 0; j < 16; ++j) { const GAS f32x4* p = (const GAS f32x4*)(base + (size_t)j * (size_t)d.N * 4 + lo); r[j] = NT ? __builtin_nontemporal_load(p) : *p; }
;     if constexpr (GAIN) { const GAS char* gb = (const GAS char*)d.gain; const unsigned go = (unsigned)(16 * kg) * 4u;
; #pragma unroll
;         for (int j4 = 0; j4 < 4; ++j4) g[j4] = *(const GAS f32x4*)(gb + 16 * j4 + go); }
;     asm volatile("" ::: "memory"); __builtin_amdgcn_sched_barrier(0);
; }
; template <bool GAIN, bool NT = false> __device__ __forceinline__ void titem8_store(const TItem& d, int lane, const f32x4 (&r)[16], const f32x4 (&g)[4]) {
;     const int q = lane & 7, kg = lane >> 3; const unsigned lo = (unsigned)((4 * q) * d.ldk + 16 * kg);
;     GAS char* base = (GAS char*)d.dst;
;     f32x4 s[16];
; #pragma unroll
;     for (int j = 0; j < 16; ++j) s[j] = r[j] * ((GAIN ? g[j >> 2][j & 3] : 1.0f) * W8_SCALE);
; #pragma unroll
;     for (int i = 0; i < 4; ++i) { v4u w;
;         w.x = pk4_fp8w(s[0][i], s[1][i], s[2][i], s[3][i]); w.y = pk4_fp8w(s[4][i], s[5][i], s[6][i], s[7][i]);
;         w.z = pk4_fp8w(s[8][i], s[9][i], s[10][i], s[11][i]); w.w = pk4_fp8w(s[12][i], s[13][i], s[14][i], s[15][i]);
;         GAS v4u* p = (GAS v4u*)(base + (size_t)i * (size_t)d.ldk + lo);
;         if (NT) __builtin_nontemporal_store(w, p); else *p = w; }
; }
	v_pk_mul_f32 v[130:131], v[130:131], s[30:31] op_sel_hi:[1,0]
	v_pk_mul_f32 v[132:133], v[132:133], s[30:31] op_sel_hi:[1,0]
	v_pk_mul_f32 v[134:135], v[134:135], s[30:31] op_sel_hi:[1,0]
	v_pk_mul_f32 v[136:137], v[136:137], s[30:31] op_sel_hi:[1,0]
	v_pk_mul_f32 v[138:139], v[138:139], s[30:31] op_sel_hi:[1,0]
	v_pk_mul_f32 v[140:141], v[140:141], s[30:31] op_sel_hi:[1,0]
	v_pk_mul_f32 v[142:143], v[142:143], s[30:31] op_sel_hi:[1,0]
	v_pk_mul_f32 v[144:145], v[144:145], s[30:31] op_sel_hi:[1,0]
	v_pk_mul_f32 v[146:147], v[146:147], s[30:31] op_sel_hi:[1,0]
	v_pk_mul_f32 v[148:149], v[148:149], s[30:31] op_sel_hi:[1,0]
	v_pk_mul_f32 v[150:151], v[150:151], s[30:31] op_sel_hi:[1,0]
	v_pk_mul_f32 v[152:153], v[152:153], s[30:31] op_sel_hi:[1,0]
	v_pk_mul_f32 v[154:155], v[154:155], s[30:31] op_sel_hi:[1,0]
	v_pk_mul_f32 v[156:157], v[156:157], s[30:31] op_sel_hi:[1,0]
	v_pk_mul_f32 v[158:159], v[158:159], s[30:31] op_sel_hi:[1,0]
	v_pk_mul_f32 v[160:161], v[160:161], s[30:31] op_sel_hi:[1,0]
	v_pk_mul_f32 v[162:163], v[162:163], s[30:31] op_sel_hi:[1,0]
	v_pk_mul_f32 v[164:165], v[164:165], s[30:31] op_sel_hi:[1,0]
	v_pk_mul_f32 v[166:167], v[166:167], s[30:31] op_sel_hi:[1,0]
	v_pk_mul_f32 v[168:169], v[168:169], s[30:31] op_sel_hi:[1,0]
	v_pk_mul_f32 v[170:171], v[170:171], s[30:31] op_sel_hi:[1,0]
	v_pk_mul_f32 v[172:173], v[172:173], s[30:31] op_sel_hi:[1,0]
	v_pk_mul_f32 v[174:175], v[174:175], s[30:31] op_sel_hi:[1,0]
	v_pk_mul_f32 v[176:177], v[176:177], s[30:31] op_sel_hi:[1,0]
	v_pk_mul_f32 v[178:179], v[178:179], s[30:31] op_sel_hi:[1,0]
	v_pk_mul_f32 v[180:181], v[180:181], s[30:31] op_sel_hi:[1,0]
	v_pk_mul_f32 v[182:183], v[182:183], s[30:31] op_sel_hi:[1,0]
	v_pk_mul_f32 v[184:185], v[184:185], s[30:31] op_sel_hi:[1,0]
	v_pk_mul_f32 v[186:187], v[186:187], s[30:31] op_sel_hi:[1,0]
	v_pk_mul_f32 v[188:189], v[188:189], s[30:31] op_sel_hi:[1,0]
	v_pk_mul_f32 v[190:191], v[190:191], s[30:31] op_sel_hi:[1,0]
	v_pk_mul_f32 v[192:193], v[192:193], s[30:31] op_sel_hi:[1,0]
	v_med3_f32 v130, v130, s24, v237
	v_med3_f32 v131, v131, s24, v237
	v_med3_f32 v132, v132, s24, v237
	v_med3_f32 v133, v133, s24, v237
	v_med3_f32 v134, v134, s24, v237
	v_med3_f32 v135, v135, s24, v237
	v_med3_f32 v136, v136, s24, v237
	v_med3_f32 v137, v137, s24, v237
	v_med3_f32 v138, v138, s24, v237
	v_med3_f32 v139, v139, s24, v237
	v_med3_f32 v140, v140, s24, v237
	v_med3_f32 v141, v141, s24, v237
	v_med3_f32 v142, v142, s24, v237
	v_med3_f32 v143, v143, s24, v237
	v_med3_f32 v144, v144, s24, v237
	v_med3_f32 v145, v145, s24, v237
	v_med3_f32 v146, v146, s24, v237
	v_med3_f32 v147, v147, s24, v237
	v_med3_f32 v148, v148, s24, v237
	v_med3_f32 v149, v149, s24, v237
	v_med3_f32 v150, v150, s24, v237
	v_med3_f32 v151, v151, s24, v237
	v_med3_f32 v152, v152, s24, v237
	v_med3_f32 v153, v153, s24, v237
	v_med3_f32 v154, v154, s24, v237
	v_med3_f32 v155, v155, s24, v237
	v_med3_f32 v156, v156, s24, v237
	v_med3_f32 v157, v157, s24, v237
	v_med3_f32 v158, v158, s24, v237
	v_med3_f32 v159, v159, s24, v237
	v_med3_f32 v160, v160, s24, v237
	v_med3_f32 v161, v161, s24, v237
	v_med3_f32 v162, v162, s24, v237
	v_med3_f32 v163, v163, s24, v237
	v_med3_f32 v164, v164, s24, v237
	v_med3_f32 v165, v165, s24, v237
	v_med3_f32 v166, v166, s24, v237
	v_med3_f32 v167, v167, s24, v237
	v_med3_f32 v168, v168, s24, v237
	v_med3_f32 v169, v169, s24, v237
	v_med3_f32 v170, v170, s24, v237
	v_med3_f32 v171, v171, s24, v237
	v_med3_f32 v172, v172, s24, v237
	v_med3_f32 v173, v173, s24, v237
	v_med3_f32 v174, v174, s24, v237
	v_med3_f32 v175, v175, s24, v237
	v_med3_f32 v176, v176, s24, v237
	v_med3_f32 v177, v177, s24, v237
	v_med3_f32 v178, v178, s24, v237
	v_med3_f32 v179, v179, s24, v237
	v_med3_f32 v180, v180, s24, v237
	v_med3_f32 v181, v181, s24, v237
	v_med3_f32 v182, v182, s24, v237
	v_med3_f32 v183, v183, s24, v237
	v_med3_f32 v184, v184, s24, v237
	v_med3_f32 v185, v185, s24, v237
	v_med3_f32 v186, v186, s24, v237
	v_med3_f32 v187, v187, s24, v237
	v_med3_f32 v188, v188, s24, v237
	v_med3_f32 v189, v189, s24, v237
	v_med3_f32 v190, v190, s24, v237
	v_med3_f32 v191, v191, s24, v237
	v_med3_f32 v192, v192, s24, v237
	v_med3_f32 v193, v193, s24, v237
	v_cvt_pk_fp8_f32 v130, v130, v134
	v_cvt_pk_fp8_f32 v130, v138, v142 op_sel:[0,0,1]
	v_cvt_pk_fp8_f32 v134, v131, v135
	v_cvt_pk_fp8_f32 v134, v139, v143 op_sel:[0,0,1]
	v_cvt_pk_fp8_f32 v138, v132, v136
	v_cvt_pk_fp8_f32 v138, v140, v144 op_sel:[0,0,1]
	v_cvt_pk_fp8_f32 v142, v133, v137
	v_cvt_pk_fp8_f32 v142, v141, v145 op_sel:[0,0,1]
	v_cvt_pk_fp8_f32 v131, v146, v150
	v_cvt_pk_fp8_f32 v131, v154, v158 op_sel:[0,0,1]
	v_cvt_pk_fp8_f32 v135, v147, v151
	v_cvt_pk_fp8_f32 v135, v155, v159 op_sel:[0,0,1]
	v_cvt_pk_fp8_f32 v139, v148, v152
	v_cvt_pk_fp8_f32 v139, v156, v160 op_sel:[0,0,1]
	v_cvt_pk_fp8_f32 v143, v149, v153
	v_cvt_pk_fp8_f32 v143, v157, v161 op_sel:[0,0,1]
	v_cvt_pk_fp8_f32 v132, v162, v166
	v_cvt_pk_fp8_f32 v132, v170, v174 op_sel:[0,0,1]
	v_cvt_pk_fp8_f32 v136, v163, v167
	v_cvt_pk_fp8_f32 v136, v171, v175 op_sel:[0,0,1]
	v_cvt_pk_fp8_f32 v140, v164, v168
	v_cvt_pk_fp8_f32 v140, v172, v176 op_sel:[0,0,1]
	v_cvt_pk_fp8_f32 v144, v165, v169
	v_cvt_pk_fp8_f32 v144, v173, v177 op_sel:[0,0,1]
	v_cvt_pk_fp8_f32 v133, v178, v182
	v_cvt_pk_fp8_f32 v133, v186, v190 op_sel:[0,0,1]
	v_cvt_pk_fp8_f32 v137, v179, v183
	v_cvt_pk_fp8_f32 v137, v187, v191 op_sel:[0,0,1]
	v_cvt_pk_fp8_f32 v141, v180, v184
	v_cvt_pk_fp8_f32 v141, v188, v192 op_sel:[0,0,1]
	v_cvt_pk_fp8_f32 v145, v181, v185
	v_cvt_pk_fp8_f32 v145, v189, v193 op_sel:[0,0,1]
	global_store_dwordx4 v250, v[130:133], s[42:43] nt
	global_store_dwordx4 v250, v[134:137], s[42:43] offset:2048 nt
	global_store_dwordx4 v251, v[138:141], s[42:43] nt
	global_store_dwordx4 v251, v[142:145], s[42:43] offset:2048 nt
	s_add_u32 s42, s42, 0x10000
	s_addc_u32 s43, s43, 0
	global_load_dwordx4 v[130:133], v246, s[4:5] offset:640 nt
	global_load_dwordx4 v[134:137], v247, s[4:5] offset:640 nt
	global_load_dwordx4 v[138:141], v248, s[4:5] offset:640 nt
	global_load_dwordx4 v[142:145], v249, s[4:5] offset:640 nt
	global_load_dwordx4 v[146:149], v246, s[6:7] offset:640 nt
	global_load_dwordx4 v[150:153], v247, s[6:7] offset:640 nt
	global_load_dwordx4 v[154:157], v248, s[6:7] offset:640 nt
	global_load_dwordx4 v[158:161], v249, s[6:7] offset:640 nt
	global_load_dwordx4 v[162:165], v246, s[8:9] offset:640 nt
	global_load_dwordx4 v[166:169], v247, s[8:9] offset:640 nt
	global_load_dwordx4 v[170:173], v248, s[8:9] offset:640 nt
	global_load_dwordx4 v[174:177], v249, s[8:9] offset:640 nt
	global_load_dwordx4 v[178:181], v246, s[38:39] offset:640 nt
	global_load_dwordx4 v[182:185], v247, s[38:39] offset:640 nt
	global_load_dwordx4 v[186:189], v248, s[38:39] offset:640 nt
	global_load_dwordx4 v[190:193], v249, s[38:39] offset:640 nt
	s_waitcnt vmcnt(40)
; #define GAS __attribute__((address_space(1)))
; template <bool GAIN, bool NT = false> __device__ __forceinline__ void titem8_load(const TItem& d, int lane, f32x4 (&r)[16], f32x4 (&g)[4]) {
;     const int q = lane & 7, kg = lane >> 3; const unsigned lo = (unsigned)((16 * kg) * d.N + 4 * q) * 4u;
;     const GAS char* base = (const GAS char*)d.src;
; #pragma unroll
;     for (int j = 0; j < 16; ++j) { const GAS f32x4* p = (const GAS f32x4*)(base + (size_t)j * (size_t)d.N * 4 + lo); r[j] = NT ? __builtin_nontemporal_load(p) : *p; }
;     if constexpr (GAIN) { const GAS char* gb = (const GAS char*)d.gain; const unsigned go = (unsigned)(16 * kg) * 4u;
; #pragma unroll
;         for (int j4 = 0; j4 < 4; ++j4) g[j4] = *(const GAS f32x4*)(gb + 16 * j4 + go); }
;     asm volatile("" ::: "memory"); __builtin_amdgcn_sched_barrier(0);
; template <bool GAIN, bool NT = false> __device__ __forceinline__ void titem8_store(const TItem& d, int lane, const f32x4 (&r)[16], const f32x4 (&g)[4]) {
;     const int q = lane & 7, kg = lane >> 3; const unsigned lo = (unsigned)((4 * q) * d.ldk + 16 * kg);
;     GAS char* base = (GAS char*)d.dst;
;     f32x4 s[16];
; #pragma unroll
;     for (int j = 0; j < 16; ++j) s[j] = r[j] * ((GAIN ? g[j >> 2][j & 3] : 1.0f) * W8_SCALE);
; #pragma unroll
;     for (int i = 0; i < 4; ++i) { v4u w;
;         w.x = pk4_fp8w(s[0][i], s[1][i], s[2][i], s[3][i]); w.y = pk4_fp8w(s[4][i], s[5][i], s[6][i], s[7][i]);
;         w.z = pk4_fp8w(s[8][i], s[9][i], s[10][i], s[11][i]); w.w = pk4_fp8w(s[12][i], s[13][i], s[14][i], s[15][i]);
;         GAS v4u* p = (GAS v4u*)(base + (size_t)i * (size_t)d.ldk + lo);
;         if (NT) __builtin_nontemporal_store(w, p); else *p = w; }
; }
	v_pk_mul_f32 v[0:1], v[0:1], s[30:31] op_sel_hi:[1,0]
	v_pk_mul_f32 v[2:3], v[2:3], s[30:31] op_sel_hi:[1,0]
	v_pk_mul_f32 v[4:5], v[4:5], s[30:31] op_sel_hi:[1,0]
	v_pk_mul_f32 v[6:7], v[6:7], s[30:31] op_sel_hi:[1,0]
	v_pk_mul_f32 v[8:9], v[8:9], s[30:31] op_sel_hi:[1,0]
	v_pk_mul_f32 v[10:11], v[10:11], s[30:31] op_sel_hi:[1,0]
	v_pk_mul_f32 v[12:13], v[12:13], s[30:31] op_sel_hi:[1,0]
	v_pk_mul_f32 v[14:15], v[14:15], s[30:31] op_sel_hi:[1,0]
	v_pk_mul_f32 v[16:17], v[16:17], s[30:31] op_sel_hi:[1,0]
	v_pk_mul_f32 v[18:19], v[18:19], s[30:31] op_sel_hi:[1,0]
	v_pk_mul_f32 v[20:21], v[20:21], s[30:31] op_sel_hi:[1,0]
	v_pk_mul_f32 v[22:23], v[22:23], s[30:31] op_sel_hi:[1,0]
	v_pk_mul_f32 v[24:25], v[24:25], s[30:31] op_sel_hi:[1,0]
	v_pk_mul_f32 v[26:27], v[26:27], s[30:31] op_sel_hi:[1,0]
	v_pk_mul_f32 v[28:29], v[28:29], s[30:31] op_sel_hi:[1,0]
	v_pk_mul_f32 v[30:31], v[30:31], s[30:31] op_sel_hi:[1,0]
	v_pk_mul_f32 v[32:33], v[32:33], s[30:31] op_sel_hi:[1,0]
	v_pk_mul_f32 v[34:35], v[34:35], s[30:31] op_sel_hi:[1,0]
	v_pk_mul_f32 v[36:37], v[36:37], s[30:31] op_sel_hi:[1,0]
	v_pk_mul_f32 v[38:39], v[38:39], s[30:31] op_sel_hi:[1,0]
	v_pk_mul_f32 v[40:41], v[40:41], s[30:31] op_sel_hi:[1,0]
	v_pk_mul_f32 v[42:43], v[42:43], s[30:31] op_sel_hi:[1,0]
	v_pk_mul_f32 v[44:45], v[44:45], s[30:31] op_sel_hi:[1,0]
	v_pk_mul_f32 v[46:47], v[46:47], s[30:31] op_sel_hi:[1,0]
	v_pk_mul_f32 v[48:49], v[48:49], s[30:31] op_sel_hi:[1,0]
	v_pk_mul_f32 v[50:51], v[50:51], s[30:31] op_sel_hi:[1,0]
	v_pk_mul_f32 v[52:53], v[52:53], s[30:31] op_sel_hi:[1,0]
	v_pk_mul_f32 v[54:55], v[54:55], s[30:31] op_sel_hi:[1,0]
	v_pk_mul_f32 v[56:57], v[56:57], s[30:31] op_sel_hi:[1,0]
	v_pk_mul_f32 v[58:59], v[58:59], s[30:31] op_sel_hi:[1,0]
	v_pk_mul_f32 v[60:61], v[60:61], s[30:31] op_sel_hi:[1,0]
	v_pk_mul_f32 v[62:63], v[62:63], s[30:31] op_sel_hi:[1,0]
	v_med3_f32 v0, v0, s24, v237
	v_med3_f32 v1, v1, s24, v237
	v_med3_f32 v2, v2, s24, v237
	v_med3_f32 v3, v3, s24, v237
	v_med3_f32 v4, v4, s24, v237
	v_med3_f32 v5, v5, s24, v237
	v_med3_f32 v6, v6, s24, v237
	v_med3_f32 v7, v7, s24, v237
	v_med3_f32 v8, v8, s24, v237
	v_med3_f32 v9, v9, s24, v237
	v_med3_f32 v10, v10, s24, v237
	v_med3_f32 v11, v11, s24, v237
	v_med3_f32 v12, v12, s24, v237
	v_med3_f32 v13, v13, s24, v237
	v_med3_f32 v14, v14, s24, v237
	v_med3_f32 v15, v15, s24, v237
	v_med3_f32 v16, v16, s24, v237
	v_med3_f32 v17, v17, s24, v237
	v_med3_f32 v18, v18, s24, v237
	v_med3_f32 v19, v19, s24, v237
	v_med3_f32 v20, v20, s24, v237
	v_med3_f32 v21, v21, s24, v237
	v_med3_f32 v22, v22, s24, v237
	v_med3_f32 v23, v23, s24, v237
	v_med3_f32 v24, v24, s24, v237
	v_med3_f32 v25, v25, s24, v237
	v_med3_f32 v26, v26, s24, v237
	v_med3_f32 v27, v27, s24, v237
	v_med3_f32 v28, v28, s24, v237
	v_med3_f32 v29, v29, s24, v237
	v_med3_f32 v30, v30, s24, v237
	v_med3_f32 v31, v31, s24, v237
	v_med3_f32 v32, v32, s24, v237
	v_med3_f32 v33, v33, s24, v237
	v_med3_f32 v34, v34, s24, v237
	v_med3_f32 v35, v35, s24, v237
	v_med3_f32 v36, v36, s24, v237
	v_med3_f32 v37, v37, s24, v237
	v_med3_f32 v38, v38, s24, v237
	v_med3_f32 v39, v39, s24, v237
	v_med3_f32 v40, v40, s24, v237
	v_med3_f32 v41, v41, s24, v237
	v_med3_f32 v42, v42, s24, v237
	v_med3_f32 v43, v43, s24, v237
	v_med3_f32 v44, v44, s24, v237
	v_med3_f32 v45, v45, s24, v237
	v_med3_f32 v46, v46, s24, v237
	v_med3_f32 v47, v47, s24, v237
	v_med3_f32 v48, v48, s24, v237
	v_med3_f32 v49, v49, s24, v237
	v_med3_f32 v50, v50, s24, v237
	v_med3_f32 v51, v51, s24, v237
	v_med3_f32 v52, v52, s24, v237
	v_med3_f32 v53, v53, s24, v237
	v_med3_f32 v54, v54, s24, v237
	v_med3_f32 v55, v55, s24, v237
	v_med3_f32 v56, v56, s24, v237
	v_med3_f32 v57, v57, s24, v237
	v_med3_f32 v58, v58, s24, v237
	v_med3_f32 v59, v59, s24, v237
	v_med3_f32 v60, v60, s24, v237
	v_med3_f32 v61, v61, s24, v237
	v_med3_f32 v62, v62, s24, v237
	v_med3_f32 v63, v63, s24, v237
	v_cvt_pk_fp8_f32 v0, v0, v4
	v_cvt_pk_fp8_f32 v0, v8, v12 op_sel:[0,0,1]
	v_cvt_pk_fp8_f32 v4, v1, v5
	v_cvt_pk_fp8_f32 v4, v9, v13 op_sel:[0,0,1]
	v_cvt_pk_fp8_f32 v8, v2, v6
	v_cvt_pk_fp8_f32 v8, v10, v14 op_sel:[0,0,1]
	v_cvt_pk_fp8_f32 v12, v3, v7
	v_cvt_pk_fp8_f32 v12, v11, v15 op_sel:[0,0,1]
	v_cvt_pk_fp8_f32 v1, v16, v20
	v_cvt_pk_fp8_f32 v1, v24, v28 op_sel:[0,0,1]
	v_cvt_pk_fp8_f32 v5, v17, v21
	v_cvt_pk_fp8_f32 v5, v25, v29 op_sel:[0,0,1]
	v_cvt_pk_fp8_f32 v9, v18, v22
	v_cvt_pk_fp8_f32 v9, v26, v30 op_sel:[0,0,1]
	v_cvt_pk_fp8_f32 v13, v19, v23
	v_cvt_pk_fp8_f32 v13, v27, v31 op_sel:[0,0,1]
	v_cvt_pk_fp8_f32 v2, v32, v36
	v_cvt_pk_fp8_f32 v2, v40, v44 op_sel:[0,0,1]
	v_cvt_pk_fp8_f32 v6, v33, v37
	v_cvt_pk_fp8_f32 v6, v41, v45 op_sel:[0,0,1]
	v_cvt_pk_fp8_f32 v10, v34, v38
	v_cvt_pk_fp8_f32 v10, v42, v46 op_sel:[0,0,1]
	v_cvt_pk_fp8_f32 v14, v35, v39
	v_cvt_pk_fp8_f32 v14, v43, v47 op_sel:[0,0,1]
	v_cvt_pk_fp8_f32 v3, v48, v52
	v_cvt_pk_fp8_f32 v3, v56, v60 op_sel:[0,0,1]
	v_cvt_pk_fp8_f32 v7, v49, v53
	v_cvt_pk_fp8_f32 v7, v57, v61 op_sel:[0,0,1]
	v_cvt_pk_fp8_f32 v11, v50, v54
	v_cvt_pk_fp8_f32 v11, v58, v62 op_sel:[0,0,1]
	v_cvt_pk_fp8_f32 v15, v51, v55
	v_cvt_pk_fp8_f32 v15, v59, v63 op_sel:[0,0,1]
	global_store_dwordx4 v250, v[0:3], s[42:43] nt
	global_store_dwordx4 v250, v[4:7], s[42:43] offset:2048 nt
	global_store_dwordx4 v251, v[8:11], s[42:43] nt
	global_store_dwordx4 v251, v[12:15], s[42:43] offset:2048 nt
	s_add_u32 s42, s42, 0x10000
	s_addc_u32 s43, s43, 0
	global_load_dwordx4 v[0:3], v246, s[4:5] offset:768 nt
	global_load_dwordx4 v[4:7], v247, s[4:5] offset:768 nt
	global_load_dwordx4 v[8:11], v248, s[4:5] offset:768 nt
	global_load_dwordx4 v[12:15], v249, s[4:5] offset:768 nt
	global_load_dwordx4 v[16:19], v246, s[6:7] offset:768 nt
	global_load_dwordx4 v[20:23], v247, s[6:7] offset:768 nt
	global_load_dwordx4 v[24:27], v248, s[6:7] offset:768 nt
	global_load_dwordx4 v[28:31], v249, s[6:7] offset:768 nt
	global_load_dwordx4 v[32:35], v246, s[8:9] offset:768 nt
	global_load_dwordx4 v[36:39], v247, s[8:9] offset:768 nt
	global_load_dwordx4 v[40:43], v248, s[8:9] offset:768 nt
	global_load_dwordx4 v[44:47], v249, s[8:9] offset:768 nt
	global_load_dwordx4 v[48:51], v246, s[38:39] offset:768 nt
	global_load_dwordx4 v[52:55], v247, s[38:39] offset:768 nt
	global_load_dwordx4 v[56:59], v248, s[38:39] offset:768 nt
	global_load_dwordx4 v[60:63], v249, s[38:39] offset:768 nt
	s_waitcnt vmcnt(40)
; #define GAS __attribute__((address_space(1)))
; template <bool GAIN, bool NT = false> __device__ __forceinline__ void titem8_load(const TItem& d, int lane, f32x4 (&r)[16], f32x4 (&g)[4]) {
;     const int q = lane & 7, kg = lane >> 3; const unsigned lo = (unsigned)((16 * kg) * d.N + 4 * q) * 4u;
;     const GAS char* base = (const GAS char*)d.src;
; #pragma unroll
;     for (int j = 0; j < 16; ++j) { const GAS f32x4* p = (const GAS f32x4*)(base + (size_t)j * (size_t)d.N * 4 + lo); r[j] = NT ? __builtin_nontemporal_load(p) : *p; }
;     if constexpr (GAIN) { const GAS char* gb = (const GAS char*)d.gain; const unsigned go = (unsigned)(16 * kg) * 4u;
; #pragma unroll
;         for (int j4 = 0; j4 < 4; ++j4) g[j4] = *(const GAS f32x4*)(gb + 16 * j4 + go); }
;     asm volatile("" ::: "memory"); __builtin_amdgcn_sched_barrier(0);
; template <bool GAIN, bool NT = false> __device__ __forceinline__ void titem8_store(const TItem& d, int lane, const f32x4 (&r)[16], const f32x4 (&g)[4]) {
;     const int q = lane & 7, kg = lane >> 3; const unsigned lo = (unsigned)((4 * q) * d.ldk + 16 * kg);
;     GAS char* base = (GAS char*)d.dst;
;     f32x4 s[16];
; #pragma unroll
;     for (int j = 0; j < 16; ++j) s[j] = r[j] * ((GAIN ? g[j >> 2][j & 3] : 1.0f) * W8_SCALE);
; #pragma unroll
;     for (int i = 0; i < 4; ++i) { v4u w;
;         w.x = pk4_fp8w(s[0][i], s[1][i], s[2][i], s[3][i]); w.y = pk4_fp8w(s[4][i], s[5][i], s[6][i], s[7][i]);
;         w.z = pk4_fp8w(s[8][i], s[9][i], s[10][i], s[11][i]); w.w = pk4_fp8w(s[12][i], s[13][i], s[14][i], s[15][i]);
;         GAS v4u* p = (GAS v4u*)(base + (size_t)i * (size_t)d.ldk + lo);
;         if (NT) __builtin_nontemporal_store(w, p); else *p = w; }
; }
	v_pk_mul_f32 v[66:67], v[66:67], s[30:31] op_sel_hi:[1,0]
	v_pk_mul_f32 v[68:69], v[68:69], s[30:31] op_sel_hi:[1,0]
	v_pk_mul_f32 v[70:71], v[70:71], s[30:31] op_sel_hi:[1,0]
	v_pk_mul_f32 v[72:73], v[72:73], s[30:31] op_sel_hi:[1,0]
	v_pk_mul_f32 v[74:75], v[74:75], s[30:31] op_sel_hi:[1,0]
	v_pk_mul_f32 v[76:77], v[76:77], s[30:31] op_sel_hi:[1,0]
	v_pk_mul_f32 v[78:79], v[78:79], s[30:31] op_sel_hi:[1,0]
	v_pk_mul_f32 v[80:81], v[80:81], s[30:31] op_sel_hi:[1,0]
	v_pk_mul_f32 v[82:83], v[82:83], s[30:31] op_sel_hi:[1,0]
	v_pk_mul_f32 v[84:85], v[84:85], s[30:31] op_sel_hi:[1,0]
	v_pk_mul_f32 v[86:87], v[86:87], s[30:31] op_sel_hi:[1,0]
	v_pk_mul_f32 v[88:89], v[88:89], s[30:31] op_sel_hi:[1,0]
	v_pk_mul_f32 v[90:91], v[90:91], s[30:31] op_sel_hi:[1,0]
	v_pk_mul_f32 v[92:93], v[92:93], s[30:31] op_sel_hi:[1,0]
	v_pk_mul_f32 v[94:95], v[94:95], s[30:31] op_sel_hi:[1,0]
	v_pk_mul_f32 v[96:97], v[96:97], s[30:31] op_sel_hi:[1,0]
	v_pk_mul_f32 v[98:99], v[98:99], s[30:31] op_sel_hi:[1,0]
	v_pk_mul_f32 v[100:101], v[100:101], s[30:31] op_sel_hi:[1,0]
	v_pk_mul_f32 v[102:103], v[102:103], s[30:31] op_sel_hi:[1,0]
	v_pk_mul_f32 v[104:105], v[104:105], s[30:31] op_sel_hi:[1,0]
	v_pk_mul_f32 v[106:107], v[106:107], s[30:31] op_sel_hi:[1,0]
	v_pk_mul_f32 v[108:109], v[108:109], s[30:31] op_sel_hi:[1,0]
	v_pk_mul_f32 v[110:111], v[110:111], s[30:31] op_sel_hi:[1,0]
	v_pk_mul_f32 v[112:113], v[112:113], s[30:31] op_sel_hi:[1,0]
	v_pk_mul_f32 v[114:115], v[114:115], s[30:31] op_sel_hi:[1,0]
	v_pk_mul_f32 v[116:117], v[116:117], s[30:31] op_sel_hi:[1,0]
	v_pk_mul_f32 v[118:119], v[118:119], s[30:31] op_sel_hi:[1,0]
	v_pk_mul_f32 v[120:121], v[120:121], s[30:31] op_sel_hi:[1,0]
	v_pk_mul_f32 v[122:123], v[122:123], s[30:31] op_sel_hi:[1,0]
	v_pk_mul_f32 v[124:125], v[124:125], s[30:31] op_sel_hi:[1,0]
	v_pk_mul_f32 v[126:127], v[126:127], s[30:31] op_sel_hi:[1,0]
	v_pk_mul_f32 v[128:129], v[128:129], s[30:31] op_sel_hi:[1,0]
	v_med3_f32 v66, v66, s24, v237
	v_med3_f32 v67, v67, s24, v237
	v_med3_f32 v68, v68, s24, v237
	v_med3_f32 v69, v69, s24, v237
	v_med3_f32 v70, v70, s24, v237
	v_med3_f32 v71, v71, s24, v237
	v_med3_f32 v72, v72, s24, v237
	v_med3_f32 v73, v73, s24, v237
	v_med3_f32 v74, v74, s24, v237
	v_med3_f32 v75, v75, s24, v237
	v_med3_f32 v76, v76, s24, v237
	v_med3_f32 v77, v77, s24, v237
	v_med3_f32 v78, v78, s24, v237
	v_med3_f32 v79, v79, s24, v237
	v_med3_f32 v80, v80, s24, v237
	v_med3_f32 v81, v81, s24, v237
	v_med3_f32 v82, v82, s24, v237
	v_med3_f32 v83, v83, s24, v237
	v_med3_f32 v84, v84, s24, v237
	v_med3_f32 v85, v85, s24, v237
	v_med3_f32 v86, v86, s24, v237
	v_med3_f32 v87, v87, s24, v237
	v_med3_f32 v88, v88, s24, v237
	v_med3_f32 v89, v89, s24, v237
	v_med3_f32 v90, v90, s24, v237
	v_med3_f32 v91, v91, s24, v237
	v_med3_f32 v92, v92, s24, v237
	v_med3_f32 v93, v93, s24, v237
	v_med3_f32 v94, v94, s24, v237
	v_med3_f32 v95, v95, s24, v237
	v_med3_f32 v96, v96, s24, v237
	v_med3_f32 v97, v97, s24, v237
	v_med3_f32 v98, v98, s24, v237
	v_med3_f32 v99, v99, s24, v237
	v_med3_f32 v100, v100, s24, v237
	v_med3_f32 v101, v101, s24, v237
	v_med3_f32 v102, v102, s24, v237
	v_med3_f32 v103, v103, s24, v237
	v_med3_f32 v104, v104, s24, v237
	v_med3_f32 v105, v105, s24, v237
	v_med3_f32 v106, v106, s24, v237
	v_med3_f32 v107, v107, s24, v237
	v_med3_f32 v108, v108, s24, v237
	v_med3_f32 v109, v109, s24, v237
	v_med3_f32 v110, v110, s24, v237
	v_med3_f32 v111, v111, s24, v237
	v_med3_f32 v112, v112, s24, v237
	v_med3_f32 v113, v113, s24, v237
	v_med3_f32 v114, v114, s24, v237
	v_med3_f32 v115, v115, s24, v237
	v_med3_f32 v116, v116, s24, v237
	v_med3_f32 v117, v117, s24, v237
	v_med3_f32 v118, v118, s24, v237
	v_med3_f32 v119, v119, s24, v237
	v_med3_f32 v120, v120, s24, v237
	v_med3_f32 v121, v121, s24, v237
	v_med3_f32 v122, v122, s24, v237
	v_med3_f32 v123, v123, s24, v237
	v_med3_f32 v124, v124, s24, v237
	v_med3_f32 v125, v125, s24, v237
	v_med3_f32 v126, v126, s24, v237
	v_med3_f32 v127, v127, s24, v237
	v_med3_f32 v128, v128, s24, v237
	v_med3_f32 v129, v129, s24, v237
	v_cvt_pk_fp8_f32 v66, v66, v70
	v_cvt_pk_fp8_f32 v66, v74, v78 op_sel:[0,0,1]
	v_cvt_pk_fp8_f32 v70, v67, v71
	v_cvt_pk_fp8_f32 v70, v75, v79 op_sel:[0,0,1]
	v_cvt_pk_fp8_f32 v74, v68, v72
	v_cvt_pk_fp8_f32 v74, v76, v80 op_sel:[0,0,1]
	v_cvt_pk_fp8_f32 v78, v69, v73
	v_cvt_pk_fp8_f32 v78, v77, v81 op_sel:[0,0,1]
	v_cvt_pk_fp8_f32 v67, v82, v86
	v_cvt_pk_fp8_f32 v67, v90, v94 op_sel:[0,0,1]
	v_cvt_pk_fp8_f32 v71, v83, v87
	v_cvt_pk_fp8_f32 v71, v91, v95 op_sel:[0,0,1]
	v_cvt_pk_fp8_f32 v75, v84, v88
	v_cvt_pk_fp8_f32 v75, v92, v96 op_sel:[0,0,1]
	v_cvt_pk_fp8_f32 v79, v85, v89
	v_cvt_pk_fp8_f32 v79, v93, v97 op_sel:[0,0,1]
	v_cvt_pk_fp8_f32 v68, v98, v102
	v_cvt_pk_fp8_f32 v68, v106, v110 op_sel:[0,0,1]
	v_cvt_pk_fp8_f32 v72, v99, v103
	v_cvt_pk_fp8_f32 v72, v107, v111 op_sel:[0,0,1]
	v_cvt_pk_fp8_f32 v76, v100, v104
	v_cvt_pk_fp8_f32 v76, v108, v112 op_sel:[0,0,1]
	v_cvt_pk_fp8_f32 v80, v101, v105
	v_cvt_pk_fp8_f32 v80, v109, v113 op_sel:[0,0,1]
	v_cvt_pk_fp8_f32 v69, v114, v118
	v_cvt_pk_fp8_f32 v69, v122, v126 op_sel:[0,0,1]
	v_cvt_pk_fp8_f32 v73, v115, v119
	v_cvt_pk_fp8_f32 v73, v123, v127 op_sel:[0,0,1]
	v_cvt_pk_fp8_f32 v77, v116, v120
	v_cvt_pk_fp8_f32 v77, v124, v128 op_sel:[0,0,1]
	v_cvt_pk_fp8_f32 v81, v117, v121
	v_cvt_pk_fp8_f32 v81, v125, v129 op_sel:[0,0,1]
	global_store_dwordx4 v250, v[66:69], s[42:43] nt
	global_store_dwordx4 v250, v[70:73], s[42:43] offset:2048 nt
	global_store_dwordx4 v251, v[74:77], s[42:43] nt
	global_store_dwordx4 v251, v[78:81], s[42:43] offset:2048 nt
	s_add_u32 s42, s42, 0x10000
	s_addc_u32 s43, s43, 0
	global_load_dwordx4 v[66:69], v246, s[4:5] offset:896 nt
	global_load_dwordx4 v[70:73], v247, s[4:5] offset:896 nt
	global_load_dwordx4 v[74:77], v248, s[4:5] offset:896 nt
	global_load_dwordx4 v[78:81], v249, s[4:5] offset:896 nt
	global_load_dwordx4 v[82:85], v246, s[6:7] offset:896 nt
	global_load_dwordx4 v[86:89], v247, s[6:7] offset:896 nt
	global_load_dwordx4 v[90:93], v248, s[6:7] offset:896 nt
	global_load_dwordx4 v[94:97], v249, s[6:7] offset:896 nt
	global_load_dwordx4 v[98:101], v246, s[8:9] offset:896 nt
	global_load_dwordx4 v[102:105], v247, s[8:9] offset:896 nt
	global_load_dwordx4 v[106:109], v248, s[8:9] offset:896 nt
	global_load_dwordx4 v[110:113], v249, s[8:9] offset:896 nt
	global_load_dwordx4 v[114:117], v246, s[38:39] offset:896 nt
	global_load_dwordx4 v[118:121], v247, s[38:39] offset:896 nt
	global_load_dwordx4 v[122:125], v248, s[38:39] offset:896 nt
	global_load_dwordx4 v[126:129], v249, s[38:39] offset:896 nt
	s_waitcnt vmcnt(40)
; #define GAS __attribute__((address_space(1)))
; template <bool GAIN, bool NT = false> __device__ __forceinline__ void titem8_load(const TItem& d, int lane, f32x4 (&r)[16], f32x4 (&g)[4]) {
;     const int q = lane & 7, kg = lane >> 3; const unsigned lo = (unsigned)((16 * kg) * d.N + 4 * q) * 4u;
;     const GAS char* base = (const GAS char*)d.src;
; #pragma unroll
;     for (int j = 0; j < 16; ++j) { const GAS f32x4* p = (const GAS f32x4*)(base + (size_t)j * (size_t)d.N * 4 + lo); r[j] = NT ? __builtin_nontemporal_load(p) : *p; }
;     if constexpr (GAIN) { const GAS char* gb = (const GAS char*)d.gain; const unsigned go = (unsigned)(16 * kg) * 4u;
; #pragma unroll
;         for (int j4 = 0; j4 < 4; ++j4) g[j4] = *(const GAS f32x4*)(gb + 16 * j4 + go); }
;     asm volatile("" ::: "memory"); __builtin_amdgcn_sched_barrier(0);
; template <bool GAIN, bool NT = false> __device__ __forceinline__ void titem8_store(const TItem& d, int lane, const f32x4 (&r)[16], const f32x4 (&g)[4]) {
;     const int q = lane & 7, kg = lane >> 3; const unsigned lo = (unsigned)((4 * q) * d.ldk + 16 * kg);
;     GAS char* base = (GAS char*)d.dst;
;     f32x4 s[16];
; #pragma unroll
;     for (int j = 0; j < 16; ++j) s[j] = r[j] * ((GAIN ? g[j >> 2][j & 3] : 1.0f) * W8_SCALE);
; #pragma unroll
;     for (int i = 0; i < 4; ++i) { v4u w;
;         w.x = pk4_fp8w(s[0][i], s[1][i], s[2][i], s[3][i]); w.y = pk4_fp8w(s[4][i], s[5][i], s[6][i], s[7][i]);
;         w.z = pk4_fp8w(s[8][i], s[9][i], s[10][i], s[11][i]); w.w = pk4_fp8w(s[12][i], s[13][i], s[14][i], s[15][i]);
;         GAS v4u* p = (GAS v4u*)(base + (size_t)i * (size_t)d.ldk + lo);
;         if (NT) __builtin_nontemporal_store(w, p); else *p = w; }
; }
	v_pk_mul_f32 v[130:131], v[130:131], s[30:31] op_sel_hi:[1,0]
	v_pk_mul_f32 v[132:133], v[132:133], s[30:31] op_sel_hi:[1,0]
	v_pk_mul_f32 v[134:135], v[134:135], s[30:31] op_sel_hi:[1,0]
	v_pk_mul_f32 v[136:137], v[136:137], s[30:31] op_sel_hi:[1,0]
	v_pk_mul_f32 v[138:139], v[138:139], s[30:31] op_sel_hi:[1,0]
	v_pk_mul_f32 v[140:141], v[140:141], s[30:31] op_sel_hi:[1,0]
	v_pk_mul_f32 v[142:143], v[142:143], s[30:31] op_sel_hi:[1,0]
	v_pk_mul_f32 v[144:145], v[144:145], s[30:31] op_sel_hi:[1,0]
	v_pk_mul_f32 v[146:147], v[146:147], s[30:31] op_sel_hi:[1,0]
	v_pk_mul_f32 v[148:149], v[148:149], s[30:31] op_sel_hi:[1,0]
	v_pk_mul_f32 v[150:151], v[150:151], s[30:31] op_sel_hi:[1,0]
	v_pk_mul_f32 v[152:153], v[152:153], s[30:31] op_sel_hi:[1,0]
	v_pk_mul_f32 v[154:155], v[154:155], s[30:31] op_sel_hi:[1,0]
	v_pk_mul_f32 v[156:157], v[156:157], s[30:31] op_sel_hi:[1,0]
	v_pk_mul_f32 v[158:159], v[158:159], s[30:31] op_sel_hi:[1,0]
	v_pk_mul_f32 v[160:161], v[160:161], s[30:31] op_sel_hi:[1,0]
	v_pk_mul_f32 v[162:163], v[162:163], s[30:31] op_sel_hi:[1,0]
	v_pk_mul_f32 v[164:165], v[164:165], s[30:31] op_sel_hi:[1,0]
	v_pk_mul_f32 v[166:167], v[166:167], s[30:31] op_sel_hi:[1,0]
	v_pk_mul_f32 v[168:169], v[168:169], s[30:31] op_sel_hi:[1,0]
	v_pk_mul_f32 v[170:171], v[170:171], s[30:31] op_sel_hi:[1,0]
	v_pk_mul_f32 v[172:173], v[172:173], s[30:31] op_sel_hi:[1,0]
	v_pk_mul_f32 v[174:175], v[174:175], s[30:31] op_sel_hi:[1,0]
	v_pk_mul_f32 v[176:177], v[176:177], s[30:31] op_sel_hi:[1,0]
	v_pk_mul_f32 v[178:179], v[178:179], s[30:31] op_sel_hi:[1,0]
	v_pk_mul_f32 v[180:181], v[180:181], s[30:31] op_sel_hi:[1,0]
	v_pk_mul_f32 v[182:183], v[182:183], s[30:31] op_sel_hi:[1,0]
	v_pk_mul_f32 v[184:185], v[184:185], s[30:31] op_sel_hi:[1,0]
	v_pk_mul_f32 v[186:187], v[186:187], s[30:31] op_sel_hi:[1,0]
	v_pk_mul_f32 v[188:189], v[188:189], s[30:31] op_sel_hi:[1,0]
	v_pk_mul_f32 v[190:191], v[190:191], s[30:31] op_sel_hi:[1,0]
	v_pk_mul_f32 v[192:193], v[192:193], s[30:31] op_sel_hi:[1,0]
	v_med3_f32 v130, v130, s24, v237
	v_med3_f32 v131, v131, s24, v237
	v_med3_f32 v132, v132, s24, v237
	v_med3_f32 v133, v133, s24, v237
	v_med3_f32 v134, v134, s24, v237
	v_med3_f32 v135, v135, s24, v237
	v_med3_f32 v136, v136, s24, v237
	v_med3_f32 v137, v137, s24, v237
	v_med3_f32 v138, v138, s24, v237
	v_med3_f32 v139, v139, s24, v237
	v_med3_f32 v140, v140, s24, v237
	v_med3_f32 v141, v141, s24, v237
	v_med3_f32 v142, v142, s24, v237
	v_med3_f32 v143, v143, s24, v237
	v_med3_f32 v144, v144, s24, v237
	v_med3_f32 v145, v145, s24, v237
	v_med3_f32 v146, v146, s24, v237
	v_med3_f32 v147, v147, s24, v237
	v_med3_f32 v148, v148, s24, v237
	v_med3_f32 v149, v149, s24, v237
	v_med3_f32 v150, v150, s24, v237
	v_med3_f32 v151, v151, s24, v237
	v_med3_f32 v152, v152, s24, v237
	v_med3_f32 v153, v153, s24, v237
	v_med3_f32 v154, v154, s24, v237
	v_med3_f32 v155, v155, s24, v237
	v_med3_f32 v156, v156, s24, v237
	v_med3_f32 v157, v157, s24, v237
	v_med3_f32 v158, v158, s24, v237
	v_med3_f32 v159, v159, s24, v237
	v_med3_f32 v160, v160, s24, v237
	v_med3_f32 v161, v161, s24, v237
	v_med3_f32 v162, v162, s24, v237
	v_med3_f32 v163, v163, s24, v237
	v_med3_f32 v164, v164, s24, v237
	v_med3_f32 v165, v165, s24, v237
	v_med3_f32 v166, v166, s24, v237
	v_med3_f32 v167, v167, s24, v237
	v_med3_f32 v168, v168, s24, v237
	v_med3_f32 v169, v169, s24, v237
	v_med3_f32 v170, v170, s24, v237
	v_med3_f32 v171, v171, s24, v237
	v_med3_f32 v172, v172, s24, v237
	v_med3_f32 v173, v173, s24, v237
	v_med3_f32 v174, v174, s24, v237
	v_med3_f32 v175, v175, s24, v237
	v_med3_f32 v176, v176, s24, v237
	v_med3_f32 v177, v177, s24, v237
	v_med3_f32 v178, v178, s24, v237
	v_med3_f32 v179, v179, s24, v237
	v_med3_f32 v180, v180, s24, v237
	v_med3_f32 v181, v181, s24, v237
	v_med3_f32 v182, v182, s24, v237
	v_med3_f32 v183, v183, s24, v237
	v_med3_f32 v184, v184, s24, v237
	v_med3_f32 v185, v185, s24, v237
	v_med3_f32 v186, v186, s24, v237
	v_med3_f32 v187, v187, s24, v237
	v_med3_f32 v188, v188, s24, v237
	v_med3_f32 v189, v189, s24, v237
	v_med3_f32 v190, v190, s24, v237
	v_med3_f32 v191, v191, s24, v237
	v_med3_f32 v192, v192, s24, v237
	v_med3_f32 v193, v193, s24, v237
	v_cvt_pk_fp8_f32 v130, v130, v134
	v_cvt_pk_fp8_f32 v130, v138, v142 op_sel:[0,0,1]
	v_cvt_pk_fp8_f32 v134, v131, v135
	v_cvt_pk_fp8_f32 v134, v139, v143 op_sel:[0,0,1]
	v_cvt_pk_fp8_f32 v138, v132, v136
	v_cvt_pk_fp8_f32 v138, v140, v144 op_sel:[0,0,1]
	v_cvt_pk_fp8_f32 v142, v133, v137
	v_cvt_pk_fp8_f32 v142, v141, v145 op_sel:[0,0,1]
	v_cvt_pk_fp8_f32 v131, v146, v150
	v_cvt_pk_fp8_f32 v131, v154, v158 op_sel:[0,0,1]
	v_cvt_pk_fp8_f32 v135, v147, v151
	v_cvt_pk_fp8_f32 v135, v155, v159 op_sel:[0,0,1]
	v_cvt_pk_fp8_f32 v139, v148, v152
	v_cvt_pk_fp8_f32 v139, v156, v160 op_sel:[0,0,1]
	v_cvt_pk_fp8_f32 v143, v149, v153
	v_cvt_pk_fp8_f32 v143, v157, v161 op_sel:[0,0,1]
	v_cvt_pk_fp8_f32 v132, v162, v166
	v_cvt_pk_fp8_f32 v132, v170, v174 op_sel:[0,0,1]
	v_cvt_pk_fp8_f32 v136, v163, v167
	v_cvt_pk_fp8_f32 v136, v171, v175 op_sel:[0,0,1]
	v_cvt_pk_fp8_f32 v140, v164, v168
	v_cvt_pk_fp8_f32 v140, v172, v176 op_sel:[0,0,1]
	v_cvt_pk_fp8_f32 v144, v165, v169
	v_cvt_pk_fp8_f32 v144, v173, v177 op_sel:[0,0,1]
	v_cvt_pk_fp8_f32 v133, v178, v182
	v_cvt_pk_fp8_f32 v133, v186, v190 op_sel:[0,0,1]
	v_cvt_pk_fp8_f32 v137, v179, v183
	v_cvt_pk_fp8_f32 v137, v187, v191 op_sel:[0,0,1]
	v_cvt_pk_fp8_f32 v141, v180, v184
	v_cvt_pk_fp8_f32 v141, v188, v192 op_sel:[0,0,1]
	v_cvt_pk_fp8_f32 v145, v181, v185
	v_cvt_pk_fp8_f32 v145, v189, v193 op_sel:[0,0,1]
	global_store_dwordx4 v250, v[130:133], s[42:43] nt
	global_store_dwordx4 v250, v[134:137], s[42:43] offset:2048 nt
	global_store_dwordx4 v251, v[138:141], s[42:43] nt
	global_store_dwordx4 v251, v[142:145], s[42:43] offset:2048 nt
	s_add_u32 s42, s42, 0x10000
	s_addc_u32 s43, s43, 0
	global_load_dwordx4 v[130:133], v246, s[4:5] offset:1024 nt
	global_load_dwordx4 v[134:137], v247, s[4:5] offset:1024 nt
	global_load_dwordx4 v[138:141], v248, s[4:5] offset:1024 nt
	global_load_dwordx4 v[142:145], v249, s[4:5] offset:1024 nt
	global_load_dwordx4 v[146:149], v246, s[6:7] offset:1024 nt
	global_load_dwordx4 v[150:153], v247, s[6:7] offset:1024 nt
	global_load_dwordx4 v[154:157], v248, s[6:7] offset:1024 nt
	global_load_dwordx4 v[158:161], v249, s[6:7] offset:1024 nt
	global_load_dwordx4 v[162:165], v246, s[8:9] offset:1024 nt
	global_load_dwordx4 v[166:169], v247, s[8:9] offset:1024 nt
	global_load_dwordx4 v[170:173], v248, s[8:9] offset:1024 nt
	global_load_dwordx4 v[174:177], v249, s[8:9] offset:1024 nt
	global_load_dwordx4 v[178:181], v246, s[38:39] offset:1024 nt
	global_load_dwordx4 v[182:185], v247, s[38:39] offset:1024 nt
	global_load_dwordx4 v[186:189], v248, s[38:39] offset:1024 nt
	global_load_dwordx4 v[190:193], v249, s[38:39] offset:1024 nt
	s_waitcnt vmcnt(40)
; #define GAS __attribute__((address_space(1)))
; template <bool GAIN, bool NT = false> __device__ __forceinline__ void titem8_load(const TItem& d, int lane, f32x4 (&r)[16], f32x4 (&g)[4]) {
;     const int q = lane & 7, kg = lane >> 3; const unsigned lo = (unsigned)((16 * kg) * d.N + 4 * q) * 4u;
;     const GAS char* base = (const GAS char*)d.src;
; #pragma unroll
;     for (int j = 0; j < 16; ++j) { const GAS f32x4* p = (const GAS f32x4*)(base + (size_t)j * (size_t)d.N * 4 + lo); r[j] = NT ? __builtin_nontemporal_load(p) : *p; }
;     if constexpr (GAIN) { const GAS char* gb = (const GAS char*)d.gain; const unsigned go = (unsigned)(16 * kg) * 4u;
; #pragma unroll
;         for (int j4 = 0; j4 < 4; ++j4) g[j4] = *(const GAS f32x4*)(gb + 16 * j4 + go); }
;     asm volatile("" ::: "memory"); __builtin_amdgcn_sched_barrier(0);
; template <bool GAIN, bool NT = false> __device__ __forceinline__ void titem8_store(const TItem& d, int lane, const f32x4 (&r)[16], const f32x4 (&g)[4]) {
;     const int q = lane & 7, kg = lane >> 3; const unsigned lo = (unsigned)((4 * q) * d.ldk + 16 * kg);
;     GAS char* base = (GAS char*)d.dst;
;     f32x4 s[16];
; #pragma unroll
;     for (int j = 0; j < 16; ++j) s[j] = r[j] * ((GAIN ? g[j >> 2][j & 3] : 1.0f) * W8_SCALE);
; #pragma unroll
;     for (int i = 0; i < 4; ++i) { v4u w;
;         w.x = pk4_fp8w(s[0][i], s[1][i], s[2][i], s[3][i]); w.y = pk4_fp8w(s[4][i], s[5][i], s[6][i], s[7][i]);
;         w.z = pk4_fp8w(s[8][i], s[9][i], s[10][i], s[11][i]); w.w = pk4_fp8w(s[12][i], s[13][i], s[14][i], s[15][i]);
;         GAS v4u* p = (GAS v4u*)(base + (size_t)i * (size_t)d.ldk + lo);
;         if (NT) __builtin_nontemporal_store(w, p); else *p = w; }
; }
	v_pk_mul_f32 v[0:1], v[0:1], s[30:31] op_sel_hi:[1,0]
	v_pk_mul_f32 v[2:3], v[2:3], s[30:31] op_sel_hi:[1,0]
	v_pk_mul_f32 v[4:5], v[4:5], s[30:31] op_sel_hi:[1,0]
	v_pk_mul_f32 v[6:7], v[6:7], s[30:31] op_sel_hi:[1,0]
	v_pk_mul_f32 v[8:9], v[8:9], s[30:31] op_sel_hi:[1,0]
	v_pk_mul_f32 v[10:11], v[10:11], s[30:31] op_sel_hi:[1,0]
	v_pk_mul_f32 v[12:13], v[12:13], s[30:31] op_sel_hi:[1,0]
	v_pk_mul_f32 v[14:15], v[14:15], s[30:31] op_sel_hi:[1,0]
	v_pk_mul_f32 v[16:17], v[16:17], s[30:31] op_sel_hi:[1,0]
	v_pk_mul_f32 v[18:19], v[18:19], s[30:31] op_sel_hi:[1,0]
	v_pk_mul_f32 v[20:21], v[20:21], s[30:31] op_sel_hi:[1,0]
	v_pk_mul_f32 v[22:23], v[22:23], s[30:31] op_sel_hi:[1,0]
	v_pk_mul_f32 v[24:25], v[24:25], s[30:31] op_sel_hi:[1,0]
	v_pk_mul_f32 v[26:27], v[26:27], s[30:31] op_sel_hi:[1,0]
	v_pk_mul_f32 v[28:29], v[28:29], s[30:31] op_sel_hi:[1,0]
	v_pk_mul_f32 v[30:31], v[30:31], s[30:31] op_sel_hi:[1,0]
	v_pk_mul_f32 v[32:33], v[32:33], s[30:31] op_sel_hi:[1,0]
	v_pk_mul_f32 v[34:35], v[34:35], s[30:31] op_sel_hi:[1,0]
	v_pk_mul_f32 v[36:37], v[36:37], s[30:31] op_sel_hi:[1,0]
	v_pk_mul_f32 v[38:39], v[38:39], s[30:31] op_sel_hi:[1,0]
	v_pk_mul_f32 v[40:41], v[40:41], s[30:31] op_sel_hi:[1,0]
	v_pk_mul_f32 v[42:43], v[42:43], s[30:31] op_sel_hi:[1,0]
	v_pk_mul_f32 v[44:45], v[44:45], s[30:31] op_sel_hi:[1,0]
	v_pk_mul_f32 v[46:47], v[46:47], s[30:31] op_sel_hi:[1,0]
	v_pk_mul_f32 v[48:49], v[48:49], s[30:31] op_sel_hi:[1,0]
	v_pk_mul_f32 v[50:51], v[50:51], s[30:31] op_sel_hi:[1,0]
	v_pk_mul_f32 v[52:53], v[52:53], s[30:31] op_sel_hi:[1,0]
	v_pk_mul_f32 v[54:55], v[54:55], s[30:31] op_sel_hi:[1,0]
	v_pk_mul_f32 v[56:57], v[56:57], s[30:31] op_sel_hi:[1,0]
	v_pk_mul_f32 v[58:59], v[58:59], s[30:31] op_sel_hi:[1,0]
	v_pk_mul_f32 v[60:61], v[60:61], s[30:31] op_sel_hi:[1,0]
	v_pk_mul_f32 v[62:63], v[62:63], s[30:31] op_sel_hi:[1,0]
	v_med3_f32 v0, v0, s24, v237
	v_med3_f32 v1, v1, s24, v237
	v_med3_f32 v2, v2, s24, v237
	v_med3_f32 v3, v3, s24, v237
	v_med3_f32 v4, v4, s24, v237
	v_med3_f32 v5, v5, s24, v237
	v_med3_f32 v6, v6, s24, v237
	v_med3_f32 v7, v7, s24, v237
	v_med3_f32 v8, v8, s24, v237
	v_med3_f32 v9, v9, s24, v237
	v_med3_f32 v10, v10, s24, v237
	v_med3_f32 v11, v11, s24, v237
	v_med3_f32 v12, v12, s24, v237
	v_med3_f32 v13, v13, s24, v237
	v_med3_f32 v14, v14, s24, v237
	v_med3_f32 v15, v15, s24, v237
	v_med3_f32 v16, v16, s24, v237
	v_med3_f32 v17, v17, s24, v237
	v_med3_f32 v18, v18, s24, v237
	v_med3_f32 v19, v19, s24, v237
	v_med3_f32 v20, v20, s24, v237
	v_med3_f32 v21, v21, s24, v237
	v_med3_f32 v22, v22, s24, v237
	v_med3_f32 v23, v23, s24, v237
	v_med3_f32 v24, v24, s24, v237
	v_med3_f32 v25, v25, s24, v237
	v_med3_f32 v26, v26, s24, v237
	v_med3_f32 v27, v27, s24, v237
	v_med3_f32 v28, v28, s24, v237
	v_med3_f32 v29, v29, s24, v237
	v_med3_f32 v30, v30, s24, v237
	v_med3_f32 v31, v31, s24, v237
	v_med3_f32 v32, v32, s24, v237
	v_med3_f32 v33, v33, s24, v237
	v_med3_f32 v34, v34, s24, v237
	v_med3_f32 v35, v35, s24, v237
	v_med3_f32 v36, v36, s24, v237
	v_med3_f32 v37, v37, s24, v237
	v_med3_f32 v38, v38, s24, v237
	v_med3_f32 v39, v39, s24, v237
	v_med3_f32 v40, v40, s24, v237
	v_med3_f32 v41, v41, s24, v237
	v_med3_f32 v42, v42, s24, v237
	v_med3_f32 v43, v43, s24, v237
	v_med3_f32 v44, v44, s24, v237
	v_med3_f32 v45, v45, s24, v237
	v_med3_f32 v46, v46, s24, v237
	v_med3_f32 v47, v47, s24, v237
	v_med3_f32 v48, v48, s24, v237
	v_med3_f32 v49, v49, s24, v237
	v_med3_f32 v50, v50, s24, v237
	v_med3_f32 v51, v51, s24, v237
	v_med3_f32 v52, v52, s24, v237
	v_med3_f32 v53, v53, s24, v237
	v_med3_f32 v54, v54, s24, v237
	v_med3_f32 v55, v55, s24, v237
	v_med3_f32 v56, v56, s24, v237
	v_med3_f32 v57, v57, s24, v237
	v_med3_f32 v58, v58, s24, v237
	v_med3_f32 v59, v59, s24, v237
	v_med3_f32 v60, v60, s24, v237
	v_med3_f32 v61, v61, s24, v237
	v_med3_f32 v62, v62, s24, v237
	v_med3_f32 v63, v63, s24, v237
	v_cvt_pk_fp8_f32 v0, v0, v4
	v_cvt_pk_fp8_f32 v0, v8, v12 op_sel:[0,0,1]
	v_cvt_pk_fp8_f32 v4, v1, v5
	v_cvt_pk_fp8_f32 v4, v9, v13 op_sel:[0,0,1]
	v_cvt_pk_fp8_f32 v8, v2, v6
	v_cvt_pk_fp8_f32 v8, v10, v14 op_sel:[0,0,1]
	v_cvt_pk_fp8_f32 v12, v3, v7
	v_cvt_pk_fp8_f32 v12, v11, v15 op_sel:[0,0,1]
	v_cvt_pk_fp8_f32 v1, v16, v20
	v_cvt_pk_fp8_f32 v1, v24, v28 op_sel:[0,0,1]
	v_cvt_pk_fp8_f32 v5, v17, v21
	v_cvt_pk_fp8_f32 v5, v25, v29 op_sel:[0,0,1]
	v_cvt_pk_fp8_f32 v9, v18, v22
	v_cvt_pk_fp8_f32 v9, v26, v30 op_sel:[0,0,1]
	v_cvt_pk_fp8_f32 v13, v19, v23
	v_cvt_pk_fp8_f32 v13, v27, v31 op_sel:[0,0,1]
	v_cvt_pk_fp8_f32 v2, v32, v36
	v_cvt_pk_fp8_f32 v2, v40, v44 op_sel:[0,0,1]
	v_cvt_pk_fp8_f32 v6, v33, v37
	v_cvt_pk_fp8_f32 v6, v41, v45 op_sel:[0,0,1]
	v_cvt_pk_fp8_f32 v10, v34, v38
	v_cvt_pk_fp8_f32 v10, v42, v46 op_sel:[0,0,1]
	v_cvt_pk_fp8_f32 v14, v35, v39
	v_cvt_pk_fp8_f32 v14, v43, v47 op_sel:[0,0,1]
	v_cvt_pk_fp8_f32 v3, v48, v52
	v_cvt_pk_fp8_f32 v3, v56, v60 op_sel:[0,0,1]
	v_cvt_pk_fp8_f32 v7, v49, v53
	v_cvt_pk_fp8_f32 v7, v57, v61 op_sel:[0,0,1]
	v_cvt_pk_fp8_f32 v11, v50, v54
	v_cvt_pk_fp8_f32 v11, v58, v62 op_sel:[0,0,1]
	v_cvt_pk_fp8_f32 v15, v51, v55
	v_cvt_pk_fp8_f32 v15, v59, v63 op_sel:[0,0,1]
	global_store_dwordx4 v250, v[0:3], s[42:43] nt
	global_store_dwordx4 v250, v[4:7], s[42:43] offset:2048 nt
	global_store_dwordx4 v251, v[8:11], s[42:43] nt
	global_store_dwordx4 v251, v[12:15], s[42:43] offset:2048 nt
	s_add_u32 s42, s42, 0x10000
	s_addc_u32 s43, s43, 0
	global_load_dwordx4 v[0:3], v246, s[4:5] offset:1152 nt
	global_load_dwordx4 v[4:7], v247, s[4:5] offset:1152 nt
	global_load_dwordx4 v[8:11], v248, s[4:5] offset:1152 nt
	global_load_dwordx4 v[12:15], v249, s[4:5] offset:1152 nt
	global_load_dwordx4 v[16:19], v246, s[6:7] offset:1152 nt
	global_load_dwordx4 v[20:23], v247, s[6:7] offset:1152 nt
	global_load_dwordx4 v[24:27], v248, s[6:7] offset:1152 nt
	global_load_dwordx4 v[28:31], v249, s[6:7] offset:1152 nt
	global_load_dwordx4 v[32:35], v246, s[8:9] offset:1152 nt
	global_load_dwordx4 v[36:39], v247, s[8:9] offset:1152 nt
	global_load_dwordx4 v[40:43], v248, s[8:9] offset:1152 nt
	global_load_dwordx4 v[44:47], v249, s[8:9] offset:1152 nt
	global_load_dwordx4 v[48:51], v246, s[38:39] offset:1152 nt
	global_load_dwordx4 v[52:55], v247, s[38:39] offset:1152 nt
	global_load_dwordx4 v[56:59], v248, s[38:39] offset:1152 nt
	global_load_dwordx4 v[60:63], v249, s[38:39] offset:1152 nt
	s_waitcnt vmcnt(40)
; #define GAS __attribute__((address_space(1)))
; template <bool GAIN, bool NT = false> __device__ __forceinline__ void titem8_load(const TItem& d, int lane, f32x4 (&r)[16], f32x4 (&g)[4]) {
;     const int q = lane & 7, kg = lane >> 3; const unsigned lo = (unsigned)((16 * kg) * d.N + 4 * q) * 4u;
;     const GAS char* base = (const GAS char*)d.src;
; #pragma unroll
;     for (int j = 0; j < 16; ++j) { const GAS f32x4* p = (const GAS f32x4*)(base + (size_t)j * (size_t)d.N * 4 + lo); r[j] = NT ? __builtin_nontemporal_load(p) : *p; }
;     if constexpr (GAIN) { const GAS char* gb = (const GAS char*)d.gain; const unsigned go = (unsigned)(16 * kg) * 4u;
; #pragma unroll
;         for (int j4 = 0; j4 < 4; ++j4) g[j4] = *(const GAS f32x4*)(gb + 16 * j4 + go); }
;     asm volatile("" ::: "memory"); __builtin_amdgcn_sched_barrier(0);
; template <bool GAIN, bool NT = false> __device__ __forceinline__ void titem8_store(const TItem& d, int lane, const f32x4 (&r)[16], const f32x4 (&g)[4]) {
;     const int q = lane & 7, kg = lane >> 3; const unsigned lo = (unsigned)((4 * q) * d.ldk + 16 * kg);
;     GAS char* base = (GAS char*)d.dst;
;     f32x4 s[16];
; #pragma unroll
;     for (int j = 0; j < 16; ++j) s[j] = r[j] * ((GAIN ? g[j >> 2][j & 3] : 1.0f) * W8_SCALE);
; #pragma unroll
;     for (int i = 0; i < 4; ++i) { v4u w;
;         w.x = pk4_fp8w(s[0][i], s[1][i], s[2][i], s[3][i]); w.y = pk4_fp8w(s[4][i], s[5][i], s[6][i], s[7][i]);
;         w.z = pk4_fp8w(s[8][i], s[9][i], s[10][i], s[11][i]); w.w = pk4_fp8w(s[12][i], s[13][i], s[14][i], s[15][i]);
;         GAS v4u* p = (GAS v4u*)(base + (size_t)i * (size_t)d.ldk + lo);
;         if (NT) __builtin_nontemporal_store(w, p); else *p = w; }
; }
	v_pk_mul_f32 v[66:67], v[66:67], s[30:31] op_sel_hi:[1,0]
	v_pk_mul_f32 v[68:69], v[68:69], s[30:31] op_sel_hi:[1,0]
	v_pk_mul_f32 v[70:71], v[70:71], s[30:31] op_sel_hi:[1,0]
	v_pk_mul_f32 v[72:73], v[72:73], s[30:31] op_sel_hi:[1,0]
	v_pk_mul_f32 v[74:75], v[74:75], s[30:31] op_sel_hi:[1,0]
	v_pk_mul_f32 v[76:77], v[76:77], s[30:31] op_sel_hi:[1,0]
	v_pk_mul_f32 v[78:79], v[78:79], s[30:31] op_sel_hi:[1,0]
	v_pk_mul_f32 v[80:81], v[80:81], s[30:31] op_sel_hi:[1,0]
	v_pk_mul_f32 v[82:83], v[82:83], s[30:31] op_sel_hi:[1,0]
	v_pk_mul_f32 v[84:85], v[84:85], s[30:31] op_sel_hi:[1,0]
	v_pk_mul_f32 v[86:87], v[86:87], s[30:31] op_sel_hi:[1,0]
	v_pk_mul_f32 v[88:89], v[88:89], s[30:31] op_sel_hi:[1,0]
	v_pk_mul_f32 v[90:91], v[90:91], s[30:31] op_sel_hi:[1,0]
	v_pk_mul_f32 v[92:93], v[92:93], s[30:31] op_sel_hi:[1,0]
	v_pk_mul_f32 v[94:95], v[94:95], s[30:31] op_sel_hi:[1,0]
	v_pk_mul_f32 v[96:97], v[96:97], s[30:31] op_sel_hi:[1,0]
	v_pk_mul_f32 v[98:99], v[98:99], s[30:31] op_sel_hi:[1,0]
	v_pk_mul_f32 v[100:101], v[100:101], s[30:31] op_sel_hi:[1,0]
	v_pk_mul_f32 v[102:103], v[102:103], s[30:31] op_sel_hi:[1,0]
	v_pk_mul_f32 v[104:105], v[104:105], s[30:31] op_sel_hi:[1,0]
	v_pk_mul_f32 v[106:107], v[106:107], s[30:31] op_sel_hi:[1,0]
	v_pk_mul_f32 v[108:109], v[108:109], s[30:31] op_sel_hi:[1,0]
	v_pk_mul_f32 v[110:111], v[110:111], s[30:31] op_sel_hi:[1,0]
	v_pk_mul_f32 v[112:113], v[112:113], s[30:31] op_sel_hi:[1,0]
	v_pk_mul_f32 v[114:115], v[114:115], s[30:31] op_sel_hi:[1,0]
	v_pk_mul_f32 v[116:117], v[116:117], s[30:31] op_sel_hi:[1,0]
	v_pk_mul_f32 v[118:119], v[118:119], s[30:31] op_sel_hi:[1,0]
	v_pk_mul_f32 v[120:121], v[120:121], s[30:31] op_sel_hi:[1,0]
	v_pk_mul_f32 v[122:123], v[122:123], s[30:31] op_sel_hi:[1,0]
	v_pk_mul_f32 v[124:125], v[124:125], s[30:31] op_sel_hi:[1,0]
	v_pk_mul_f32 v[126:127], v[126:127], s[30:31] op_sel_hi:[1,0]
	v_pk_mul_f32 v[128:129], v[128:129], s[30:31] op_sel_hi:[1,0]
	v_med3_f32 v66, v66, s24, v237
	v_med3_f32 v67, v67, s24, v237
	v_med3_f32 v68, v68, s24, v237
	v_med3_f32 v69, v69, s24, v237
	v_med3_f32 v70, v70, s24, v237
	v_med3_f32 v71, v71, s24, v237
	v_med3_f32 v72, v72, s24, v237
	v_med3_f32 v73, v73, s24, v237
	v_med3_f32 v74, v74, s24, v237
	v_med3_f32 v75, v75, s24, v237
	v_med3_f32 v76, v76, s24, v237
	v_med3_f32 v77, v77, s24, v237
	v_med3_f32 v78, v78, s24, v237
	v_med3_f32 v79, v79, s24, v237
	v_med3_f32 v80, v80, s24, v237
	v_med3_f32 v81, v81, s24, v237
	v_med3_f32 v82, v82, s24, v237
	v_med3_f32 v83, v83, s24, v237
	v_med3_f32 v84, v84, s24, v237
	v_med3_f32 v85, v85, s24, v237
	v_med3_f32 v86, v86, s24, v237
	v_med3_f32 v87, v87, s24, v237
	v_med3_f32 v88, v88, s24, v237
	v_med3_f32 v89, v89, s24, v237
	v_med3_f32 v90, v90, s24, v237
	v_med3_f32 v91, v91, s24, v237
	v_med3_f32 v92, v92, s24, v237
	v_med3_f32 v93, v93, s24, v237
	v_med3_f32 v94, v94, s24, v237
	v_med3_f32 v95, v95, s24, v237
	v_med3_f32 v96, v96, s24, v237
	v_med3_f32 v97, v97, s24, v237
	v_med3_f32 v98, v98, s24, v237
	v_med3_f32 v99, v99, s24, v237
	v_med3_f32 v100, v100, s24, v237
	v_med3_f32 v101, v101, s24, v237
	v_med3_f32 v102, v102, s24, v237
	v_med3_f32 v103, v103, s24, v237
	v_med3_f32 v104, v104, s24, v237
	v_med3_f32 v105, v105, s24, v237
	v_med3_f32 v106, v106, s24, v237
	v_med3_f32 v107, v107, s24, v237
	v_med3_f32 v108, v108, s24, v237
	v_med3_f32 v109, v109, s24, v237
	v_med3_f32 v110, v110, s24, v237
	v_med3_f32 v111, v111, s24, v237
	v_med3_f32 v112, v112, s24, v237
	v_med3_f32 v113, v113, s24, v237
	v_med3_f32 v114, v114, s24, v237
	v_med3_f32 v115, v115, s24, v237
	v_med3_f32 v116, v116, s24, v237
	v_med3_f32 v117, v117, s24, v237
	v_med3_f32 v118, v118, s24, v237
	v_med3_f32 v119, v119, s24, v237
	v_med3_f32 v120, v120, s24, v237
	v_med3_f32 v121, v121, s24, v237
	v_med3_f32 v122, v122, s24, v237
	v_med3_f32 v123, v123, s24, v237
	v_med3_f32 v124, v124, s24, v237
	v_med3_f32 v125, v125, s24, v237
	v_med3_f32 v126, v126, s24, v237
	v_med3_f32 v127, v127, s24, v237
	v_med3_f32 v128, v128, s24, v237
	v_med3_f32 v129, v129, s24, v237
	v_cvt_pk_fp8_f32 v66, v66, v70
	v_cvt_pk_fp8_f32 v66, v74, v78 op_sel:[0,0,1]
	v_cvt_pk_fp8_f32 v70, v67, v71
	v_cvt_pk_fp8_f32 v70, v75, v79 op_sel:[0,0,1]
	v_cvt_pk_fp8_f32 v74, v68, v72
	v_cvt_pk_fp8_f32 v74, v76, v80 op_sel:[0,0,1]
	v_cvt_pk_fp8_f32 v78, v69, v73
	v_cvt_pk_fp8_f32 v78, v77, v81 op_sel:[0,0,1]
	v_cvt_pk_fp8_f32 v67, v82, v86
	v_cvt_pk_fp8_f32 v67, v90, v94 op_sel:[0,0,1]
	v_cvt_pk_fp8_f32 v71, v83, v87
	v_cvt_pk_fp8_f32 v71, v91, v95 op_sel:[0,0,1]
	v_cvt_pk_fp8_f32 v75, v84, v88
	v_cvt_pk_fp8_f32 v75, v92, v96 op_sel:[0,0,1]
	v_cvt_pk_fp8_f32 v79, v85, v89
	v_cvt_pk_fp8_f32 v79, v93, v97 op_sel:[0,0,1]
	v_cvt_pk_fp8_f32 v68, v98, v102
	v_cvt_pk_fp8_f32 v68, v106, v110 op_sel:[0,0,1]
	v_cvt_pk_fp8_f32 v72, v99, v103
	v_cvt_pk_fp8_f32 v72, v107, v111 op_sel:[0,0,1]
	v_cvt_pk_fp8_f32 v76, v100, v104
	v_cvt_pk_fp8_f32 v76, v108, v112 op_sel:[0,0,1]
	v_cvt_pk_fp8_f32 v80, v101, v105
	v_cvt_pk_fp8_f32 v80, v109, v113 op_sel:[0,0,1]
	v_cvt_pk_fp8_f32 v69, v114, v118
	v_cvt_pk_fp8_f32 v69, v122, v126 op_sel:[0,0,1]
	v_cvt_pk_fp8_f32 v73, v115, v119
	v_cvt_pk_fp8_f32 v73, v123, v127 op_sel:[0,0,1]
	v_cvt_pk_fp8_f32 v77, v116, v120
	v_cvt_pk_fp8_f32 v77, v124, v128 op_sel:[0,0,1]
	v_cvt_pk_fp8_f32 v81, v117, v121
	v_cvt_pk_fp8_f32 v81, v125, v129 op_sel:[0,0,1]
	global_store_dwordx4 v250, v[66:69], s[42:43] nt
	global_store_dwordx4 v250, v[70:73], s[42:43] offset:2048 nt
	global_store_dwordx4 v251, v[74:77], s[42:43] nt
	global_store_dwordx4 v251, v[78:81], s[42:43] offset:2048 nt
	s_add_u32 s42, s42, 0x10000
	s_addc_u32 s43, s43, 0
	global_load_dwordx4 v[66:69], v246, s[4:5] offset:1280 nt
	global_load_dwordx4 v[70:73], v247, s[4:5] offset:1280 nt
	global_load_dwordx4 v[74:77], v248, s[4:5] offset:1280 nt
	global_load_dwordx4 v[78:81], v249, s[4:5] offset:1280 nt
	global_load_dwordx4 v[82:85], v246, s[6:7] offset:1280 nt
	global_load_dwordx4 v[86:89], v247, s[6:7] offset:1280 nt
	global_load_dwordx4 v[90:93], v248, s[6:7] offset:1280 nt
	global_load_dwordx4 v[94:97], v249, s[6:7] offset:1280 nt
	global_load_dwordx4 v[98:101], v246, s[8:9] offset:1280 nt
	global_load_dwordx4 v[102:105], v247, s[8:9] offset:1280 nt
	global_load_dwordx4 v[106:109], v248, s[8:9] offset:1280 nt
	global_load_dwordx4 v[110:113], v249, s[8:9] offset:1280 nt
	global_load_dwordx4 v[114:117], v246, s[38:39] offset:1280 nt
	global_load_dwordx4 v[118:121], v247, s[38:39] offset:1280 nt
	global_load_dwordx4 v[122:125], v248, s[38:39] offset:1280 nt
	global_load_dwordx4 v[126:129], v249, s[38:39] offset:1280 nt
	s_waitcnt vmcnt(40)
; #define GAS __attribute__((address_space(1)))
; template <bool GAIN, bool NT = false> __device__ __forceinline__ void titem8_load(const TItem& d, int lane, f32x4 (&r)[16], f32x4 (&g)[4]) {
;     const int q = lane & 7, kg = lane >> 3; const unsigned lo = (unsigned)((16 * kg) * d.N + 4 * q) * 4u;
;     const GAS char* base = (const GAS char*)d.src;
; #pragma unroll
;     for (int j = 0; j < 16; ++j) { const GAS f32x4* p = (const GAS f32x4*)(base + (size_t)j * (size_t)d.N * 4 + lo); r[j] = NT ? __builtin_nontemporal_load(p) : *p; }
;     if constexpr (GAIN) { const GAS char* gb = (const GAS char*)d.gain; const unsigned go = (unsigned)(16 * kg) * 4u;
; #pragma unroll
;         for (int j4 = 0; j4 < 4; ++j4) g[j4] = *(const GAS f32x4*)(gb + 16 * j4 + go); }
;     asm volatile("" ::: "memory"); __builtin_amdgcn_sched_barrier(0);
; template <bool GAIN, bool NT = false> __device__ __forceinline__ void titem8_store(const TItem& d, int lane, const f32x4 (&r)[16], const f32x4 (&g)[4]) {
;     const int q = lane & 7, kg = lane >> 3; const unsigned lo = (unsigned)((4 * q) * d.ldk + 16 * kg);
;     GAS char* base = (GAS char*)d.dst;
;     f32x4 s[16];
; #pragma unroll
;     for (int j = 0; j < 16; ++j) s[j] = r[j] * ((GAIN ? g[j >> 2][j & 3] : 1.0f) * W8_SCALE);
; #pragma unroll
;     for (int i = 0; i < 4; ++i) { v4u w;
;         w.x = pk4_fp8w(s[0][i], s[1][i], s[2][i], s[3][i]); w.y = pk4_fp8w(s[4][i], s[5][i], s[6][i], s[7][i]);
;         w.z = pk4_fp8w(s[8][i], s[9][i], s[10][i], s[11][i]); w.w = pk4_fp8w(s[12][i], s[13][i], s[14][i], s[15][i]);
;         GAS v4u* p = (GAS v4u*)(base + (size_t)i * (size_t)d.ldk + lo);
;         if (NT) __builtin_nontemporal_store(w, p); else *p = w; }
; }
	v_pk_mul_f32 v[130:131], v[130:131], s[30:31] op_sel_hi:[1,0]
	v_pk_mul_f32 v[132:133], v[132:133], s[30:31] op_sel_hi:[1,0]
	v_pk_mul_f32 v[134:135], v[134:135], s[30:31] op_sel_hi:[1,0]
	v_pk_mul_f32 v[136:137], v[136:137], s[30:31] op_sel_hi:[1,0]
	v_pk_mul_f32 v[138:139], v[138:139], s[30:31] op_sel_hi:[1,0]
	v_pk_mul_f32 v[140:141], v[140:141], s[30:31] op_sel_hi:[1,0]
	v_pk_mul_f32 v[142:143], v[142:143], s[30:31] op_sel_hi:[1,0]
	v_pk_mul_f32 v[144:145], v[144:145], s[30:31] op_sel_hi:[1,0]
	v_pk_mul_f32 v[146:147], v[146:147], s[30:31] op_sel_hi:[1,0]
	v_pk_mul_f32 v[148:149], v[148:149], s[30:31] op_sel_hi:[1,0]
	v_pk_mul_f32 v[150:151], v[150:151], s[30:31] op_sel_hi:[1,0]
	v_pk_mul_f32 v[152:153], v[152:153], s[30:31] op_sel_hi:[1,0]
	v_pk_mul_f32 v[154:155], v[154:155], s[30:31] op_sel_hi:[1,0]
	v_pk_mul_f32 v[156:157], v[156:157], s[30:31] op_sel_hi:[1,0]
	v_pk_mul_f32 v[158:159], v[158:159], s[30:31] op_sel_hi:[1,0]
	v_pk_mul_f32 v[160:161], v[160:161], s[30:31] op_sel_hi:[1,0]
	v_pk_mul_f32 v[162:163], v[162:163], s[30:31] op_sel_hi:[1,0]
	v_pk_mul_f32 v[164:165], v[164:165], s[30:31] op_sel_hi:[1,0]
	v_pk_mul_f32 v[166:167], v[166:167], s[30:31] op_sel_hi:[1,0]
	v_pk_mul_f32 v[168:169], v[168:169], s[30:31] op_sel_hi:[1,0]
	v_pk_mul_f32 v[170:171], v[170:171], s[30:31] op_sel_hi:[1,0]
	v_pk_mul_f32 v[172:173], v[172:173], s[30:31] op_sel_hi:[1,0]
	v_pk_mul_f32 v[174:175], v[174:175], s[30:31] op_sel_hi:[1,0]
	v_pk_mul_f32 v[176:177], v[176:177], s[30:31] op_sel_hi:[1,0]
	v_pk_mul_f32 v[178:179], v[178:179], s[30:31] op_sel_hi:[1,0]
	v_pk_mul_f32 v[180:181], v[180:181], s[30:31] op_sel_hi:[1,0]
	v_pk_mul_f32 v[182:183], v[182:183], s[30:31] op_sel_hi:[1,0]
	v_pk_mul_f32 v[184:185], v[184:185], s[30:31] op_sel_hi:[1,0]
	v_pk_mul_f32 v[186:187], v[186:187], s[30:31] op_sel_hi:[1,0]
	v_pk_mul_f32 v[188:189], v[188:189], s[30:31] op_sel_hi:[1,0]
	v_pk_mul_f32 v[190:191], v[190:191], s[30:31] op_sel_hi:[1,0]
	v_pk_mul_f32 v[192:193], v[192:193], s[30:31] op_sel_hi:[1,0]
	v_med3_f32 v130, v130, s24, v237
	v_med3_f32 v131, v131, s24, v237
	v_med3_f32 v132, v132, s24, v237
	v_med3_f32 v133, v133, s24, v237
	v_med3_f32 v134, v134, s24, v237
	v_med3_f32 v135, v135, s24, v237
	v_med3_f32 v136, v136, s24, v237
	v_med3_f32 v137, v137, s24, v237
	v_med3_f32 v138, v138, s24, v237
	v_med3_f32 v139, v139, s24, v237
	v_med3_f32 v140, v140, s24, v237
	v_med3_f32 v141, v141, s24, v237
	v_med3_f32 v142, v142, s24, v237
	v_med3_f32 v143, v143, s24, v237
	v_med3_f32 v144, v144, s24, v237
	v_med3_f32 v145, v145, s24, v237
	v_med3_f32 v146, v146, s24, v237
	v_med3_f32 v147, v147, s24, v237
	v_med3_f32 v148, v148, s24, v237
	v_med3_f32 v149, v149, s24, v237
	v_med3_f32 v150, v150, s24, v237
	v_med3_f32 v151, v151, s24, v237
	v_med3_f32 v152, v152, s24, v237
	v_med3_f32 v153, v153, s24, v237
	v_med3_f32 v154, v154, s24, v237
	v_med3_f32 v155, v155, s24, v237
	v_med3_f32 v156, v156, s24, v237
	v_med3_f32 v157, v157, s24, v237
	v_med3_f32 v158, v158, s24, v237
	v_med3_f32 v159, v159, s24, v237
	v_med3_f32 v160, v160, s24, v237
	v_med3_f32 v161, v161, s24, v237
	v_med3_f32 v162, v162, s24, v237
	v_med3_f32 v163, v163, s24, v237
	v_med3_f32 v164, v164, s24, v237
	v_med3_f32 v165, v165, s24, v237
	v_med3_f32 v166, v166, s24, v237
	v_med3_f32 v167, v167, s24, v237
	v_med3_f32 v168, v168, s24, v237
	v_med3_f32 v169, v169, s24, v237
	v_med3_f32 v170, v170, s24, v237
	v_med3_f32 v171, v171, s24, v237
	v_med3_f32 v172, v172, s24, v237
	v_med3_f32 v173, v173, s24, v237
	v_med3_f32 v174, v174, s24, v237
	v_med3_f32 v175, v175, s24, v237
	v_med3_f32 v176, v176, s24, v237
	v_med3_f32 v177, v177, s24, v237
	v_med3_f32 v178, v178, s24, v237
	v_med3_f32 v179, v179, s24, v237
	v_med3_f32 v180, v180, s24, v237
	v_med3_f32 v181, v181, s24, v237
	v_med3_f32 v182, v182, s24, v237
	v_med3_f32 v183, v183, s24, v237
	v_med3_f32 v184, v184, s24, v237
	v_med3_f32 v185, v185, s24, v237
	v_med3_f32 v186, v186, s24, v237
	v_med3_f32 v187, v187, s24, v237
	v_med3_f32 v188, v188, s24, v237
	v_med3_f32 v189, v189, s24, v237
	v_med3_f32 v190, v190, s24, v237
	v_med3_f32 v191, v191, s24, v237
	v_med3_f32 v192, v192, s24, v237
	v_med3_f32 v193, v193, s24, v237
	v_cvt_pk_fp8_f32 v130, v130, v134
	v_cvt_pk_fp8_f32 v130, v138, v142 op_sel:[0,0,1]
	v_cvt_pk_fp8_f32 v134, v131, v135
	v_cvt_pk_fp8_f32 v134, v139, v143 op_sel:[0,0,1]
	v_cvt_pk_fp8_f32 v138, v132, v136
	v_cvt_pk_fp8_f32 v138, v140, v144 op_sel:[0,0,1]
	v_cvt_pk_fp8_f32 v142, v133, v137
	v_cvt_pk_fp8_f32 v142, v141, v145 op_sel:[0,0,1]
	v_cvt_pk_fp8_f32 v131, v146, v150
	v_cvt_pk_fp8_f32 v131, v154, v158 op_sel:[0,0,1]
	v_cvt_pk_fp8_f32 v135, v147, v151
	v_cvt_pk_fp8_f32 v135, v155, v159 op_sel:[0,0,1]
	v_cvt_pk_fp8_f32 v139, v148, v152
	v_cvt_pk_fp8_f32 v139, v156, v160 op_sel:[0,0,1]
	v_cvt_pk_fp8_f32 v143, v149, v153
	v_cvt_pk_fp8_f32 v143, v157, v161 op_sel:[0,0,1]
	v_cvt_pk_fp8_f32 v132, v162, v166
	v_cvt_pk_fp8_f32 v132, v170, v174 op_sel:[0,0,1]
	v_cvt_pk_fp8_f32 v136, v163, v167
	v_cvt_pk_fp8_f32 v136, v171, v175 op_sel:[0,0,1]
	v_cvt_pk_fp8_f32 v140, v164, v168
	v_cvt_pk_fp8_f32 v140, v172, v176 op_sel:[0,0,1]
	v_cvt_pk_fp8_f32 v144, v165, v169
	v_cvt_pk_fp8_f32 v144, v173, v177 op_sel:[0,0,1]
	v_cvt_pk_fp8_f32 v133, v178, v182
	v_cvt_pk_fp8_f32 v133, v186, v190 op_sel:[0,0,1]
	v_cvt_pk_fp8_f32 v137, v179, v183
	v_cvt_pk_fp8_f32 v137, v187, v191 op_sel:[0,0,1]
	v_cvt_pk_fp8_f32 v141, v180, v184
	v_cvt_pk_fp8_f32 v141, v188, v192 op_sel:[0,0,1]
	v_cvt_pk_fp8_f32 v145, v181, v185
	v_cvt_pk_fp8_f32 v145, v189, v193 op_sel:[0,0,1]
	global_store_dwordx4 v250, v[130:133], s[42:43] nt
	global_store_dwordx4 v250, v[134:137], s[42:43] offset:2048 nt
	global_store_dwordx4 v251, v[138:141], s[42:43] nt
	global_store_dwordx4 v251, v[142:145], s[42:43] offset:2048 nt
	s_add_u32 s42, s42, 0x10000
	s_addc_u32 s43, s43, 0
	global_load_dwordx4 v[130:133], v246, s[4:5] offset:1408 nt
	global_load_dwordx4 v[134:137], v247, s[4:5] offset:1408 nt
	global_load_dwordx4 v[138:141], v248, s[4:5] offset:1408 nt
	global_load_dwordx4 v[142:145], v249, s[4:5] offset:1408 nt
	global_load_dwordx4 v[146:149], v246, s[6:7] offset:1408 nt
	global_load_dwordx4 v[150:153], v247, s[6:7] offset:1408 nt
	global_load_dwordx4 v[154:157], v248, s[6:7] offset:1408 nt
	global_load_dwordx4 v[158:161], v249, s[6:7] offset:1408 nt
	global_load_dwordx4 v[162:165], v246, s[8:9] offset:1408 nt
	global_load_dwordx4 v[166:169], v247, s[8:9] offset:1408 nt
	global_load_dwordx4 v[170:173], v248, s[8:9] offset:1408 nt
	global_load_dwordx4 v[174:177], v249, s[8:9] offset:1408 nt
	global_load_dwordx4 v[178:181], v246, s[38:39] offset:1408 nt
	global_load_dwordx4 v[182:185], v247, s[38:39] offset:1408 nt
	global_load_dwordx4 v[186:189], v248, s[38:39] offset:1408 nt
	global_load_dwordx4 v[190:193], v249, s[38:39] offset:1408 nt
	s_waitcnt vmcnt(40)
; #define GAS __attribute__((address_space(1)))
; template <bool GAIN, bool NT = false> __device__ __forceinline__ void titem8_load(const TItem& d, int lane, f32x4 (&r)[16], f32x4 (&g)[4]) {
;     const int q = lane & 7, kg = lane >> 3; const unsigned lo = (unsigned)((16 * kg) * d.N + 4 * q) * 4u;
;     const GAS char* base = (const GAS char*)d.src;
; #pragma unroll
;     for (int j = 0; j < 16; ++j) { const GAS f32x4* p = (const GAS f32x4*)(base + (size_t)j * (size_t)d.N * 4 + lo); r[j] = NT ? __builtin_nontemporal_load(p) : *p; }
;     if constexpr (GAIN) { const GAS char* gb = (const GAS char*)d.gain; const unsigned go = (unsigned)(16 * kg) * 4u;
; #pragma unroll
;         for (int j4 = 0; j4 < 4; ++j4) g[j4] = *(const GAS f32x4*)(gb + 16 * j4 + go); }
;     asm volatile("" ::: "memory"); __builtin_amdgcn_sched_barrier(0);
; template <bool GAIN, bool NT = false> __device__ __forceinline__ void titem8_store(const TItem& d, int lane, const f32x4 (&r)[16], const f32x4 (&g)[4]) {
;     const int q = lane & 7, kg = lane >> 3; const unsigned lo = (unsigned)((4 * q) * d.ldk + 16 * kg);
;     GAS char* base = (GAS char*)d.dst;
;     f32x4 s[16];
; #pragma unroll
;     for (int j = 0; j < 16; ++j) s[j] = r[j] * ((GAIN ? g[j >> 2][j & 3] : 1.0f) * W8_SCALE);
; #pragma unroll
;     for (int i = 0; i < 4; ++i) { v4u w;
;         w.x = pk4_fp8w(s[0][i], s[1][i], s[2][i], s[3][i]); w.y = pk4_fp8w(s[4][i], s[5][i], s[6][i], s[7][i]);
;         w.z = pk4_fp8w(s[8][i], s[9][i], s[10][i], s[11][i]); w.w = pk4_fp8w(s[12][i], s[13][i], s[14][i], s[15][i]);
;         GAS v4u* p = (GAS v4u*)(base + (size_t)i * (size_t)d.ldk + lo);
;         if (NT) __builtin_nontemporal_store(w, p); else *p = w; }
; }
	v_pk_mul_f32 v[0:1], v[0:1], s[30:31] op_sel_hi:[1,0]
	v_pk_mul_f32 v[2:3], v[2:3], s[30:31] op_sel_hi:[1,0]
	v_pk_mul_f32 v[4:5], v[4:5], s[30:31] op_sel_hi:[1,0]
	v_pk_mul_f32 v[6:7], v[6:7], s[30:31] op_sel_hi:[1,0]
	v_pk_mul_f32 v[8:9], v[8:9], s[30:31] op_sel_hi:[1,0]
	v_pk_mul_f32 v[10:11], v[10:11], s[30:31] op_sel_hi:[1,0]
	v_pk_mul_f32 v[12:13], v[12:13], s[30:31] op_sel_hi:[1,0]
	v_pk_mul_f32 v[14:15], v[14:15], s[30:31] op_sel_hi:[1,0]
	v_pk_mul_f32 v[16:17], v[16:17], s[30:31] op_sel_hi:[1,0]
	v_pk_mul_f32 v[18:19], v[18:19], s[30:31] op_sel_hi:[1,0]
	v_pk_mul_f32 v[20:21], v[20:21], s[30:31] op_sel_hi:[1,0]
	v_pk_mul_f32 v[22:23], v[22:23], s[30:31] op_sel_hi:[1,0]
	v_pk_mul_f32 v[24:25], v[24:25], s[30:31] op_sel_hi:[1,0]
	v_pk_mul_f32 v[26:27], v[26:27], s[30:31] op_sel_hi:[1,0]
	v_pk_mul_f32 v[28:29], v[28:29], s[30:31] op_sel_hi:[1,0]
	v_pk_mul_f32 v[30:31], v[30:31], s[30:31] op_sel_hi:[1,0]
	v_pk_mul_f32 v[32:33], v[32:33], s[30:31] op_sel_hi:[1,0]
	v_pk_mul_f32 v[34:35], v[34:35], s[30:31] op_sel_hi:[1,0]
	v_pk_mul_f32 v[36:37], v[36:37], s[30:31] op_sel_hi:[1,0]
	v_pk_mul_f32 v[38:39], v[38:39], s[30:31] op_sel_hi:[1,0]
	v_pk_mul_f32 v[40:41], v[40:41], s[30:31] op_sel_hi:[1,0]
	v_pk_mul_f32 v[42:43], v[42:43], s[30:31] op_sel_hi:[1,0]
	v_pk_mul_f32 v[44:45], v[44:45], s[30:31] op_sel_hi:[1,0]
	v_pk_mul_f32 v[46:47], v[46:47], s[30:31] op_sel_hi:[1,0]
	v_pk_mul_f32 v[48:49], v[48:49], s[30:31] op_sel_hi:[1,0]
	v_pk_mul_f32 v[50:51], v[50:51], s[30:31] op_sel_hi:[1,0]
	v_pk_mul_f32 v[52:53], v[52:53], s[30:31] op_sel_hi:[1,0]
	v_pk_mul_f32 v[54:55], v[54:55], s[30:31] op_sel_hi:[1,0]
	v_pk_mul_f32 v[56:57], v[56:57], s[30:31] op_sel_hi:[1,0]
	v_pk_mul_f32 v[58:59], v[58:59], s[30:31] op_sel_hi:[1,0]
	v_pk_mul_f32 v[60:61], v[60:61], s[30:31] op_sel_hi:[1,0]
	v_pk_mul_f32 v[62:63], v[62:63], s[30:31] op_sel_hi:[1,0]
	v_med3_f32 v0, v0, s24, v237
	v_med3_f32 v1, v1, s24, v237
	v_med3_f32 v2, v2, s24, v237
	v_med3_f32 v3, v3, s24, v237
	v_med3_f32 v4, v4, s24, v237
	v_med3_f32 v5, v5, s24, v237
	v_med3_f32 v6, v6, s24, v237
	v_med3_f32 v7, v7, s24, v237
	v_med3_f32 v8, v8, s24, v237
	v_med3_f32 v9, v9, s24, v237
	v_med3_f32 v10, v10, s24, v237
	v_med3_f32 v11, v11, s24, v237
	v_med3_f32 v12, v12, s24, v237
	v_med3_f32 v13, v13, s24, v237
	v_med3_f32 v14, v14, s24, v237
	v_med3_f32 v15, v15, s24, v237
	v_med3_f32 v16, v16, s24, v237
	v_med3_f32 v17, v17, s24, v237
	v_med3_f32 v18, v18, s24, v237
	v_med3_f32 v19, v19, s24, v237
	v_med3_f32 v20, v20, s24, v237
	v_med3_f32 v21, v21, s24, v237
	v_med3_f32 v22, v22, s24, v237
	v_med3_f32 v23, v23, s24, v237
	v_med3_f32 v24, v24, s24, v237
	v_med3_f32 v25, v25, s24, v237
	v_med3_f32 v26, v26, s24, v237
	v_med3_f32 v27, v27, s24, v237
	v_med3_f32 v28, v28, s24, v237
	v_med3_f32 v29, v29, s24, v237
	v_med3_f32 v30, v30, s24, v237
	v_med3_f32 v31, v31, s24, v237
	v_med3_f32 v32, v32, s24, v237
	v_med3_f32 v33, v33, s24, v237
	v_med3_f32 v34, v34, s24, v237
	v_med3_f32 v35, v35, s24, v237
	v_med3_f32 v36, v36, s24, v237
	v_med3_f32 v37, v37, s24, v237
	v_med3_f32 v38, v38, s24, v237
	v_med3_f32 v39, v39, s24, v237
	v_med3_f32 v40, v40, s24, v237
	v_med3_f32 v41, v41, s24, v237
	v_med3_f32 v42, v42, s24, v237
	v_med3_f32 v43, v43, s24, v237
	v_med3_f32 v44, v44, s24, v237
	v_med3_f32 v45, v45, s24, v237
	v_med3_f32 v46, v46, s24, v237
	v_med3_f32 v47, v47, s24, v237
	v_med3_f32 v48, v48, s24, v237
	v_med3_f32 v49, v49, s24, v237
	v_med3_f32 v50, v50, s24, v237
	v_med3_f32 v51, v51, s24, v237
	v_med3_f32 v52, v52, s24, v237
	v_med3_f32 v53, v53, s24, v237
	v_med3_f32 v54, v54, s24, v237
	v_med3_f32 v55, v55, s24, v237
	v_med3_f32 v56, v56, s24, v237
	v_med3_f32 v57, v57, s24, v237
	v_med3_f32 v58, v58, s24, v237
	v_med3_f32 v59, v59, s24, v237
	v_med3_f32 v60, v60, s24, v237
	v_med3_f32 v61, v61, s24, v237
	v_med3_f32 v62, v62, s24, v237
	v_med3_f32 v63, v63, s24, v237
	v_cvt_pk_fp8_f32 v0, v0, v4
	v_cvt_pk_fp8_f32 v0, v8, v12 op_sel:[0,0,1]
	v_cvt_pk_fp8_f32 v4, v1, v5
	v_cvt_pk_fp8_f32 v4, v9, v13 op_sel:[0,0,1]
	v_cvt_pk_fp8_f32 v8, v2, v6
	v_cvt_pk_fp8_f32 v8, v10, v14 op_sel:[0,0,1]
	v_cvt_pk_fp8_f32 v12, v3, v7
	v_cvt_pk_fp8_f32 v12, v11, v15 op_sel:[0,0,1]
	v_cvt_pk_fp8_f32 v1, v16, v20
	v_cvt_pk_fp8_f32 v1, v24, v28 op_sel:[0,0,1]
	v_cvt_pk_fp8_f32 v5, v17, v21
	v_cvt_pk_fp8_f32 v5, v25, v29 op_sel:[0,0,1]
	v_cvt_pk_fp8_f32 v9, v18, v22
	v_cvt_pk_fp8_f32 v9, v26, v30 op_sel:[0,0,1]
	v_cvt_pk_fp8_f32 v13, v19, v23
	v_cvt_pk_fp8_f32 v13, v27, v31 op_sel:[0,0,1]
	v_cvt_pk_fp8_f32 v2, v32, v36
	v_cvt_pk_fp8_f32 v2, v40, v44 op_sel:[0,0,1]
	v_cvt_pk_fp8_f32 v6, v33, v37
	v_cvt_pk_fp8_f32 v6, v41, v45 op_sel:[0,0,1]
	v_cvt_pk_fp8_f32 v10, v34, v38
	v_cvt_pk_fp8_f32 v10, v42, v46 op_sel:[0,0,1]
	v_cvt_pk_fp8_f32 v14, v35, v39
	v_cvt_pk_fp8_f32 v14, v43, v47 op_sel:[0,0,1]
	v_cvt_pk_fp8_f32 v3, v48, v52
	v_cvt_pk_fp8_f32 v3, v56, v60 op_sel:[0,0,1]
	v_cvt_pk_fp8_f32 v7, v49, v53
	v_cvt_pk_fp8_f32 v7, v57, v61 op_sel:[0,0,1]
	v_cvt_pk_fp8_f32 v11, v50, v54
	v_cvt_pk_fp8_f32 v11, v58, v62 op_sel:[0,0,1]
	v_cvt_pk_fp8_f32 v15, v51, v55
	v_cvt_pk_fp8_f32 v15, v59, v63 op_sel:[0,0,1]
	global_store_dwordx4 v250, v[0:3], s[42:43] nt
	global_store_dwordx4 v250, v[4:7], s[42:43] offset:2048 nt
	global_store_dwordx4 v251, v[8:11], s[42:43] nt
	global_store_dwordx4 v251, v[12:15], s[42:43] offset:2048 nt
	s_add_u32 s42, s42, 0x10000
	s_addc_u32 s43, s43, 0
	global_load_dwordx4 v[0:3], v246, s[4:5] offset:1536 nt
	global_load_dwordx4 v[4:7], v247, s[4:5] offset:1536 nt
	global_load_dwordx4 v[8:11], v248, s[4:5] offset:1536 nt
	global_load_dwordx4 v[12:15], v249, s[4:5] offset:1536 nt
	global_load_dwordx4 v[16:19], v246, s[6:7] offset:1536 nt
	global_load_dwordx4 v[20:23], v247, s[6:7] offset:1536 nt
	global_load_dwordx4 v[24:27], v248, s[6:7] offset:1536 nt
	global_load_dwordx4 v[28:31], v249, s[6:7] offset:1536 nt
	global_load_dwordx4 v[32:35], v246, s[8:9] offset:1536 nt
	global_load_dwordx4 v[36:39], v247, s[8:9] offset:1536 nt
	global_load_dwordx4 v[40:43], v248, s[8:9] offset:1536 nt
	global_load_dwordx4 v[44:47], v249, s[8:9] offset:1536 nt
	global_load_dwordx4 v[48:51], v246, s[38:39] offset:1536 nt
	global_load_dwordx4 v[52:55], v247, s[38:39] offset:1536 nt
	global_load_dwordx4 v[56:59], v248, s[38:39] offset:1536 nt
	global_load_dwordx4 v[60:63], v249, s[38:39] offset:1536 nt
	s_waitcnt vmcnt(40)
; #define GAS __attribute__((address_space(1)))
; template <bool GAIN, bool NT = false> __device__ __forceinline__ void titem8_load(const TItem& d, int lane, f32x4 (&r)[16], f32x4 (&g)[4]) {
;     const int q = lane & 7, kg = lane >> 3; const unsigned lo = (unsigned)((16 * kg) * d.N + 4 * q) * 4u;
;     const GAS char* base = (const GAS char*)d.src;
; #pragma unroll
;     for (int j = 0; j < 16; ++j) { const GAS f32x4* p = (const GAS f32x4*)(base + (size_t)j * (size_t)d.N * 4 + lo); r[j] = NT ? __builtin_nontemporal_load(p) : *p; }
;     if constexpr (GAIN) { const GAS char* gb = (const GAS char*)d.gain; const unsigned go = (unsigned)(16 * kg) * 4u;
; #pragma unroll
;         for (int j4 = 0; j4 < 4; ++j4) g[j4] = *(const GAS f32x4*)(gb + 16 * j4 + go); }
;     asm volatile("" ::: "memory"); __builtin_amdgcn_sched_barrier(0);
; template <bool GAIN, bool NT = false> __device__ __forceinline__ void titem8_store(const TItem& d, int lane, const f32x4 (&r)[16], const f32x4 (&g)[4]) {
;     const int q = lane & 7, kg = lane >> 3; const unsigned lo = (unsigned)((4 * q) * d.ldk + 16 * kg);
;     GAS char* base = (GAS char*)d.dst;
;     f32x4 s[16];
; #pragma unroll
;     for (int j = 0; j < 16; ++j) s[j] = r[j] * ((GAIN ? g[j >> 2][j & 3] : 1.0f) * W8_SCALE);
; #pragma unroll
;     for (int i = 0; i < 4; ++i) { v4u w;
;         w.x = pk4_fp8w(s[0][i], s[1][i], s[2][i], s[3][i]); w.y = pk4_fp8w(s[4][i], s[5][i], s[6][i], s[7][i]);
;         w.z = pk4_fp8w(s[8][i], s[9][i], s[10][i], s[11][i]); w.w = pk4_fp8w(s[12][i], s[13][i], s[14][i], s[15][i]);
;         GAS v4u* p = (GAS v4u*)(base + (size_t)i * (size_t)d.ldk + lo);
;         if (NT) __builtin_nontemporal_store(w, p); else *p = w; }
; }
	v_pk_mul_f32 v[66:67], v[66:67], s[30:31] op_sel_hi:[1,0]
	v_pk_mul_f32 v[68:69], v[68:69], s[30:31] op_sel_hi:[1,0]
	v_pk_mul_f32 v[70:71], v[70:71], s[30:31] op_sel_hi:[1,0]
	v_pk_mul_f32 v[72:73], v[72:73], s[30:31] op_sel_hi:[1,0]
	v_pk_mul_f32 v[74:75], v[74:75], s[30:31] op_sel_hi:[1,0]
	v_pk_mul_f32 v[76:77], v[76:77], s[30:31] op_sel_hi:[1,0]
	v_pk_mul_f32 v[78:79], v[78:79], s[30:31] op_sel_hi:[1,0]
	v_pk_mul_f32 v[80:81], v[80:81], s[30:31] op_sel_hi:[1,0]
	v_pk_mul_f32 v[82:83], v[82:83], s[30:31] op_sel_hi:[1,0]
	v_pk_mul_f32 v[84:85], v[84:85], s[30:31] op_sel_hi:[1,0]
	v_pk_mul_f32 v[86:87], v[86:87], s[30:31] op_sel_hi:[1,0]
	v_pk_mul_f32 v[88:89], v[88:89], s[30:31] op_sel_hi:[1,0]
	v_pk_mul_f32 v[90:91], v[90:91], s[30:31] op_sel_hi:[1,0]
	v_pk_mul_f32 v[92:93], v[92:93], s[30:31] op_sel_hi:[1,0]
	v_pk_mul_f32 v[94:95], v[94:95], s[30:31] op_sel_hi:[1,0]
	v_pk_mul_f32 v[96:97], v[96:97], s[30:31] op_sel_hi:[1,0]
	v_pk_mul_f32 v[98:99], v[98:99], s[30:31] op_sel_hi:[1,0]
	v_pk_mul_f32 v[100:101], v[100:101], s[30:31] op_sel_hi:[1,0]
	v_pk_mul_f32 v[102:103], v[102:103], s[30:31] op_sel_hi:[1,0]
	v_pk_mul_f32 v[104:105], v[104:105], s[30:31] op_sel_hi:[1,0]
	v_pk_mul_f32 v[106:107], v[106:107], s[30:31] op_sel_hi:[1,0]
	v_pk_mul_f32 v[108:109], v[108:109], s[30:31] op_sel_hi:[1,0]
	v_pk_mul_f32 v[110:111], v[110:111], s[30:31] op_sel_hi:[1,0]
	v_pk_mul_f32 v[112:113], v[112:113], s[30:31] op_sel_hi:[1,0]
	v_pk_mul_f32 v[114:115], v[114:115], s[30:31] op_sel_hi:[1,0]
	v_pk_mul_f32 v[116:117], v[116:117], s[30:31] op_sel_hi:[1,0]
	v_pk_mul_f32 v[118:119], v[118:119], s[30:31] op_sel_hi:[1,0]
	v_pk_mul_f32 v[120:121], v[120:121], s[30:31] op_sel_hi:[1,0]
	v_pk_mul_f32 v[122:123], v[122:123], s[30:31] op_sel_hi:[1,0]
	v_pk_mul_f32 v[124:125], v[124:125], s[30:31] op_sel_hi:[1,0]
	v_pk_mul_f32 v[126:127], v[126:127], s[30:31] op_sel_hi:[1,0]
	v_pk_mul_f32 v[128:129], v[128:129], s[30:31] op_sel_hi:[1,0]
	v_med3_f32 v66, v66, s24, v237
	v_med3_f32 v67, v67, s24, v237
	v_med3_f32 v68, v68, s24, v237
	v_med3_f32 v69, v69, s24, v237
	v_med3_f32 v70, v70, s24, v237
	v_med3_f32 v71, v71, s24, v237
	v_med3_f32 v72, v72, s24, v237
	v_med3_f32 v73, v73, s24, v237
	v_med3_f32 v74, v74, s24, v237
	v_med3_f32 v75, v75, s24, v237
	v_med3_f32 v76, v76, s24, v237
	v_med3_f32 v77, v77, s24, v237
	v_med3_f32 v78, v78, s24, v237
	v_med3_f32 v79, v79, s24, v237
	v_med3_f32 v80, v80, s24, v237
	v_med3_f32 v81, v81, s24, v237
	v_med3_f32 v82, v82, s24, v237
	v_med3_f32 v83, v83, s24, v237
	v_med3_f32 v84, v84, s24, v237
	v_med3_f32 v85, v85, s24, v237
	v_med3_f32 v86, v86, s24, v237
	v_med3_f32 v87, v87, s24, v237
	v_med3_f32 v88, v88, s24, v237
	v_med3_f32 v89, v89, s24, v237
	v_med3_f32 v90, v90, s24, v237
	v_med3_f32 v91, v91, s24, v237
	v_med3_f32 v92, v92, s24, v237
	v_med3_f32 v93, v93, s24, v237
	v_med3_f32 v94, v94, s24, v237
	v_med3_f32 v95, v95, s24, v237
	v_med3_f32 v96, v96, s24, v237
	v_med3_f32 v97, v97, s24, v237
	v_med3_f32 v98, v98, s24, v237
	v_med3_f32 v99, v99, s24, v237
	v_med3_f32 v100, v100, s24, v237
	v_med3_f32 v101, v101, s24, v237
	v_med3_f32 v102, v102, s24, v237
	v_med3_f32 v103, v103, s24, v237
	v_med3_f32 v104, v104, s24, v237
	v_med3_f32 v105, v105, s24, v237
	v_med3_f32 v106, v106, s24, v237
	v_med3_f32 v107, v107, s24, v237
	v_med3_f32 v108, v108, s24, v237
	v_med3_f32 v109, v109, s24, v237
	v_med3_f32 v110, v110, s24, v237
	v_med3_f32 v111, v111, s24, v237
	v_med3_f32 v112, v112, s24, v237
	v_med3_f32 v113, v113, s24, v237
	v_med3_f32 v114, v114, s24, v237
	v_med3_f32 v115, v115, s24, v237
	v_med3_f32 v116, v116, s24, v237
	v_med3_f32 v117, v117, s24, v237
	v_med3_f32 v118, v118, s24, v237
	v_med3_f32 v119, v119, s24, v237
	v_med3_f32 v120, v120, s24, v237
	v_med3_f32 v121, v121, s24, v237
	v_med3_f32 v122, v122, s24, v237
	v_med3_f32 v123, v123, s24, v237
	v_med3_f32 v124, v124, s24, v237
	v_med3_f32 v125, v125, s24, v237
	v_med3_f32 v126, v126, s24, v237
	v_med3_f32 v127, v127, s24, v237
	v_med3_f32 v128, v128, s24, v237
	v_med3_f32 v129, v129, s24, v237
	v_cvt_pk_fp8_f32 v66, v66, v70
	v_cvt_pk_fp8_f32 v66, v74, v78 op_sel:[0,0,1]
	v_cvt_pk_fp8_f32 v70, v67, v71
	v_cvt_pk_fp8_f32 v70, v75, v79 op_sel:[0,0,1]
	v_cvt_pk_fp8_f32 v74, v68, v72
	v_cvt_pk_fp8_f32 v74, v76, v80 op_sel:[0,0,1]
	v_cvt_pk_fp8_f32 v78, v69, v73
	v_cvt_pk_fp8_f32 v78, v77, v81 op_sel:[0,0,1]
	v_cvt_pk_fp8_f32 v67, v82, v86
	v_cvt_pk_fp8_f32 v67, v90, v94 op_sel:[0,0,1]
	v_cvt_pk_fp8_f32 v71, v83, v87
	v_cvt_pk_fp8_f32 v71, v91, v95 op_sel:[0,0,1]
	v_cvt_pk_fp8_f32 v75, v84, v88
	v_cvt_pk_fp8_f32 v75, v92, v96 op_sel:[0,0,1]
	v_cvt_pk_fp8_f32 v79, v85, v89
	v_cvt_pk_fp8_f32 v79, v93, v97 op_sel:[0,0,1]
	v_cvt_pk_fp8_f32 v68, v98, v102
	v_cvt_pk_fp8_f32 v68, v106, v110 op_sel:[0,0,1]
	v_cvt_pk_fp8_f32 v72, v99, v103
	v_cvt_pk_fp8_f32 v72, v107, v111 op_sel:[0,0,1]
	v_cvt_pk_fp8_f32 v76, v100, v104
	v_cvt_pk_fp8_f32 v76, v108, v112 op_sel:[0,0,1]
	v_cvt_pk_fp8_f32 v80, v101, v105
	v_cvt_pk_fp8_f32 v80, v109, v113 op_sel:[0,0,1]
	v_cvt_pk_fp8_f32 v69, v114, v118
	v_cvt_pk_fp8_f32 v69, v122, v126 op_sel:[0,0,1]
	v_cvt_pk_fp8_f32 v73, v115, v119
	v_cvt_pk_fp8_f32 v73, v123, v127 op_sel:[0,0,1]
	v_cvt_pk_fp8_f32 v77, v116, v120
	v_cvt_pk_fp8_f32 v77, v124, v128 op_sel:[0,0,1]
	v_cvt_pk_fp8_f32 v81, v117, v121
	v_cvt_pk_fp8_f32 v81, v125, v129 op_sel:[0,0,1]
	global_store_dwordx4 v250, v[66:69], s[42:43] nt
	global_store_dwordx4 v250, v[70:73], s[42:43] offset:2048 nt
	global_store_dwordx4 v251, v[74:77], s[42:43] nt
	global_store_dwordx4 v251, v[78:81], s[42:43] offset:2048 nt
	s_add_u32 s42, s42, 0x10000
	s_addc_u32 s43, s43, 0
	global_load_dwordx4 v[66:69], v246, s[4:5] offset:1664 nt
	global_load_dwordx4 v[70:73], v247, s[4:5] offset:1664 nt
	global_load_dwordx4 v[74:77], v248, s[4:5] offset:1664 nt
	global_load_dwordx4 v[78:81], v249, s[4:5] offset:1664 nt
	global_load_dwordx4 v[82:85], v246, s[6:7] offset:1664 nt
	global_load_dwordx4 v[86:89], v247, s[6:7] offset:1664 nt
	global_load_dwordx4 v[90:93], v248, s[6:7] offset:1664 nt
	global_load_dwordx4 v[94:97], v249, s[6:7] offset:1664 nt
	global_load_dwordx4 v[98:101], v246, s[8:9] offset:1664 nt
	global_load_dwordx4 v[102:105], v247, s[8:9] offset:1664 nt
	global_load_dwordx4 v[106:109], v248, s[8:9] offset:1664 nt
	global_load_dwordx4 v[110:113], v249, s[8:9] offset:1664 nt
	global_load_dwordx4 v[114:117], v246, s[38:39] offset:1664 nt
	global_load_dwordx4 v[118:121], v247, s[38:39] offset:1664 nt
	global_load_dwordx4 v[122:125], v248, s[38:39] offset:1664 nt
	global_load_dwordx4 v[126:129], v249, s[38:39] offset:1664 nt
	s_waitcnt vmcnt(40)
; #define GAS __attribute__((address_space(1)))
; template <bool GAIN, bool NT = false> __device__ __forceinline__ void titem8_load(const TItem& d, int lane, f32x4 (&r)[16], f32x4 (&g)[4]) {
;     const int q = lane & 7, kg = lane >> 3; const unsigned lo = (unsigned)((16 * kg) * d.N + 4 * q) * 4u;
;     const GAS char* base = (const GAS char*)d.src;
; #pragma unroll
;     for (int j = 0; j < 16; ++j) { const GAS f32x4* p = (const GAS f32x4*)(base + (size_t)j * (size_t)d.N * 4 + lo); r[j] = NT ? __builtin_nontemporal_load(p) : *p; }
;     if constexpr (GAIN) { const GAS char* gb = (const GAS char*)d.gain; const unsigned go = (unsigned)(16 * kg) * 4u;
; #pragma unroll
;         for (int j4 = 0; j4 < 4; ++j4) g[j4] = *(const GAS f32x4*)(gb + 16 * j4 + go); }
;     asm volatile("" ::: "memory"); __builtin_amdgcn_sched_barrier(0);
; template <bool GAIN, bool NT = false> __device__ __forceinline__ void titem8_store(const TItem& d, int lane, const f32x4 (&r)[16], const f32x4 (&g)[4]) {
;     const int q = lane & 7, kg = lane >> 3; const unsigned lo = (unsigned)((4 * q) * d.ldk + 16 * kg);
;     GAS char* base = (GAS char*)d.dst;
;     f32x4 s[16];
; #pragma unroll
;     for (int j = 0; j < 16; ++j) s[j] = r[j] * ((GAIN ? g[j >> 2][j & 3] : 1.0f) * W8_SCALE);
; #pragma unroll
;     for (int i = 0; i < 4; ++i) { v4u w;
;         w.x = pk4_fp8w(s[0][i], s[1][i], s[2][i], s[3][i]); w.y = pk4_fp8w(s[4][i], s[5][i], s[6][i], s[7][i]);
;         w.z = pk4_fp8w(s[8][i], s[9][i], s[10][i], s[11][i]); w.w = pk4_fp8w(s[12][i], s[13][i], s[14][i], s[15][i]);
;         GAS v4u* p = (GAS v4u*)(base + (size_t)i * (size_t)d.ldk + lo);
;         if (NT) __builtin_nontemporal_store(w, p); else *p = w; }
; }
	v_pk_mul_f32 v[130:131], v[130:131], s[30:31] op_sel_hi:[1,0]
	v_pk_mul_f32 v[132:133], v[132:133], s[30:31] op_sel_hi:[1,0]
	v_pk_mul_f32 v[134:135], v[134:135], s[30:31] op_sel_hi:[1,0]
	v_pk_mul_f32 v[136:137], v[136:137], s[30:31] op_sel_hi:[1,0]
	v_pk_mul_f32 v[138:139], v[138:139], s[30:31] op_sel_hi:[1,0]
	v_pk_mul_f32 v[140:141], v[140:141], s[30:31] op_sel_hi:[1,0]
	v_pk_mul_f32 v[142:143], v[142:143], s[30:31] op_sel_hi:[1,0]
	v_pk_mul_f32 v[144:145], v[144:145], s[30:31] op_sel_hi:[1,0]
	v_pk_mul_f32 v[146:147], v[146:147], s[30:31] op_sel_hi:[1,0]
	v_pk_mul_f32 v[148:149], v[148:149], s[30:31] op_sel_hi:[1,0]
	v_pk_mul_f32 v[150:151], v[150:151], s[30:31] op_sel_hi:[1,0]
	v_pk_mul_f32 v[152:153], v[152:153], s[30:31] op_sel_hi:[1,0]
	v_pk_mul_f32 v[154:155], v[154:155], s[30:31] op_sel_hi:[1,0]
	v_pk_mul_f32 v[156:157], v[156:157], s[30:31] op_sel_hi:[1,0]
	v_pk_mul_f32 v[158:159], v[158:159], s[30:31] op_sel_hi:[1,0]
	v_pk_mul_f32 v[160:161], v[160:161], s[30:31] op_sel_hi:[1,0]
	v_pk_mul_f32 v[162:163], v[162:163], s[30:31] op_sel_hi:[1,0]
	v_pk_mul_f32 v[164:165], v[164:165], s[30:31] op_sel_hi:[1,0]
	v_pk_mul_f32 v[166:167], v[166:167], s[30:31] op_sel_hi:[1,0]
	v_pk_mul_f32 v[168:169], v[168:169], s[30:31] op_sel_hi:[1,0]
	v_pk_mul_f32 v[170:171], v[170:171], s[30:31] op_sel_hi:[1,0]
	v_pk_mul_f32 v[172:173], v[172:173], s[30:31] op_sel_hi:[1,0]
	v_pk_mul_f32 v[174:175], v[174:175], s[30:31] op_sel_hi:[1,0]
	v_pk_mul_f32 v[176:177], v[176:177], s[30:31] op_sel_hi:[1,0]
	v_pk_mul_f32 v[178:179], v[178:179], s[30:31] op_sel_hi:[1,0]
	v_pk_mul_f32 v[180:181], v[180:181], s[30:31] op_sel_hi:[1,0]
	v_pk_mul_f32 v[182:183], v[182:183], s[30:31] op_sel_hi:[1,0]
	v_pk_mul_f32 v[184:185], v[184:185], s[30:31] op_sel_hi:[1,0]
	v_pk_mul_f32 v[186:187], v[186:187], s[30:31] op_sel_hi:[1,0]
	v_pk_mul_f32 v[188:189], v[188:189], s[30:31] op_sel_hi:[1,0]
	v_pk_mul_f32 v[190:191], v[190:191], s[30:31] op_sel_hi:[1,0]
	v_pk_mul_f32 v[192:193], v[192:193], s[30:31] op_sel_hi:[1,0]
	v_med3_f32 v130, v130, s24, v237
	v_med3_f32 v131, v131, s24, v237
	v_med3_f32 v132, v132, s24, v237
	v_med3_f32 v133, v133, s24, v237
	v_med3_f32 v134, v134, s24, v237
	v_med3_f32 v135, v135, s24, v237
	v_med3_f32 v136, v136, s24, v237
	v_med3_f32 v137, v137, s24, v237
	v_med3_f32 v138, v138, s24, v237
	v_med3_f32 v139, v139, s24, v237
	v_med3_f32 v140, v140, s24, v237
	v_med3_f32 v141, v141, s24, v237
	v_med3_f32 v142, v142, s24, v237
	v_med3_f32 v143, v143, s24, v237
	v_med3_f32 v144, v144, s24, v237
	v_med3_f32 v145, v145, s24, v237
	v_med3_f32 v146, v146, s24, v237
	v_med3_f32 v147, v147, s24, v237
	v_med3_f32 v148, v148, s24, v237
	v_med3_f32 v149, v149, s24, v237
	v_med3_f32 v150, v150, s24, v237
	v_med3_f32 v151, v151, s24, v237
	v_med3_f32 v152, v152, s24, v237
	v_med3_f32 v153, v153, s24, v237
	v_med3_f32 v154, v154, s24, v237
	v_med3_f32 v155, v155, s24, v237
	v_med3_f32 v156, v156, s24, v237
	v_med3_f32 v157, v157, s24, v237
	v_med3_f32 v158, v158, s24, v237
	v_med3_f32 v159, v159, s24, v237
	v_med3_f32 v160, v160, s24, v237
	v_med3_f32 v161, v161, s24, v237
	v_med3_f32 v162, v162, s24, v237
	v_med3_f32 v163, v163, s24, v237
	v_med3_f32 v164, v164, s24, v237
	v_med3_f32 v165, v165, s24, v237
	v_med3_f32 v166, v166, s24, v237
	v_med3_f32 v167, v167, s24, v237
	v_med3_f32 v168, v168, s24, v237
	v_med3_f32 v169, v169, s24, v237
	v_med3_f32 v170, v170, s24, v237
	v_med3_f32 v171, v171, s24, v237
	v_med3_f32 v172, v172, s24, v237
	v_med3_f32 v173, v173, s24, v237
	v_med3_f32 v174, v174, s24, v237
	v_med3_f32 v175, v175, s24, v237
	v_med3_f32 v176, v176, s24, v237
	v_med3_f32 v177, v177, s24, v237
	v_med3_f32 v178, v178, s24, v237
	v_med3_f32 v179, v179, s24, v237
	v_med3_f32 v180, v180, s24, v237
	v_med3_f32 v181, v181, s24, v237
	v_med3_f32 v182, v182, s24, v237
	v_med3_f32 v183, v183, s24, v237
	v_med3_f32 v184, v184, s24, v237
	v_med3_f32 v185, v185, s24, v237
	v_med3_f32 v186, v186, s24, v237
	v_med3_f32 v187, v187, s24, v237
	v_med3_f32 v188, v188, s24, v237
	v_med3_f32 v189, v189, s24, v237
	v_med3_f32 v190, v190, s24, v237
	v_med3_f32 v191, v191, s24, v237
	v_med3_f32 v192, v192, s24, v237
	v_med3_f32 v193, v193, s24, v237
	v_cvt_pk_fp8_f32 v130, v130, v134
	v_cvt_pk_fp8_f32 v130, v138, v142 op_sel:[0,0,1]
	v_cvt_pk_fp8_f32 v134, v131, v135
	v_cvt_pk_fp8_f32 v134, v139, v143 op_sel:[0,0,1]
	v_cvt_pk_fp8_f32 v138, v132, v136
	v_cvt_pk_fp8_f32 v138, v140, v144 op_sel:[0,0,1]
	v_cvt_pk_fp8_f32 v142, v133, v137
	v_cvt_pk_fp8_f32 v142, v141, v145 op_sel:[0,0,1]
	v_cvt_pk_fp8_f32 v131, v146, v150
	v_cvt_pk_fp8_f32 v131, v154, v158 op_sel:[0,0,1]
	v_cvt_pk_fp8_f32 v135, v147, v151
	v_cvt_pk_fp8_f32 v135, v155, v159 op_sel:[0,0,1]
	v_cvt_pk_fp8_f32 v139, v148, v152
	v_cvt_pk_fp8_f32 v139, v156, v160 op_sel:[0,0,1]
	v_cvt_pk_fp8_f32 v143, v149, v153
	v_cvt_pk_fp8_f32 v143, v157, v161 op_sel:[0,0,1]
	v_cvt_pk_fp8_f32 v132, v162, v166
	v_cvt_pk_fp8_f32 v132, v170, v174 op_sel:[0,0,1]
	v_cvt_pk_fp8_f32 v136, v163, v167
	v_cvt_pk_fp8_f32 v136, v171, v175 op_sel:[0,0,1]
	v_cvt_pk_fp8_f32 v140, v164, v168
	v_cvt_pk_fp8_f32 v140, v172, v176 op_sel:[0,0,1]
	v_cvt_pk_fp8_f32 v144, v165, v169
	v_cvt_pk_fp8_f32 v144, v173, v177 op_sel:[0,0,1]
	v_cvt_pk_fp8_f32 v133, v178, v182
	v_cvt_pk_fp8_f32 v133, v186, v190 op_sel:[0,0,1]
	v_cvt_pk_fp8_f32 v137, v179, v183
	v_cvt_pk_fp8_f32 v137, v187, v191 op_sel:[0,0,1]
	v_cvt_pk_fp8_f32 v141, v180, v184
	v_cvt_pk_fp8_f32 v141, v188, v192 op_sel:[0,0,1]
	v_cvt_pk_fp8_f32 v145, v181, v185
	v_cvt_pk_fp8_f32 v145, v189, v193 op_sel:[0,0,1]
	global_store_dwordx4 v250, v[130:133], s[42:43] nt
	global_store_dwordx4 v250, v[134:137], s[42:43] offset:2048 nt
	global_store_dwordx4 v251, v[138:141], s[42:43] nt
	global_store_dwordx4 v251, v[142:145], s[42:43] offset:2048 nt
	s_add_u32 s42, s42, 0x10000
	s_addc_u32 s43, s43, 0
	global_load_dwordx4 v[130:133], v246, s[4:5] offset:1792 nt
	global_load_dwordx4 v[134:137], v247, s[4:5] offset:1792 nt
	global_load_dwordx4 v[138:141], v248, s[4:5] offset:1792 nt
	global_load_dwordx4 v[142:145], v249, s[4:5] offset:1792 nt
	global_load_dwordx4 v[146:149], v246, s[6:7] offset:1792 nt
	global_load_dwordx4 v[150:153], v247, s[6:7] offset:1792 nt
	global_load_dwordx4 v[154:157], v248, s[6:7] offset:1792 nt
	global_load_dwordx4 v[158:161], v249, s[6:7] offset:1792 nt
	global_load_dwordx4 v[162:165], v246, s[8:9] offset:1792 nt
	global_load_dwordx4 v[166:169], v247, s[8:9] offset:1792 nt
	global_load_dwordx4 v[170:173], v248, s[8:9] offset:1792 nt
	global_load_dwordx4 v[174:177], v249, s[8:9] offset:1792 nt
	global_load_dwordx4 v[178:181], v246, s[38:39] offset:1792 nt
	global_load_dwordx4 v[182:185], v247, s[38:39] offset:1792 nt
	global_load_dwordx4 v[186:189], v248, s[38:39] offset:1792 nt
	global_load_dwordx4 v[190:193], v249, s[38:39] offset:1792 nt
	s_waitcnt vmcnt(40)
; #define GAS __attribute__((address_space(1)))
; template <bool GAIN, bool NT = false> __device__ __forceinline__ void titem8_load(const TItem& d, int lane, f32x4 (&r)[16], f32x4 (&g)[4]) {
;     const int q = lane & 7, kg = lane >> 3; const unsigned lo = (unsigned)((16 * kg) * d.N + 4 * q) * 4u;
;     const GAS char* base = (const GAS char*)d.src;
; #pragma unroll
;     for (int j = 0; j < 16; ++j) { const GAS f32x4* p = (const GAS f32x4*)(base + (size_t)j * (size_t)d.N * 4 + lo); r[j] = NT ? __builtin_nontemporal_load(p) : *p; }
;     if constexpr (GAIN) { const GAS char* gb = (const GAS char*)d.gain; const unsigned go = (unsigned)(16 * kg) * 4u;
; #pragma unroll
;         for (int j4 = 0; j4 < 4; ++j4) g[j4] = *(const GAS f32x4*)(gb + 16 * j4 + go); }
;     asm volatile("" ::: "memory"); __builtin_amdgcn_sched_barrier(0);
; template <bool GAIN, bool NT = false> __device__ __forceinline__ void titem8_store(const TItem& d, int lane, const f32x4 (&r)[16], const f32x4 (&g)[4]) {
;     const int q = lane & 7, kg = lane >> 3; const unsigned lo = (unsigned)((4 * q) * d.ldk + 16 * kg);
;     GAS char* base = (GAS char*)d.dst;
;     f32x4 s[16];
; #pragma unroll
;     for (int j = 0; j < 16; ++j) s[j] = r[j] * ((GAIN ? g[j >> 2][j & 3] : 1.0f) * W8_SCALE);
; #pragma unroll
;     for (int i = 0; i < 4; ++i) { v4u w;
;         w.x = pk4_fp8w(s[0][i], s[1][i], s[2][i], s[3][i]); w.y = pk4_fp8w(s[4][i], s[5][i], s[6][i], s[7][i]);
;         w.z = pk4_fp8w(s[8][i], s[9][i], s[10][i], s[11][i]); w.w = pk4_fp8w(s[12][i], s[13][i], s[14][i], s[15][i]);
;         GAS v4u* p = (GAS v4u*)(base + (size_t)i * (size_t)d.ldk + lo);
;         if (NT) __builtin_nontemporal_store(w, p); else *p = w; }
; }
	v_pk_mul_f32 v[0:1], v[0:1], s[30:31] op_sel_hi:[1,0]
	v_pk_mul_f32 v[2:3], v[2:3], s[30:31] op_sel_hi:[1,0]
	v_pk_mul_f32 v[4:5], v[4:5], s[30:31] op_sel_hi:[1,0]
	v_pk_mul_f32 v[6:7], v[6:7], s[30:31] op_sel_hi:[1,0]
	v_pk_mul_f32 v[8:9], v[8:9], s[30:31] op_sel_hi:[1,0]
	v_pk_mul_f32 v[10:11], v[10:11], s[30:31] op_sel_hi:[1,0]
	v_pk_mul_f32 v[12:13], v[12:13], s[30:31] op_sel_hi:[1,0]
	v_pk_mul_f32 v[14:15], v[14:15], s[30:31] op_sel_hi:[1,0]
	v_pk_mul_f32 v[16:17], v[16:17], s[30:31] op_sel_hi:[1,0]
	v_pk_mul_f32 v[18:19], v[18:19], s[30:31] op_sel_hi:[1,0]
	v_pk_mul_f32 v[20:21], v[20:21], s[30:31] op_sel_hi:[1,0]
	v_pk_mul_f32 v[22:23], v[22:23], s[30:31] op_sel_hi:[1,0]
	v_pk_mul_f32 v[24:25], v[24:25], s[30:31] op_sel_hi:[1,0]
	v_pk_mul_f32 v[26:27], v[26:27], s[30:31] op_sel_hi:[1,0]
	v_pk_mul_f32 v[28:29], v[28:29], s[30:31] op_sel_hi:[1,0]
	v_pk_mul_f32 v[30:31], v[30:31], s[30:31] op_sel_hi:[1,0]
	v_pk_mul_f32 v[32:33], v[32:33], s[30:31] op_sel_hi:[1,0]
	v_pk_mul_f32 v[34:35], v[34:35], s[30:31] op_sel_hi:[1,0]
	v_pk_mul_f32 v[36:37], v[36:37], s[30:31] op_sel_hi:[1,0]
	v_pk_mul_f32 v[38:39], v[38:39], s[30:31] op_sel_hi:[1,0]
	v_pk_mul_f32 v[40:41], v[40:41], s[30:31] op_sel_hi:[1,0]
	v_pk_mul_f32 v[42:43], v[42:43], s[30:31] op_sel_hi:[1,0]
	v_pk_mul_f32 v[44:45], v[44:45], s[30:31] op_sel_hi:[1,0]
	v_pk_mul_f32 v[46:47], v[46:47], s[30:31] op_sel_hi:[1,0]
	v_pk_mul_f32 v[48:49], v[48:49], s[30:31] op_sel_hi:[1,0]
	v_pk_mul_f32 v[50:51], v[50:51], s[30:31] op_sel_hi:[1,0]
	v_pk_mul_f32 v[52:53], v[52:53], s[30:31] op_sel_hi:[1,0]
	v_pk_mul_f32 v[54:55], v[54:55], s[30:31] op_sel_hi:[1,0]
	v_pk_mul_f32 v[56:57], v[56:57], s[30:31] op_sel_hi:[1,0]
	v_pk_mul_f32 v[58:59], v[58:59], s[30:31] op_sel_hi:[1,0]
	v_pk_mul_f32 v[60:61], v[60:61], s[30:31] op_sel_hi:[1,0]
	v_pk_mul_f32 v[62:63], v[62:63], s[30:31] op_sel_hi:[1,0]
	v_med3_f32 v0, v0, s24, v237
	v_med3_f32 v1, v1, s24, v237
	v_med3_f32 v2, v2, s24, v237
	v_med3_f32 v3, v3, s24, v237
	v_med3_f32 v4, v4, s24, v237
	v_med3_f32 v5, v5, s24, v237
	v_med3_f32 v6, v6, s24, v237
	v_med3_f32 v7, v7, s24, v237
	v_med3_f32 v8, v8, s24, v237
	v_med3_f32 v9, v9, s24, v237
	v_med3_f32 v10, v10, s24, v237
	v_med3_f32 v11, v11, s24, v237
	v_med3_f32 v12, v12, s24, v237
	v_med3_f32 v13, v13, s24, v237
	v_med3_f32 v14, v14, s24, v237
	v_med3_f32 v15, v15, s24, v237
	v_med3_f32 v16, v16, s24, v237
	v_med3_f32 v17, v17, s24, v237
	v_med3_f32 v18, v18, s24, v237
	v_med3_f32 v19, v19, s24, v237
	v_med3_f32 v20, v20, s24, v237
	v_med3_f32 v21, v21, s24, v237
	v_med3_f32 v22, v22, s24, v237
	v_med3_f32 v23, v23, s24, v237
	v_med3_f32 v24, v24, s24, v237
	v_med3_f32 v25, v25, s24, v237
	v_med3_f32 v26, v26, s24, v237
	v_med3_f32 v27, v27, s24, v237
	v_med3_f32 v28, v28, s24, v237
	v_med3_f32 v29, v29, s24, v237
	v_med3_f32 v30, v30, s24, v237
	v_med3_f32 v31, v31, s24, v237
	v_med3_f32 v32, v32, s24, v237
	v_med3_f32 v33, v33, s24, v237
	v_med3_f32 v34, v34, s24, v237
	v_med3_f32 v35, v35, s24, v237
	v_med3_f32 v36, v36, s24, v237
	v_med3_f32 v37, v37, s24, v237
	v_med3_f32 v38, v38, s24, v237
	v_med3_f32 v39, v39, s24, v237
	v_med3_f32 v40, v40, s24, v237
	v_med3_f32 v41, v41, s24, v237
	v_med3_f32 v42, v42, s24, v237
	v_med3_f32 v43, v43, s24, v237
	v_med3_f32 v44, v44, s24, v237
	v_med3_f32 v45, v45, s24, v237
	v_med3_f32 v46, v46, s24, v237
	v_med3_f32 v47, v47, s24, v237
	v_med3_f32 v48, v48, s24, v237
	v_med3_f32 v49, v49, s24, v237
	v_med3_f32 v50, v50, s24, v237
	v_med3_f32 v51, v51, s24, v237
	v_med3_f32 v52, v52, s24, v237
	v_med3_f32 v53, v53, s24, v237
	v_med3_f32 v54, v54, s24, v237
	v_med3_f32 v55, v55, s24, v237
	v_med3_f32 v56, v56, s24, v237
	v_med3_f32 v57, v57, s24, v237
	v_med3_f32 v58, v58, s24, v237
	v_med3_f32 v59, v59, s24, v237
	v_med3_f32 v60, v60, s24, v237
	v_med3_f32 v61, v61, s24, v237
	v_med3_f32 v62, v62, s24, v237
	v_med3_f32 v63, v63, s24, v237
	v_cvt_pk_fp8_f32 v0, v0, v4
	v_cvt_pk_fp8_f32 v0, v8, v12 op_sel:[0,0,1]
	v_cvt_pk_fp8_f32 v4, v1, v5
	v_cvt_pk_fp8_f32 v4, v9, v13 op_sel:[0,0,1]
	v_cvt_pk_fp8_f32 v8, v2, v6
	v_cvt_pk_fp8_f32 v8, v10, v14 op_sel:[0,0,1]
	v_cvt_pk_fp8_f32 v12, v3, v7
	v_cvt_pk_fp8_f32 v12, v11, v15 op_sel:[0,0,1]
	v_cvt_pk_fp8_f32 v1, v16, v20
	v_cvt_pk_fp8_f32 v1, v24, v28 op_sel:[0,0,1]
	v_cvt_pk_fp8_f32 v5, v17, v21
	v_cvt_pk_fp8_f32 v5, v25, v29 op_sel:[0,0,1]
	v_cvt_pk_fp8_f32 v9, v18, v22
	v_cvt_pk_fp8_f32 v9, v26, v30 op_sel:[0,0,1]
	v_cvt_pk_fp8_f32 v13, v19, v23
	v_cvt_pk_fp8_f32 v13, v27, v31 op_sel:[0,0,1]
	v_cvt_pk_fp8_f32 v2, v32, v36
	v_cvt_pk_fp8_f32 v2, v40, v44 op_sel:[0,0,1]
	v_cvt_pk_fp8_f32 v6, v33, v37
	v_cvt_pk_fp8_f32 v6, v41, v45 op_sel:[0,0,1]
	v_cvt_pk_fp8_f32 v10, v34, v38
	v_cvt_pk_fp8_f32 v10, v42, v46 op_sel:[0,0,1]
	v_cvt_pk_fp8_f32 v14, v35, v39
	v_cvt_pk_fp8_f32 v14, v43, v47 op_sel:[0,0,1]
	v_cvt_pk_fp8_f32 v3, v48, v52
	v_cvt_pk_fp8_f32 v3, v56, v60 op_sel:[0,0,1]
	v_cvt_pk_fp8_f32 v7, v49, v53
	v_cvt_pk_fp8_f32 v7, v57, v61 op_sel:[0,0,1]
	v_cvt_pk_fp8_f32 v11, v50, v54
	v_cvt_pk_fp8_f32 v11, v58, v62 op_sel:[0,0,1]
	v_cvt_pk_fp8_f32 v15, v51, v55
	v_cvt_pk_fp8_f32 v15, v59, v63 op_sel:[0,0,1]
	global_store_dwordx4 v250, v[0:3], s[42:43] nt
	global_store_dwordx4 v250, v[4:7], s[42:43] offset:2048 nt
	global_store_dwordx4 v251, v[8:11], s[42:43] nt
	global_store_dwordx4 v251, v[12:15], s[42:43] offset:2048 nt
	s_add_u32 s42, s42, 0x10000
	s_addc_u32 s43, s43, 0
	global_load_dwordx4 v[0:3], v246, s[4:5] offset:1920 nt
	global_load_dwordx4 v[4:7], v247, s[4:5] offset:1920 nt
	global_load_dwordx4 v[8:11], v248, s[4:5] offset:1920 nt
	global_load_dwordx4 v[12:15], v249, s[4:5] offset:1920 nt
	global_load_dwordx4 v[16:19], v246, s[6:7] offset:1920 nt
	global_load_dwordx4 v[20:23], v247, s[6:7] offset:1920 nt
	global_load_dwordx4 v[24:27], v248, s[6:7] offset:1920 nt
	global_load_dwordx4 v[28:31], v249, s[6:7] offset:1920 nt
	global_load_dwordx4 v[32:35], v246, s[8:9] offset:1920 nt
	global_load_dwordx4 v[36:39], v247, s[8:9] offset:1920 nt
	global_load_dwordx4 v[40:43], v248, s[8:9] offset:1920 nt
	global_load_dwordx4 v[44:47], v249, s[8:9] offset:1920 nt
	global_load_dwordx4 v[48:51], v246, s[38:39] offset:1920 nt
	global_load_dwordx4 v[52:55], v247, s[38:39] offset:1920 nt
	global_load_dwordx4 v[56:59], v248, s[38:39] offset:1920 nt
	global_load_dwordx4 v[60:63], v249, s[38:39] offset:1920 nt
	s_waitcnt vmcnt(40)
; #define GAS __attribute__((address_space(1)))
; template <bool GAIN, bool NT = false> __device__ __forceinline__ void titem8_store(const TItem& d, int lane, const f32x4 (&r)[16], const f32x4 (&g)[4]) {
;     const int q = lane & 7, kg = lane >> 3; const unsigned lo = (unsigned)((4 * q) * d.ldk + 16 * kg);
;     GAS char* base = (GAS char*)d.dst;
;     f32x4 s[16];
; #pragma unroll
;     for (int j = 0; j < 16; ++j) s[j] = r[j] * ((GAIN ? g[j >> 2][j & 3] : 1.0f) * W8_SCALE);
; #pragma unroll
;     for (int i = 0; i < 4; ++i) { v4u w;
;         w.x = pk4_fp8w(s[0][i], s[1][i], s[2][i], s[3][i]); w.y = pk4_fp8w(s[4][i], s[5][i], s[6][i], s[7][i]);
;         w.z = pk4_fp8w(s[8][i], s[9][i], s[10][i], s[11][i]); w.w = pk4_fp8w(s[12][i], s[13][i], s[14][i], s[15][i]);
;         GAS v4u* p = (GAS v4u*)(base + (size_t)i * (size_t)d.ldk + lo);
;         if (NT) __builtin_nontemporal_store(w, p); else *p = w; }
; }
	v_pk_mul_f32 v[66:67], v[66:67], s[30:31] op_sel_hi:[1,0]
	v_pk_mul_f32 v[68:69], v[68:69], s[30:31] op_sel_hi:[1,0]
	v_pk_mul_f32 v[70:71], v[70:71], s[30:31] op_sel_hi:[1,0]
	v_pk_mul_f32 v[72:73], v[72:73], s[30:31] op_sel_hi:[1,0]
	v_pk_mul_f32 v[74:75], v[74:75], s[30:31] op_sel_hi:[1,0]
	v_pk_mul_f32 v[76:77], v[76:77], s[30:31] op_sel_hi:[1,0]
	v_pk_mul_f32 v[78:79], v[78:79], s[30:31] op_sel_hi:[1,0]
	v_pk_mul_f32 v[80:81], v[80:81], s[30:31] op_sel_hi:[1,0]
	v_pk_mul_f32 v[82:83], v[82:83], s[30:31] op_sel_hi:[1,0]
	v_pk_mul_f32 v[84:85], v[84:85], s[30:31] op_sel_hi:[1,0]
	v_pk_mul_f32 v[86:87], v[86:87], s[30:31] op_sel_hi:[1,0]
	v_pk_mul_f32 v[88:89], v[88:89], s[30:31] op_sel_hi:[1,0]
	v_pk_mul_f32 v[90:91], v[90:91], s[30:31] op_sel_hi:[1,0]
	v_pk_mul_f32 v[92:93], v[92:93], s[30:31] op_sel_hi:[1,0]
	v_pk_mul_f32 v[94:95], v[94:95], s[30:31] op_sel_hi:[1,0]
	v_pk_mul_f32 v[96:97], v[96:97], s[30:31] op_sel_hi:[1,0]
	v_pk_mul_f32 v[98:99], v[98:99], s[30:31] op_sel_hi:[1,0]
	v_pk_mul_f32 v[100:101], v[100:101], s[30:31] op_sel_hi:[1,0]
	v_pk_mul_f32 v[102:103], v[102:103], s[30:31] op_sel_hi:[1,0]
	v_pk_mul_f32 v[104:105], v[104:105], s[30:31] op_sel_hi:[1,0]
	v_pk_mul_f32 v[106:107], v[106:107], s[30:31] op_sel_hi:[1,0]
	v_pk_mul_f32 v[108:109], v[108:109], s[30:31] op_sel_hi:[1,0]
	v_pk_mul_f32 v[110:111], v[110:111], s[30:31] op_sel_hi:[1,0]
	v_pk_mul_f32 v[112:113], v[112:113], s[30:31] op_sel_hi:[1,0]
	v_pk_mul_f32 v[114:115], v[114:115], s[30:31] op_sel_hi:[1,0]
	v_pk_mul_f32 v[116:117], v[116:117], s[30:31] op_sel_hi:[1,0]
	v_pk_mul_f32 v[118:119], v[118:119], s[30:31] op_sel_hi:[1,0]
	v_pk_mul_f32 v[120:121], v[120:121], s[30:31] op_sel_hi:[1,0]
	v_pk_mul_f32 v[122:123], v[122:123], s[30:31] op_sel_hi:[1,0]
	v_pk_mul_f32 v[124:125], v[124:125], s[30:31] op_sel_hi:[1,0]
	v_pk_mul_f32 v[126:127], v[126:127], s[30:31] op_sel_hi:[1,0]
	v_pk_mul_f32 v[128:129], v[128:129], s[30:31] op_sel_hi:[1,0]
	v_med3_f32 v66, v66, s24, v237
	v_med3_f32 v67, v67, s24, v237
	v_med3_f32 v68, v68, s24, v237
	v_med3_f32 v69, v69, s24, v237
	v_med3_f32 v70, v70, s24, v237
	v_med3_f32 v71, v71, s24, v237
	v_med3_f32 v72, v72, s24, v237
	v_med3_f32 v73, v73, s24, v237
	v_med3_f32 v74, v74, s24, v237
	v_med3_f32 v75, v75, s24, v237
	v_med3_f32 v76, v76, s24, v237
	v_med3_f32 v77, v77, s24, v237
	v_med3_f32 v78, v78, s24, v237
	v_med3_f32 v79, v79, s24, v237
	v_med3_f32 v80, v80, s24, v237
	v_med3_f32 v81, v81, s24, v237
	v_med3_f32 v82, v82, s24, v237
	v_med3_f32 v83, v83, s24, v237
	v_med3_f32 v84, v84, s24, v237
	v_med3_f32 v85, v85, s24, v237
	v_med3_f32 v86, v86, s24, v237
	v_med3_f32 v87, v87, s24, v237
	v_med3_f32 v88, v88, s24, v237
	v_med3_f32 v89, v89, s24, v237
	v_med3_f32 v90, v90, s24, v237
	v_med3_f32 v91, v91, s24, v237
	v_med3_f32 v92, v92, s24, v237
	v_med3_f32 v93, v93, s24, v237
	v_med3_f32 v94, v94, s24, v237
	v_med3_f32 v95, v95, s24, v237
	v_med3_f32 v96, v96, s24, v237
	v_med3_f32 v97, v97, s24, v237
	v_med3_f32 v98, v98, s24, v237
	v_med3_f32 v99, v99, s24, v237
	v_med3_f32 v100, v100, s24, v237
	v_med3_f32 v101, v101, s24, v237
	v_med3_f32 v102, v102, s24, v237
	v_med3_f32 v103, v103, s24, v237
	v_med3_f32 v104, v104, s24, v237
	v_med3_f32 v105, v105, s24, v237
	v_med3_f32 v106, v106, s24, v237
	v_med3_f32 v107, v107, s24, v237
	v_med3_f32 v108, v108, s24, v237
	v_med3_f32 v109, v109, s24, v237
	v_med3_f32 v110, v110, s24, v237
	v_med3_f32 v111, v111, s24, v237
	v_med3_f32 v112, v112, s24, v237
	v_med3_f32 v113, v113, s24, v237
	v_med3_f32 v114, v114, s24, v237
	v_med3_f32 v115, v115, s24, v237
	v_med3_f32 v116, v116, s24, v237
	v_med3_f32 v117, v117, s24, v237
	v_med3_f32 v118, v118, s24, v237
	v_med3_f32 v119, v119, s24, v237
	v_med3_f32 v120, v120, s24, v237
	v_med3_f32 v121, v121, s24, v237
	v_med3_f32 v122, v122, s24, v237
	v_med3_f32 v123, v123, s24, v237
	v_med3_f32 v124, v124, s24, v237
	v_med3_f32 v125, v125, s24, v237
	v_med3_f32 v126, v126, s24, v237
	v_med3_f32 v127, v127, s24, v237
	v_med3_f32 v128, v128, s24, v237
	v_med3_f32 v129, v129, s24, v237
	v_cvt_pk_fp8_f32 v66, v66, v70
	v_cvt_pk_fp8_f32 v66, v74, v78 op_sel:[0,0,1]
	v_cvt_pk_fp8_f32 v70, v67, v71
	v_cvt_pk_fp8_f32 v70, v75, v79 op_sel:[0,0,1]
	v_cvt_pk_fp8_f32 v74, v68, v72
	v_cvt_pk_fp8_f32 v74, v76, v80 op_sel:[0,0,1]
	v_cvt_pk_fp8_f32 v78, v69, v73
	v_cvt_pk_fp8_f32 v78, v77, v81 op_sel:[0,0,1]
	v_cvt_pk_fp8_f32 v67, v82, v86
	v_cvt_pk_fp8_f32 v67, v90, v94 op_sel:[0,0,1]
	v_cvt_pk_fp8_f32 v71, v83, v87
	v_cvt_pk_fp8_f32 v71, v91, v95 op_sel:[0,0,1]
	v_cvt_pk_fp8_f32 v75, v84, v88
	v_cvt_pk_fp8_f32 v75, v92, v96 op_sel:[0,0,1]
	v_cvt_pk_fp8_f32 v79, v85, v89
	v_cvt_pk_fp8_f32 v79, v93, v97 op_sel:[0,0,1]
	v_cvt_pk_fp8_f32 v68, v98, v102
	v_cvt_pk_fp8_f32 v68, v106, v110 op_sel:[0,0,1]
	v_cvt_pk_fp8_f32 v72, v99, v103
	v_cvt_pk_fp8_f32 v72, v107, v111 op_sel:[0,0,1]
	v_cvt_pk_fp8_f32 v76, v100, v104
	v_cvt_pk_fp8_f32 v76, v108, v112 op_sel:[0,0,1]
	v_cvt_pk_fp8_f32 v80, v101, v105
	v_cvt_pk_fp8_f32 v80, v109, v113 op_sel:[0,0,1]
	v_cvt_pk_fp8_f32 v69, v114, v118
	v_cvt_pk_fp8_f32 v69, v122, v126 op_sel:[0,0,1]
	v_cvt_pk_fp8_f32 v73, v115, v119
	v_cvt_pk_fp8_f32 v73, v123, v127 op_sel:[0,0,1]
	v_cvt_pk_fp8_f32 v77, v116, v120
	v_cvt_pk_fp8_f32 v77, v124, v128 op_sel:[0,0,1]
	v_cvt_pk_fp8_f32 v81, v117, v121
	v_cvt_pk_fp8_f32 v81, v125, v129 op_sel:[0,0,1]
	global_store_dwordx4 v250, v[66:69], s[42:43] nt
	global_store_dwordx4 v250, v[70:73], s[42:43] offset:2048 nt
	global_store_dwordx4 v251, v[74:77], s[42:43] nt
	global_store_dwordx4 v251, v[78:81], s[42:43] offset:2048 nt
	s_add_u32 s42, s42, 0x10000
	s_addc_u32 s43, s43, 0
	s_waitcnt vmcnt(24)
; #define GAS __attribute__((address_space(1)))
; template <bool GAIN, bool NT = false> __device__ __forceinline__ void titem8_store(const TItem& d, int lane, const f32x4 (&r)[16], const f32x4 (&g)[4]) {
;     const int q = lane & 7, kg = lane >> 3; const unsigned lo = (unsigned)((4 * q) * d.ldk + 16 * kg);
;     GAS char* base = (GAS char*)d.dst;
;     f32x4 s[16];
; #pragma unroll
;     for (int j = 0; j < 16; ++j) s[j] = r[j] * ((GAIN ? g[j >> 2][j & 3] : 1.0f) * W8_SCALE);
; #pragma unroll
;     for (int i = 0; i < 4; ++i) { v4u w;
;         w.x = pk4_fp8w(s[0][i], s[1][i], s[2][i], s[3][i]); w.y = pk4_fp8w(s[4][i], s[5][i], s[6][i], s[7][i]);
;         w.z = pk4_fp8w(s[8][i], s[9][i], s[10][i], s[11][i]); w.w = pk4_fp8w(s[12][i], s[13][i], s[14][i], s[15][i]);
;         GAS v4u* p = (GAS v4u*)(base + (size_t)i * (size_t)d.ldk + lo);
;         if (NT) __builtin_nontemporal_store(w, p); else *p = w; }
; }
	v_pk_mul_f32 v[130:131], v[130:131], s[30:31] op_sel_hi:[1,0]
	v_pk_mul_f32 v[132:133], v[132:133], s[30:31] op_sel_hi:[1,0]
	v_pk_mul_f32 v[134:135], v[134:135], s[30:31] op_sel_hi:[1,0]
	v_pk_mul_f32 v[136:137], v[136:137], s[30:31] op_sel_hi:[1,0]
	v_pk_mul_f32 v[138:139], v[138:139], s[30:31] op_sel_hi:[1,0]
	v_pk_mul_f32 v[140:141], v[140:141], s[30:31] op_sel_hi:[1,0]
	v_pk_mul_f32 v[142:143], v[142:143], s[30:31] op_sel_hi:[1,0]
	v_pk_mul_f32 v[144:145], v[144:145], s[30:31] op_sel_hi:[1,0]
	v_pk_mul_f32 v[146:147], v[146:147], s[30:31] op_sel_hi:[1,0]
	v_pk_mul_f32 v[148:149], v[148:149], s[30:31] op_sel_hi:[1,0]
	v_pk_mul_f32 v[150:151], v[150:151], s[30:31] op_sel_hi:[1,0]
	v_pk_mul_f32 v[152:153], v[152:153], s[30:31] op_sel_hi:[1,0]
	v_pk_mul_f32 v[154:155], v[154:155], s[30:31] op_sel_hi:[1,0]
	v_pk_mul_f32 v[156:157], v[156:157], s[30:31] op_sel_hi:[1,0]
	v_pk_mul_f32 v[158:159], v[158:159], s[30:31] op_sel_hi:[1,0]
	v_pk_mul_f32 v[160:161], v[160:161], s[30:31] op_sel_hi:[1,0]
	v_pk_mul_f32 v[162:163], v[162:163], s[30:31] op_sel_hi:[1,0]
	v_pk_mul_f32 v[164:165], v[164:165], s[30:31] op_sel_hi:[1,0]
	v_pk_mul_f32 v[166:167], v[166:167], s[30:31] op_sel_hi:[1,0]
	v_pk_mul_f32 v[168:169], v[168:169], s[30:31] op_sel_hi:[1,0]
	v_pk_mul_f32 v[170:171], v[170:171], s[30:31] op_sel_hi:[1,0]
	v_pk_mul_f32 v[172:173], v[172:173], s[30:31] op_sel_hi:[1,0]
	v_pk_mul_f32 v[174:175], v[174:175], s[30:31] op_sel_hi:[1,0]
	v_pk_mul_f32 v[176:177], v[176:177], s[30:31] op_sel_hi:[1,0]
	v_pk_mul_f32 v[178:179], v[178:179], s[30:31] op_sel_hi:[1,0]
	v_pk_mul_f32 v[180:181], v[180:181], s[30:31] op_sel_hi:[1,0]
	v_pk_mul_f32 v[182:183], v[182:183], s[30:31] op_sel_hi:[1,0]
	v_pk_mul_f32 v[184:185], v[184:185], s[30:31] op_sel_hi:[1,0]
	v_pk_mul_f32 v[186:187], v[186:187], s[30:31] op_sel_hi:[1,0]
	v_pk_mul_f32 v[188:189], v[188:189], s[30:31] op_sel_hi:[1,0]
	v_pk_mul_f32 v[190:191], v[190:191], s[30:31] op_sel_hi:[1,0]
	v_pk_mul_f32 v[192:193], v[192:193], s[30:31] op_sel_hi:[1,0]
	v_med3_f32 v130, v130, s24, v237
	v_med3_f32 v131, v131, s24, v237
	v_med3_f32 v132, v132, s24, v237
	v_med3_f32 v133, v133, s24, v237
	v_med3_f32 v134, v134, s24, v237
	v_med3_f32 v135, v135, s24, v237
	v_med3_f32 v136, v136, s24, v237
	v_med3_f32 v137, v137, s24, v237
	v_med3_f32 v138, v138, s24, v237
	v_med3_f32 v139, v139, s24, v237
	v_med3_f32 v140, v140, s24, v237
	v_med3_f32 v141, v141, s24, v237
	v_med3_f32 v142, v142, s24, v237
	v_med3_f32 v143, v143, s24, v237
	v_med3_f32 v144, v144, s24, v237
	v_med3_f32 v145, v145, s24, v237
	v_med3_f32 v146, v146, s24, v237
	v_med3_f32 v147, v147, s24, v237
	v_med3_f32 v148, v148, s24, v237
	v_med3_f32 v149, v149, s24, v237
	v_med3_f32 v150, v150, s24, v237
	v_med3_f32 v151, v151, s24, v237
	v_med3_f32 v152, v152, s24, v237
	v_med3_f32 v153, v153, s24, v237
	v_med3_f32 v154, v154, s24, v237
	v_med3_f32 v155, v155, s24, v237
	v_med3_f32 v156, v156, s24, v237
	v_med3_f32 v157, v157, s24, v237
	v_med3_f32 v158, v158, s24, v237
	v_med3_f32 v159, v159, s24, v237
	v_med3_f32 v160, v160, s24, v237
	v_med3_f32 v161, v161, s24, v237
	v_med3_f32 v162, v162, s24, v237
	v_med3_f32 v163, v163, s24, v237
	v_med3_f32 v164, v164, s24, v237
	v_med3_f32 v165, v165, s24, v237
	v_med3_f32 v166, v166, s24, v237
	v_med3_f32 v167, v167, s24, v237
	v_med3_f32 v168, v168, s24, v237
	v_med3_f32 v169, v169, s24, v237
	v_med3_f32 v170, v170, s24, v237
	v_med3_f32 v171, v171, s24, v237
	v_med3_f32 v172, v172, s24, v237
	v_med3_f32 v173, v173, s24, v237
	v_med3_f32 v174, v174, s24, v237
	v_med3_f32 v175, v175, s24, v237
	v_med3_f32 v176, v176, s24, v237
	v_med3_f32 v177, v177, s24, v237
	v_med3_f32 v178, v178, s24, v237
	v_med3_f32 v179, v179, s24, v237
	v_med3_f32 v180, v180, s24, v237
	v_med3_f32 v181, v181, s24, v237
	v_med3_f32 v182, v182, s24, v237
	v_med3_f32 v183, v183, s24, v237
	v_med3_f32 v184, v184, s24, v237
	v_med3_f32 v185, v185, s24, v237
	v_med3_f32 v186, v186, s24, v237
	v_med3_f32 v187, v187, s24, v237
	v_med3_f32 v188, v188, s24, v237
	v_med3_f32 v189, v189, s24, v237
	v_med3_f32 v190, v190, s24, v237
	v_med3_f32 v191, v191, s24, v237
	v_med3_f32 v192, v192, s24, v237
	v_med3_f32 v193, v193, s24, v237
	v_cvt_pk_fp8_f32 v130, v130, v134
	v_cvt_pk_fp8_f32 v130, v138, v142 op_sel:[0,0,1]
	v_cvt_pk_fp8_f32 v134, v131, v135
	v_cvt_pk_fp8_f32 v134, v139, v143 op_sel:[0,0,1]
	v_cvt_pk_fp8_f32 v138, v132, v136
	v_cvt_pk_fp8_f32 v138, v140, v144 op_sel:[0,0,1]
	v_cvt_pk_fp8_f32 v142, v133, v137
	v_cvt_pk_fp8_f32 v142, v141, v145 op_sel:[0,0,1]
	v_cvt_pk_fp8_f32 v131, v146, v150
	v_cvt_pk_fp8_f32 v131, v154, v158 op_sel:[0,0,1]
	v_cvt_pk_fp8_f32 v135, v147, v151
	v_cvt_pk_fp8_f32 v135, v155, v159 op_sel:[0,0,1]
	v_cvt_pk_fp8_f32 v139, v148, v152
	v_cvt_pk_fp8_f32 v139, v156, v160 op_sel:[0,0,1]
	v_cvt_pk_fp8_f32 v143, v149, v153
	v_cvt_pk_fp8_f32 v143, v157, v161 op_sel:[0,0,1]
	v_cvt_pk_fp8_f32 v132, v162, v166
	v_cvt_pk_fp8_f32 v132, v170, v174 op_sel:[0,0,1]
	v_cvt_pk_fp8_f32 v136, v163, v167
	v_cvt_pk_fp8_f32 v136, v171, v175 op_sel:[0,0,1]
	v_cvt_pk_fp8_f32 v140, v164, v168
	v_cvt_pk_fp8_f32 v140, v172, v176 op_sel:[0,0,1]
	v_cvt_pk_fp8_f32 v144, v165, v169
	v_cvt_pk_fp8_f32 v144, v173, v177 op_sel:[0,0,1]
	v_cvt_pk_fp8_f32 v133, v178, v182
	v_cvt_pk_fp8_f32 v133, v186, v190 op_sel:[0,0,1]
	v_cvt_pk_fp8_f32 v137, v179, v183
	v_cvt_pk_fp8_f32 v137, v187, v191 op_sel:[0,0,1]
	v_cvt_pk_fp8_f32 v141, v180, v184
	v_cvt_pk_fp8_f32 v141, v188, v192 op_sel:[0,0,1]
	v_cvt_pk_fp8_f32 v145, v181, v185
	v_cvt_pk_fp8_f32 v145, v189, v193 op_sel:[0,0,1]
	global_store_dwordx4 v250, v[130:133], s[42:43] nt
	global_store_dwordx4 v250, v[134:137], s[42:43] offset:2048 nt
	global_store_dwordx4 v251, v[138:141], s[42:43] nt
	global_store_dwordx4 v251, v[142:145], s[42:43] offset:2048 nt
	s_add_u32 s42, s42, 0x10000
	s_addc_u32 s43, s43, 0
	s_waitcnt vmcnt(8)
; #define GAS __attribute__((address_space(1)))
; template <bool GAIN, bool NT = false> __device__ __forceinline__ void titem8_store(const TItem& d, int lane, const f32x4 (&r)[16], const f32x4 (&g)[4]) {
;     const int q = lane & 7, kg = lane >> 3; const unsigned lo = (unsigned)((4 * q) * d.ldk + 16 * kg);
;     GAS char* base = (GAS char*)d.dst;
;     f32x4 s[16];
; #pragma unroll
;     for (int j = 0; j < 16; ++j) s[j] = r[j] * ((GAIN ? g[j >> 2][j & 3] : 1.0f) * W8_SCALE);
; #pragma unroll
;     for (int i = 0; i < 4; ++i) { v4u w;
;         w.x = pk4_fp8w(s[0][i], s[1][i], s[2][i], s[3][i]); w.y = pk4_fp8w(s[4][i], s[5][i], s[6][i], s[7][i]);
;         w.z = pk4_fp8w(s[8][i], s[9][i], s[10][i], s[11][i]); w.w = pk4_fp8w(s[12][i], s[13][i], s[14][i], s[15][i]);
;         GAS v4u* p = (GAS v4u*)(base + (size_t)i * (size_t)d.ldk + lo);
;         if (NT) __builtin_nontemporal_store(w, p); else *p = w; }
; }
	v_pk_mul_f32 v[0:1], v[0:1], s[30:31] op_sel_hi:[1,0]
	v_pk_mul_f32 v[2:3], v[2:3], s[30:31] op_sel_hi:[1,0]
	v_pk_mul_f32 v[4:5], v[4:5], s[30:31] op_sel_hi:[1,0]
	v_pk_mul_f32 v[6:7], v[6:7], s[30:31] op_sel_hi:[1,0]
	v_pk_mul_f32 v[8:9], v[8:9], s[30:31] op_sel_hi:[1,0]
	v_pk_mul_f32 v[10:11], v[10:11], s[30:31] op_sel_hi:[1,0]
	v_pk_mul_f32 v[12:13], v[12:13], s[30:31] op_sel_hi:[1,0]
	v_pk_mul_f32 v[14:15], v[14:15], s[30:31] op_sel_hi:[1,0]
	v_pk_mul_f32 v[16:17], v[16:17], s[30:31] op_sel_hi:[1,0]
	v_pk_mul_f32 v[18:19], v[18:19], s[30:31] op_sel_hi:[1,0]
	v_pk_mul_f32 v[20:21], v[20:21], s[30:31] op_sel_hi:[1,0]
	v_pk_mul_f32 v[22:23], v[22:23], s[30:31] op_sel_hi:[1,0]
	v_pk_mul_f32 v[24:25], v[24:25], s[30:31] op_sel_hi:[1,0]
	v_pk_mul_f32 v[26:27], v[26:27], s[30:31] op_sel_hi:[1,0]
	v_pk_mul_f32 v[28:29], v[28:29], s[30:31] op_sel_hi:[1,0]
	v_pk_mul_f32 v[30:31], v[30:31], s[30:31] op_sel_hi:[1,0]
	v_pk_mul_f32 v[32:33], v[32:33], s[30:31] op_sel_hi:[1,0]
	v_pk_mul_f32 v[34:35], v[34:35], s[30:31] op_sel_hi:[1,0]
	v_pk_mul_f32 v[36:37], v[36:37], s[30:31] op_sel_hi:[1,0]
	v_pk_mul_f32 v[38:39], v[38:39], s[30:31] op_sel_hi:[1,0]
	v_pk_mul_f32 v[40:41], v[40:41], s[30:31] op_sel_hi:[1,0]
	v_pk_mul_f32 v[42:43], v[42:43], s[30:31] op_sel_hi:[1,0]
	v_pk_mul_f32 v[44:45], v[44:45], s[30:31] op_sel_hi:[1,0]
	v_pk_mul_f32 v[46:47], v[46:47], s[30:31] op_sel_hi:[1,0]
	v_pk_mul_f32 v[48:49], v[48:49], s[30:31] op_sel_hi:[1,0]
	v_pk_mul_f32 v[50:51], v[50:51], s[30:31] op_sel_hi:[1,0]
	v_pk_mul_f32 v[52:53], v[52:53], s[30:31] op_sel_hi:[1,0]
	v_pk_mul_f32 v[54:55], v[54:55], s[30:31] op_sel_hi:[1,0]
	v_pk_mul_f32 v[56:57], v[56:57], s[30:31] op_sel_hi:[1,0]
	v_pk_mul_f32 v[58:59], v[58:59], s[30:31] op_sel_hi:[1,0]
	v_pk_mul_f32 v[60:61], v[60:61], s[30:31] op_sel_hi:[1,0]
	v_pk_mul_f32 v[62:63], v[62:63], s[30:31] op_sel_hi:[1,0]
	v_med3_f32 v0, v0, s24, v237
	v_med3_f32 v1, v1, s24, v237
	v_med3_f32 v2, v2, s24, v237
	v_med3_f32 v3, v3, s24, v237
	v_med3_f32 v4, v4, s24, v237
	v_med3_f32 v5, v5, s24, v237
	v_med3_f32 v6, v6, s24, v237
	v_med3_f32 v7, v7, s24, v237
	v_med3_f32 v8, v8, s24, v237
	v_med3_f32 v9, v9, s24, v237
	v_med3_f32 v10, v10, s24, v237
	v_med3_f32 v11, v11, s24, v237
	v_med3_f32 v12, v12, s24, v237
	v_med3_f32 v13, v13, s24, v237
	v_med3_f32 v14, v14, s24, v237
	v_med3_f32 v15, v15, s24, v237
	v_med3_f32 v16, v16, s24, v237
	v_med3_f32 v17, v17, s24, v237
	v_med3_f32 v18, v18, s24, v237
	v_med3_f32 v19, v19, s24, v237
	v_med3_f32 v20, v20, s24, v237
	v_med3_f32 v21, v21, s24, v237
	v_med3_f32 v22, v22, s24, v237
	v_med3_f32 v23, v23, s24, v237
	v_med3_f32 v24, v24, s24, v237
	v_med3_f32 v25, v25, s24, v237
	v_med3_f32 v26, v26, s24, v237
	v_med3_f32 v27, v27, s24, v237
	v_med3_f32 v28, v28, s24, v237
	v_med3_f32 v29, v29, s24, v237
	v_med3_f32 v30, v30, s24, v237
	v_med3_f32 v31, v31, s24, v237
	v_med3_f32 v32, v32, s24, v237
	v_med3_f32 v33, v33, s24, v237
	v_med3_f32 v34, v34, s24, v237
	v_med3_f32 v35, v35, s24, v237
	v_med3_f32 v36, v36, s24, v237
	v_med3_f32 v37, v37, s24, v237
	v_med3_f32 v38, v38, s24, v237
	v_med3_f32 v39, v39, s24, v237
	v_med3_f32 v40, v40, s24, v237
	v_med3_f32 v41, v41, s24, v237
	v_med3_f32 v42, v42, s24, v237
	v_med3_f32 v43, v43, s24, v237
	v_med3_f32 v44, v44, s24, v237
	v_med3_f32 v45, v45, s24, v237
	v_med3_f32 v46, v46, s24, v237
	v_med3_f32 v47, v47, s24, v237
	v_med3_f32 v48, v48, s24, v237
	v_med3_f32 v49, v49, s24, v237
	v_med3_f32 v50, v50, s24, v237
	v_med3_f32 v51, v51, s24, v237
	v_med3_f32 v52, v52, s24, v237
	v_med3_f32 v53, v53, s24, v237
	v_med3_f32 v54, v54, s24, v237
	v_med3_f32 v55, v55, s24, v237
	v_med3_f32 v56, v56, s24, v237
	v_med3_f32 v57, v57, s24, v237
	v_med3_f32 v58, v58, s24, v237
	v_med3_f32 v59, v59, s24, v237
	v_med3_f32 v60, v60, s24, v237
	v_med3_f32 v61, v61, s24, v237
	v_med3_f32 v62, v62, s24, v237
	v_med3_f32 v63, v63, s24, v237
	v_cvt_pk_fp8_f32 v0, v0, v4
	v_cvt_pk_fp8_f32 v0, v8, v12 op_sel:[0,0,1]
	v_cvt_pk_fp8_f32 v4, v1, v5
	v_cvt_pk_fp8_f32 v4, v9, v13 op_sel:[0,0,1]
	v_cvt_pk_fp8_f32 v8, v2, v6
	v_cvt_pk_fp8_f32 v8, v10, v14 op_sel:[0,0,1]
	v_cvt_pk_fp8_f32 v12, v3, v7
	v_cvt_pk_fp8_f32 v12, v11, v15 op_sel:[0,0,1]
	v_cvt_pk_fp8_f32 v1, v16, v20
	v_cvt_pk_fp8_f32 v1, v24, v28 op_sel:[0,0,1]
	v_cvt_pk_fp8_f32 v5, v17, v21
	v_cvt_pk_fp8_f32 v5, v25, v29 op_sel:[0,0,1]
	v_cvt_pk_fp8_f32 v9, v18, v22
	v_cvt_pk_fp8_f32 v9, v26, v30 op_sel:[0,0,1]
	v_cvt_pk_fp8_f32 v13, v19, v23
	v_cvt_pk_fp8_f32 v13, v27, v31 op_sel:[0,0,1]
	v_cvt_pk_fp8_f32 v2, v32, v36
	v_cvt_pk_fp8_f32 v2, v40, v44 op_sel:[0,0,1]
	v_cvt_pk_fp8_f32 v6, v33, v37
	v_cvt_pk_fp8_f32 v6, v41, v45 op_sel:[0,0,1]
	v_cvt_pk_fp8_f32 v10, v34, v38
	v_cvt_pk_fp8_f32 v10, v42, v46 op_sel:[0,0,1]
	v_cvt_pk_fp8_f32 v14, v35, v39
	v_cvt_pk_fp8_f32 v14, v43, v47 op_sel:[0,0,1]
	v_cvt_pk_fp8_f32 v3, v48, v52
	v_cvt_pk_fp8_f32 v3, v56, v60 op_sel:[0,0,1]
	v_cvt_pk_fp8_f32 v7, v49, v53
	v_cvt_pk_fp8_f32 v7, v57, v61 op_sel:[0,0,1]
	v_cvt_pk_fp8_f32 v11, v50, v54
	v_cvt_pk_fp8_f32 v11, v58, v62 op_sel:[0,0,1]
	v_cvt_pk_fp8_f32 v15, v51, v55
	v_cvt_pk_fp8_f32 v15, v59, v63 op_sel:[0,0,1]
	global_store_dwordx4 v250, v[0:3], s[42:43] nt
	global_store_dwordx4 v250, v[4:7], s[42:43] offset:2048 nt
	global_store_dwordx4 v251, v[8:11], s[42:43] nt
	global_store_dwordx4 v251, v[12:15], s[42:43] offset:2048 nt
	s_add_u32 s42, s42, 0x10000
	s_addc_u32 s43, s43, 0
	v_mov_b32_e32 v65, 0
